# plus: packed f32 VALU ops in P2 (HGRN2 scan) and P3 (attention) split into scalar pairs (bit-identical)
# speedup vs baseline: 1.0088x; 1.0027x over previous
; DI int opaque_tid() { int t = threadIdx.x; asm volatile("" : "+v"(t)); return t; }
; DI void p2_hgrn_roles(Frame& F, ArgsP A) {
;     ...
;     for (int item = F.vcu; item < 256; item += F.G) {
;         const int bh = item >> 1, vhalf = item & 1, b = bh >> 4, h = bh & 15;
;         const size_t rb = (size_t)b * SEQ * D;
;         unsigned CR[72];
;         f32x16 S0, S1;
; #pragma unroll
;         for (int i = 0; i < 72; ++i) CR[i] = 0u;
; #pragma unroll
;         for (int i = 0; i < 16; ++i) { S0[i] = 0.f; S1[i] = 0.f; }
;     ...
;         if (prep) {
;             const int pt = opaque_tid() & 255, k2 = pt & 63, tgp = pt >> 6, v64 = pt & 63;
;             const bf16_t* qp = (const bf16_t*)(A->ws + WS_QA) + rb + (size_t)(8 * tgp) * D + h * 128 + 2 * k2; const bf16_t* fp = (const bf16_t*)(A->ws + WS_LF) + rb + (size_t)(8 * tgp) * D + h * 128 + 2 * k2;
;             const bf16_t* ip = (const bf16_t*)(A->ws + WS_IA) + rb + (size_t)(8 * tgp) * D + h * 128 + vhalf * 64 + v64;
;             h_load8<0>(CR, qp, fp, ip, 0); h_load8<1>(CR, qp, fp, ip, 1); h_load8<2>(CR, qp, fp, ip, 2); h_totals8<0>(CR, lds, tgp, k2);
.LBB0_405:
	s_ashr_i32 s6, s95, 5
	s_ashr_i32 s7, s6, 31
	s_bfe_u32 s9, s95, 0x40001
	s_and_b32 s8, s95, 1
	s_lshl_b64 s[52:53], s[6:7], 22
	s_and_b64 vcc, exec, s[36:37]
	s_waitcnt vmcnt(2)
	v_mov_b32_e32 v180, v3
	v_mov_b32_e32 v169, v3
	v_mov_b32_e32 v165, v3
	v_mov_b32_e32 v153, v3
	v_mov_b32_e32 v148, v3
	v_mov_b32_e32 v146, v3
	v_mov_b32_e32 v127, v3
	v_mov_b32_e32 v125, v3
	v_mov_b32_e32 v175, v3
	v_mov_b32_e32 v172, v3
	v_mov_b32_e32 v167, v3
	v_mov_b32_e32 v155, v3
	v_mov_b32_e32 v157, v3
	v_mov_b32_e32 v140, v3
	v_mov_b32_e32 v131, v3
	v_mov_b32_e32 v129, v3
	s_waitcnt vmcnt(0)
	v_mov_b32_e32 v182, v3
	v_mov_b32_e32 v178, v3
	v_mov_b32_e32 v162, v3
	v_mov_b32_e32 v160, v3
	v_mov_b32_e32 v151, v3
	v_mov_b32_e32 v134, v3
	v_mov_b32_e32 v138, v3
	v_mov_b32_e32 v135, v3
	v_mov_b32_e32 v181, v3
	v_mov_b32_e32 v170, v3
	v_mov_b32_e32 v166, v3
	v_mov_b32_e32 v154, v3
	v_mov_b32_e32 v149, v3
	v_mov_b32_e32 v147, v3
	v_mov_b32_e32 v128, v3
	v_mov_b32_e32 v126, v3
	v_mov_b32_e32 v176, v3
	v_mov_b32_e32 v173, v3
	v_mov_b32_e32 v168, v3
	v_mov_b32_e32 v156, v3
	v_mov_b32_e32 v158, v3
	v_mov_b32_e32 v141, v3
	v_mov_b32_e32 v132, v3
	v_mov_b32_e32 v130, v3
	v_mov_b32_e32 v183, v3
	v_mov_b32_e32 v179, v3
	v_mov_b32_e32 v163, v3
	v_mov_b32_e32 v161, v3
	v_mov_b32_e32 v152, v3
	v_mov_b32_e32 v136, v3
	v_mov_b32_e32 v139, v3
	v_mov_b32_e32 v137, v3
	v_mov_b32_e32 v187, v3
	v_mov_b32_e32 v190, v3
	v_mov_b32_e32 v192, v3
	v_mov_b32_e32 v191, v3
	v_mov_b32_e32 v186, v3
	v_mov_b32_e32 v188, v3
	v_mov_b32_e32 v185, v3
	v_mov_b32_e32 v189, v3
	v_mov_b32_e32 v174, v3
	v_mov_b32_e32 v171, v3
	v_mov_b32_e32 v164, v3
	v_mov_b32_e32 v150, v3
	v_mov_b32_e32 v144, v3
	v_mov_b32_e32 v133, v3
	v_mov_b32_e32 v122, v3
	v_mov_b32_e32 v121, v3
	v_mov_b32_e32 v177, v3
	v_mov_b32_e32 v184, v3
	v_mov_b32_e32 v159, v3
	v_mov_b32_e32 v145, v3
	v_mov_b32_e32 v143, v3
	v_mov_b32_e32 v123, v3
	v_mov_b32_e32 v124, v3
	v_mov_b32_e32 v142, v3
	s_cbranch_vccnz .LBB0_407
	v_mov_b32_e32 v2, v0
	s_load_dwordx2 s[4:5], s[40:41], 0x98
	s_lshl_b64 s[10:11], s[52:53], 1
	s_lshl_b32 s48, s9, 8
	v_bfe_u32 v77, v2, 6, 2
	v_and_b32_e32 v76, 63, v2
	s_waitcnt lgkmcnt(0)
	s_add_u32 s4, s4, s10
	v_lshlrev_b32_e32 v2, 15, v77
	s_addc_u32 s5, s5, s11
	v_lshl_add_u64 v[8:9], s[4:5], 0, v[2:3]
	v_lshlrev_b32_e32 v6, 2, v76
	v_mov_b32_e32 v7, v3
	v_lshl_add_u64 v[8:9], v[8:9], 0, s[48:49]
	s_lshl_b32 s48, s8, 7
	v_lshlrev_b32_e32 v4, 1, v76
	v_mov_b32_e32 v5, v3
	v_lshl_add_u64 v[12:13], v[8:9], 0, v[6:7]
	v_lshl_add_u64 v[6:7], v[8:9], 0, s[48:49]
	s_mov_b32 s4, 0xa201000
	v_lshl_add_u64 v[10:11], v[6:7], 0, v[4:5]
	v_add_co_u32_e32 v4, vcc, s4, v12
	s_mov_b32 s4, 0xe201000
	s_nop 0
	v_addc_co_u32_e32 v5, vcc, 0, v13, vcc
	v_add_co_u32_e32 v14, vcc, s4, v12
	s_mov_b32 s4, 0x12201000
	s_nop 0
	v_addc_co_u32_e32 v15, vcc, 0, v13, vcc
	v_add_co_u32_e32 v6, vcc, s4, v10
	s_mov_b32 s4, 0xa203000
	s_nop 0
	v_addc_co_u32_e32 v7, vcc, 0, v11, vcc
	v_add_co_u32_e32 v24, vcc, s4, v12
	s_mov_b32 s4, 0xe203000
	s_nop 0
	v_addc_co_u32_e32 v25, vcc, 0, v13, vcc
	v_add_co_u32_e32 v20, vcc, s4, v12
	s_mov_b32 s4, 0x12203000
	s_nop 0
	v_addc_co_u32_e32 v21, vcc, 0, v13, vcc
	v_add_co_u32_e32 v8, vcc, s4, v10
	s_mov_b32 s4, 0xa205000
	s_nop 0
	v_addc_co_u32_e32 v9, vcc, 0, v11, vcc
	v_add_co_u32_e32 v28, vcc, s4, v12
	s_mov_b32 s4, 0xe205000
	s_nop 0
	v_addc_co_u32_e32 v29, vcc, 0, v13, vcc
	v_add_co_u32_e32 v22, vcc, s4, v12
	s_mov_b32 s4, 0x12205000
	s_nop 0
	v_addc_co_u32_e32 v23, vcc, 0, v13, vcc
	v_add_co_u32_e32 v16, vcc, s4, v10
	s_mov_b32 s4, 0xa207000
	s_nop 0
	v_addc_co_u32_e32 v17, vcc, 0, v11, vcc
	v_add_co_u32_e32 v18, vcc, s4, v12
	s_mov_b32 s4, 0xe207000
	s_nop 0
	v_addc_co_u32_e32 v19, vcc, 0, v13, vcc
	v_add_co_u32_e32 v32, vcc, s4, v12
	s_mov_b32 s4, 0x12207000
	s_nop 0
	v_addc_co_u32_e32 v33, vcc, 0, v13, vcc
	v_add_co_u32_e32 v26, vcc, s4, v10
	s_mov_b32 s4, 0xa221000
	s_nop 0
	v_addc_co_u32_e32 v27, vcc, 0, v11, vcc
	v_add_co_u32_e32 v30, vcc, s4, v12
	s_mov_b32 s4, 0xe221000
	s_nop 0
	v_addc_co_u32_e32 v31, vcc, 0, v13, vcc
	v_add_co_u32_e32 v34, vcc, s4, v12
	s_mov_b32 s4, 0x12221000
	s_nop 0
	v_addc_co_u32_e32 v35, vcc, 0, v13, vcc
	v_add_co_u32_e32 v36, vcc, s4, v10
	s_mov_b32 s4, 0xa223000
	s_nop 0
	v_addc_co_u32_e32 v37, vcc, 0, v11, vcc
	v_add_co_u32_e32 v38, vcc, s4, v12
	s_mov_b32 s4, 0xe223000
	s_nop 0
	v_addc_co_u32_e32 v39, vcc, 0, v13, vcc
	v_add_co_u32_e32 v40, vcc, s4, v12
	s_mov_b32 s4, 0x12223000
	s_nop 0
	v_addc_co_u32_e32 v41, vcc, 0, v13, vcc
	v_add_co_u32_e32 v42, vcc, s4, v10
	s_mov_b32 s4, 0xa225000
	s_nop 0
	v_addc_co_u32_e32 v43, vcc, 0, v11, vcc
	v_add_co_u32_e32 v44, vcc, s4, v12
	s_mov_b32 s4, 0xe225000
	s_nop 0
	v_addc_co_u32_e32 v45, vcc, 0, v13, vcc
	v_add_co_u32_e32 v46, vcc, s4, v12
	s_mov_b32 s4, 0x12225000
	s_nop 0
	v_addc_co_u32_e32 v47, vcc, 0, v13, vcc
	v_add_co_u32_e32 v48, vcc, s4, v10
	s_mov_b32 s4, 0xa227000
	s_nop 0
	v_addc_co_u32_e32 v49, vcc, 0, v11, vcc
	v_add_co_u32_e32 v50, vcc, s4, v12
	s_mov_b32 s4, 0xe227000
	s_nop 0
	v_addc_co_u32_e32 v51, vcc, 0, v13, vcc
	v_add_co_u32_e32 v52, vcc, s4, v12
	s_mov_b32 s4, 0x12227000
	s_nop 0
	v_addc_co_u32_e32 v53, vcc, 0, v13, vcc
	v_add_co_u32_e32 v54, vcc, s4, v10
	s_mov_b32 s4, 0xa241000
	s_nop 0
	v_addc_co_u32_e32 v55, vcc, 0, v11, vcc
	v_add_co_u32_e32 v56, vcc, s4, v12
	s_mov_b32 s4, 0xe241000
	s_nop 0
	v_addc_co_u32_e32 v57, vcc, 0, v13, vcc
	v_add_co_u32_e32 v58, vcc, s4, v12
	s_mov_b32 s4, 0x12241000
	s_nop 0
	v_addc_co_u32_e32 v59, vcc, 0, v13, vcc
	v_add_co_u32_e32 v60, vcc, s4, v10
	s_mov_b32 s4, 0xa243000
	s_nop 0
	v_addc_co_u32_e32 v61, vcc, 0, v11, vcc
	v_add_co_u32_e32 v62, vcc, s4, v12
	global_load_dword v123, v[24:25], off offset:-4096
	global_load_dword v143, v[24:25], off
	global_load_dword v121, v[14:15], off offset:-4096
	global_load_ushort v185, v[6:7], off
	global_load_dword v122, v[14:15], off
	global_load_dword v124, v[4:5], off
	v_addc_co_u32_e32 v63, vcc, 0, v13, vcc
	v_add_co_u32_e32 v64, vcc, s74, v12
	global_load_dword v145, v[28:29], off offset:-4096
	global_load_dword v164, v[22:23], off
	global_load_dword v159, v[28:29], off
	global_load_dword v133, v[20:21], off offset:-4096
	global_load_ushort v186, v[8:9], off
	global_load_dword v144, v[20:21], off
	v_addc_co_u32_e32 v65, vcc, 0, v13, vcc
	v_add_co_u32_e32 v66, vcc, s75, v10
	global_load_dword v150, v[22:23], off offset:-4096
	s_nop 0
	v_addc_co_u32_e32 v67, vcc, 0, v11, vcc
	v_add_co_u32_e32 v68, vcc, s76, v12
	global_load_dword v171, v[32:33], off offset:-4096
	global_load_ushort v187, v[26:27], off
	global_load_dword v174, v[32:33], off
	global_load_dword v177, v[18:19], off
	v_addc_co_u32_e32 v69, vcc, 0, v13, vcc
	v_add_co_u32_e32 v70, vcc, s77, v12
	v_lshlrev_b32_e32 v2, 9, v77
	s_nop 0
	v_addc_co_u32_e32 v71, vcc, 0, v13, vcc
	v_add_co_u32_e32 v72, vcc, s79, v12
	s_waitcnt vmcnt(14)
; #define LAS __attribute__((address_space(3)))
; template <int SET> DI void h_load8(unsigned (&CR)[72], const bf16_t* qp, const bf16_t* fp, const bf16_t* ip, int c) {
; #pragma unroll
;     for (int j = 0; j < 8; ++j) { const size_t ro = (size_t)(32 * c + j) * D; CR[24 * SET + j] = *(const unsigned*)(qp + ro); CR[24 * SET + 8 + j] = *(const unsigned*)(fp + ro); CR[24 * SET + 16 + j] = ip[ro]; }
; }
; template <int SET> DI void h_totals8(const unsigned (&CR)[72], LAS unsigned char* buf, int tgp, int k2) {
;     float lo = 0.f, hi = 0.f;
; #pragma unroll
;     for (int j = 0; j < 8; ++j) { lo += bflo(CR[24 * SET + 8 + j]); hi += bfhi(CR[24 * SET + 8 + j]); }
;     *(LAS f32x2_t*)(buf + H_TOT + (tgp * 128 + 2 * k2) * 4) = (f32x2_t){lo, hi};
; }
; template <int SET> DI void h_prep8(const unsigned (&CR)[72], LAS unsigned char* buf, int tgp, int k2, int v64) {
;     float base0 = 0.f, base1 = 0.f, bm0 = 0.f, bm1 = 0.f, bl0 = 0.f, bl1 = 0.f;
; #pragma unroll
;     for (int g = 0; g < 4; ++g) { const f32x2_t tt = *(const LAS f32x2_t*)(buf + H_TOT + (g * 128 + 2 * k2) * 4);
;         if (g < tgp) { base0 += tt[0]; base1 += tt[1]; } if (g < 2) { bm0 += tt[0]; bm1 += tt[1]; } bl0 += tt[0]; bl1 += tt[1]; }
;     const float ebm0 = __expf(bm0), ebm1 = __expf(bm1), elm0 = __expf(bl0 - bm0), elm1 = __expf(bl1 - bm1);
;     float e20 = __expf(base0 - bm0), e21 = __expf(base1 - bm1); unsigned kup0[4], kup1[4];
	v_lshlrev_b32_e32 v14, 16, v121
	v_addc_co_u32_e32 v73, vcc, 0, v13, vcc
	v_add_co_u32_e32 v12, vcc, s80, v12
	v_and_b32_e32 v15, 0xffff0000, v121
	s_nop 0
	v_addc_co_u32_e32 v13, vcc, 0, v13, vcc
	v_add_co_u32_e32 v74, vcc, s78, v10
	v_add_f32_e32 v15, 0, v15
	v_add_f32_e32 v14, 0, v14
	s_nop 0
	v_addc_co_u32_e32 v75, vcc, 0, v11, vcc
	v_add_co_u32_e32 v10, vcc, s81, v10
	s_waitcnt vmcnt(12)
	v_lshlrev_b32_e32 v24, 16, v122
	v_addc_co_u32_e32 v11, vcc, 0, v11, vcc
	global_load_ushort v188, v[8:9], off offset:-4096
	global_load_ushort v189, v[6:7], off offset:-4096
	global_load_dword v142, v[4:5], off offset:-4096
	global_load_ushort v190, v[26:27], off offset:-4096
	global_load_ushort v191, v[16:17], off offset:-4096
	global_load_ushort v192, v[16:17], off
	global_load_dword v184, v[18:19], off offset:-4096
	global_load_ushort v126, v[36:37], off offset:-4096
	global_load_ushort v128, v[36:37], off
	global_load_dword v136, v[38:39], off offset:-4096
	global_load_dword v152, v[38:39], off
	global_load_dword v130, v[34:35], off offset:-4096
	global_load_dword v132, v[34:35], off
	global_load_dword v137, v[30:31], off offset:-4096
	global_load_dword v139, v[30:31], off
	global_load_ushort v147, v[42:43], off offset:-4096
	global_load_ushort v149, v[42:43], off
	global_load_dword v156, v[46:47], off offset:-4096
	global_load_dword v168, v[46:47], off
	global_load_dword v161, v[44:45], off offset:-4096
	global_load_dword v163, v[44:45], off
	global_load_dword v141, v[40:41], off offset:-4096
	global_load_dword v158, v[40:41], off
	global_load_ushort v154, v[48:49], off offset:-4096
	global_load_ushort v166, v[48:49], off
	global_load_ushort v170, v[54:55], off offset:-4096
	global_load_ushort v181, v[54:55], off
	global_load_dword v173, v[52:53], off offset:-4096
	global_load_dword v176, v[52:53], off
	global_load_dword v179, v[50:51], off offset:-4096
	global_load_dword v183, v[50:51], off
	global_load_ushort v125, v[60:61], off offset:-4096
	global_load_ushort v127, v[60:61], off
	global_load_dword v134, v[62:63], off offset:-4096
	global_load_dword v151, v[62:63], off
	global_load_dword v129, v[58:59], off offset:-4096
	global_load_dword v131, v[58:59], off
	global_load_dword v135, v[56:57], off offset:-4096
	global_load_dword v138, v[56:57], off
	global_load_ushort v146, v[66:67], off offset:-4096
	global_load_ushort v148, v[66:67], off
	global_load_dword v155, v[70:71], off offset:-4096
	global_load_dword v167, v[70:71], off
	global_load_dword v160, v[68:69], off offset:-4096
	global_load_dword v162, v[68:69], off
	global_load_dword v140, v[64:65], off offset:-4096
	global_load_dword v157, v[64:65], off
	global_load_ushort v153, v[74:75], off offset:-4096
	global_load_ushort v165, v[74:75], off
	global_load_ushort v169, v[10:11], off offset:-4096
	global_load_ushort v180, v[10:11], off
	global_load_dword v172, v[12:13], off offset:-4096
	global_load_dword v175, v[12:13], off
	global_load_dword v178, v[72:73], off offset:-4096
	global_load_dword v182, v[72:73], off
	v_and_b32_e32 v25, 0xffff0000, v122
	v_add_f32_e32 v15, v15, v25
	v_add_f32_e32 v14, v14, v24
	s_waitcnt vmcnt(62)
	v_lshlrev_b32_e32 v20, 16, v133
	v_and_b32_e32 v21, 0xffff0000, v133
	v_add_f32_e32 v15, v15, v21
	v_add_f32_e32 v14, v14, v20
	s_waitcnt vmcnt(60)
	v_lshlrev_b32_e32 v20, 16, v144
	v_and_b32_e32 v21, 0xffff0000, v144
	v_add_f32_e32 v15, v15, v21
	v_add_f32_e32 v14, v14, v20
	s_waitcnt vmcnt(59)
	v_lshlrev_b32_e32 v20, 16, v150
	v_and_b32_e32 v21, 0xffff0000, v150
	v_add_f32_e32 v15, v15, v21
	v_add_f32_e32 v14, v14, v20
	v_lshlrev_b32_e32 v20, 16, v164
	v_and_b32_e32 v21, 0xffff0000, v164
	v_add_f32_e32 v15, v15, v21
	v_add_f32_e32 v14, v14, v20
	s_waitcnt vmcnt(58)
	v_lshlrev_b32_e32 v20, 16, v171
	v_and_b32_e32 v21, 0xffff0000, v171
	v_add_f32_e32 v15, v15, v21
	v_add_f32_e32 v14, v14, v20
	s_waitcnt vmcnt(56)
	v_lshlrev_b32_e32 v20, 16, v174
	v_and_b32_e32 v21, 0xffff0000, v174
	v_lshlrev_b32_e32 v4, 3, v76
	v_add_f32_e32 v15, v15, v21
	v_add_f32_e32 v14, v14, v20
	v_add3_u32 v2, 0, v2, v4
	ds_write_b64 v2, v[14:15] offset:41984
.LBB0_407:
	s_and_b64 vcc, exec, s[36:37]
	s_waitcnt lgkmcnt(0)
	s_barrier
	s_cbranch_vccnz .LBB0_411
	v_mov_b32_e32 v2, v0
	s_nop 0
	v_and_b32_e32 v8, 63, v2
	v_lshlrev_b32_e32 v6, 3, v8
	v_add_u32_e32 v18, 0, v6
	ds_read2st64_b64 v[10:13], v18 offset0:82 offset1:83
	ds_read2st64_b64 v[14:17], v18 offset0:84 offset1:85
	v_bfe_u32 v7, v2, 6, 2
	v_cmp_eq_u32_e32 vcc, 0, v7
	v_cmp_lt_u32_e64 s[4:5], 1, v7
	s_waitcnt lgkmcnt(1)
	v_add_f32_e32 v2, 0, v10
	v_add_f32_e32 v4, 0, v11
	v_cndmask_b32_e64 v9, v2, 0, vcc
	v_cndmask_b32_e64 v5, v4, 0, vcc
	v_add_f32_e32 v10, v12, v9
	v_add_f32_e32 v11, v13, v5
	v_cndmask_b32_e64 v10, v9, v10, s[4:5]
	v_cndmask_b32_e64 v11, v5, v11, s[4:5]
	v_add_f32_e32 v9, v2, v12
	s_waitcnt lgkmcnt(0)
	v_add_f32_e32 v2, v14, v10
	v_cmp_eq_u32_e64 s[4:5], 3, v7
	v_add_f32_e32 v5, v4, v13
	v_add_f32_e32 v4, v15, v11
	v_cndmask_b32_e64 v10, v10, v2, s[4:5]
	v_add_f32_e32 v2, v9, v14
	v_add_f32_e32 v2, v2, v16
	v_cndmask_b32_e64 v11, v11, v4, s[4:5]
	v_add_f32_e32 v4, v5, v15
	v_sub_f32_e32 v2, v2, v9
	v_add_f32_e32 v12, v4, v17
	v_mul_f32_e32 v2, 0x3fb8aa3b, v2
	v_exp_f32_e32 v4, v2
	v_sub_f32_e32 v2, v12, v5
	v_sub_f32_e32 v10, v10, v9
	v_sub_f32_e32 v11, v11, v5
	v_lshlrev_b32_e32 v12, 16, v121
	v_and_b32_e32 v13, 0xffff0000, v121
	v_mul_f32_e32 v10, 0x3fb8aa3b, v10
	v_mul_f32_e32 v11, 0x3fb8aa3b, v11
	v_mul_f32_e32 v12, 0x3fb8aa3b, v12
	v_mul_f32_e32 v13, 0x3fb8aa3b, v13
	v_exp_f32_e32 v10, v10
	v_exp_f32_e32 v11, v11
	v_exp_f32_e32 v12, v12
	v_exp_f32_e32 v13, v13
	v_lshlrev_b32_e32 v14, 2, v8
	v_sub_u32_e32 v18, v18, v14
	s_waitcnt vmcnt(52)
; template <int SET> DI void h_prep8(const unsigned (&CR)[72], LAS unsigned char* buf, int tgp, int k2, int v64) {
;     float base0 = 0.f, base1 = 0.f, bm0 = 0.f, bm1 = 0.f, bl0 = 0.f, bl1 = 0.f;
; #pragma unroll
;     for (int g = 0; g < 4; ++g) { const f32x2_t tt = *(const LAS f32x2_t*)(buf + H_TOT + (g * 128 + 2 * k2) * 4);
;         if (g < tgp) { base0 += tt[0]; base1 += tt[1]; } if (g < 2) { bm0 += tt[0]; bm1 += tt[1]; } bl0 += tt[0]; bl1 += tt[1]; }
;     const float ebm0 = __expf(bm0), ebm1 = __expf(bm1), elm0 = __expf(bl0 - bm0), elm1 = __expf(bl1 - bm1);
;     float e20 = __expf(base0 - bm0), e21 = __expf(base1 - bm1); unsigned kup0[4], kup1[4];
; #pragma unroll
;     for (int jp = 0; jp < 4; ++jp) {
;         float ku0[2], ku1[2];
; #pragma unroll
;         for (int jj = 0; jj < 2; ++jj) {
;             const int j = 2 * jp + jj;
;             const unsigned fw = CR[24 * SET + 8 + j], qw = CR[24 * SET + j];
;             const float f0 = __expf(bflo(fw)), f1 = __expf(bfhi(fw)), q0 = bflo(qw), q1 = bfhi(qw);
;             e20 *= f0; e21 *= f1;
;             const float e30 = __builtin_amdgcn_rcpf(e20), e31 = __builtin_amdgcn_rcpf(e21);
;             const float kk0 = 1.0f - f0, kk1 = 1.0f - f1;
;             const int t = 8 * tgp + j;
;             *(LAS unsigned*)(buf + H_QS + t * 272 + 4 * k2) = pk2(q0 * e20, q1 * e21);
;             *(LAS unsigned*)(buf + H_KS + t * 272 + 4 * k2) = pk2(kk0 * e30, kk1 * e31);
;             ku0[jj] = kk0 * e30 * elm0; ku1[jj] = kk1 * e31 * elm1;
;         }
;         kup0[jp] = pk2(ku0[0], ku0[1]); kup1[jp] = pk2(ku1[0], ku1[1]);
;     }
;     { u32x4 w; w.x = kup0[0]; w.y = kup0[1]; w.z = kup0[2]; w.w = kup0[3]; *(LAS u32x4*)(buf + H_KU + (2 * k2) * 80 + 16 * tgp) = w;
;       w.x = kup1[0]; w.y = kup1[1]; w.z = kup1[2]; w.w = kup1[3]; *(LAS u32x4*)(buf + H_KU + (2 * k2 + 1) * 80 + 16 * tgp) = w; }
;     if (tgp == 0) { *(LAS f32x2_t*)(buf + H_DEC + 8 * k2) = (f32x2_t){ebm0 * elm0, ebm1 * elm1}; *(LAS f32x2_t*)(buf + H_EBM + 8 * k2) = (f32x2_t){ebm0, ebm1}; }
;     { u32x4 w; w.x = (CR[24 * SET + 16] & 0xffffu) | (CR[24 * SET + 17] << 16); w.y = (CR[24 * SET + 18] & 0xffffu) | (CR[24 * SET + 19] << 16);
;       w.z = (CR[24 * SET + 20] & 0xffffu) | (CR[24 * SET + 21] << 16); w.w = (CR[24 * SET + 22] & 0xffffu) | (CR[24 * SET + 23] << 16);
;       *(LAS u32x4*)(buf + H_VT + v64 * 80 + 16 * tgp) = w; }
; }
	v_lshlrev_b32_e32 v14, 16, v142
	v_and_b32_e32 v15, 0xffff0000, v142
	v_mul_f32_e32 v11, v13, v11
	v_mul_f32_e32 v10, v12, v10
	v_mad_u32_u24 v28, v7, s82, v18
	v_mul_f32_e32 v15, v11, v15
	v_mul_f32_e32 v14, v10, v14
	v_rcp_f32_e32 v16, v10
	v_cvt_pk_bf16_f32 v20, v14, v15
	v_lshlrev_b32_e32 v14, 16, v122
	v_and_b32_e32 v15, 0xffff0000, v122
	v_mul_f32_e32 v14, 0x3fb8aa3b, v14
	v_mul_f32_e32 v15, 0x3fb8aa3b, v15
	v_exp_f32_e32 v14, v14
	v_exp_f32_e32 v15, v15
	v_rcp_f32_e32 v17, v11
	v_sub_f32_e32 v13, 1.0, v13
	v_sub_f32_e32 v12, 1.0, v12
	v_mul_f32_e32 v2, 0x3fb8aa3b, v2
	v_mul_f32_e32 v11, v15, v11
	v_mul_f32_e32 v10, v14, v10
	v_mul_f32_e32 v13, v13, v17
	v_mul_f32_e32 v12, v12, v16
	v_rcp_f32_e32 v18, v10
	v_rcp_f32_e32 v19, v11
	v_lshlrev_b32_e32 v16, 16, v124
	v_and_b32_e32 v17, 0xffff0000, v124
	v_mul_f32_e32 v17, v11, v17
	v_mul_f32_e32 v16, v10, v16
	v_sub_f32_e32 v15, 1.0, v15
	v_sub_f32_e32 v14, 1.0, v14
	v_cvt_pk_bf16_f32 v16, v16, v17
	v_add_u32_e32 v17, 0x2000, v28
	v_mul_f32_e32 v15, v15, v19
	v_mul_f32_e32 v14, v14, v18
	v_cvt_pk_bf16_f32 v21, v12, v13
	ds_write2_b32 v17, v20, v16 offset0:128 offset1:196
	v_cvt_pk_bf16_f32 v16, v14, v15
	v_mov_b32_e32 v17, v14
	v_mov_b32_e32 v14, v13
	v_lshlrev_b32_e32 v13, 16, v133
	v_mul_f32_e32 v13, 0x3fb8aa3b, v13
	v_exp_f32_e32 v18, v13
	v_and_b32_e32 v13, 0xffff0000, v133
	v_exp_f32_e32 v2, v2
	v_mul_f32_e32 v13, 0x3fb8aa3b, v13
	v_exp_f32_e32 v19, v13
	v_add_u32_e32 v24, 0x4400, v28
	ds_write2_b32 v24, v21, v16 offset1:68
	v_mov_b32_e32 v16, v12
	v_mul_f32_e32 v17, v4, v17
	v_mul_f32_e32 v16, v4, v16
	v_mul_f32_e32 v15, v2, v15
	v_mul_f32_e32 v14, v2, v14
	v_cvt_pk_bf16_f32 v12, v16, v17
	v_cvt_pk_bf16_f32 v16, v14, v15
	v_lshlrev_b32_e32 v14, 16, v123
	v_and_b32_e32 v15, 0xffff0000, v123
	v_mul_f32_e32 v11, v19, v11
	v_mul_f32_e32 v10, v18, v10
	v_lshlrev_b32_e32 v17, 16, v144
	v_mul_f32_e32 v15, v11, v15
	v_mul_f32_e32 v14, v10, v14
	v_mul_f32_e32 v17, 0x3fb8aa3b, v17
	v_cvt_pk_bf16_f32 v13, v14, v15
	v_sub_f32_e32 v15, 1.0, v19
	v_sub_f32_e32 v14, 1.0, v18
	v_exp_f32_e32 v18, v17
	v_and_b32_e32 v17, 0xffff0000, v144
	v_mul_f32_e32 v17, 0x3fb8aa3b, v17
	v_exp_f32_e32 v19, v17
	v_rcp_f32_e32 v20, v10
	v_rcp_f32_e32 v21, v11
	v_add_u32_e32 v25, 0x2400, v28
	v_mul_f32_e32 v11, v19, v11
	v_mul_f32_e32 v10, v18, v10
	v_sub_f32_e32 v19, 1.0, v19
	v_sub_f32_e32 v18, 1.0, v18
	v_rcp_f32_e32 v22, v10
	v_rcp_f32_e32 v23, v11
	v_mul_f32_e32 v15, v15, v21
	v_mul_f32_e32 v14, v14, v20
	v_lshlrev_b32_e32 v20, 16, v143
	v_and_b32_e32 v21, 0xffff0000, v143
	v_mul_f32_e32 v21, v11, v21
	v_mul_f32_e32 v20, v10, v20
	v_mul_f32_e32 v19, v19, v23
	v_mul_f32_e32 v18, v18, v22
	v_cvt_pk_bf16_f32 v20, v20, v21
	v_cvt_pk_bf16_f32 v17, v14, v15
	ds_write2_b32 v25, v13, v20 offset0:8 offset1:76
	v_cvt_pk_bf16_f32 v13, v18, v19
	ds_write2_b32 v24, v17, v13 offset0:136 offset1:204
	v_lshlrev_b32_e32 v17, 16, v150
	v_mov_b32_e32 v21, v18
	v_mov_b32_e32 v18, v15
	v_mul_f32_e32 v17, 0x3fb8aa3b, v17
	v_mov_b32_e32 v20, v14
	v_mul_f32_e32 v15, v2, v19
	v_mul_f32_e32 v14, v2, v18
	v_exp_f32_e32 v18, v17
	v_and_b32_e32 v17, 0xffff0000, v150
	v_mul_f32_e32 v17, 0x3fb8aa3b, v17
	v_exp_f32_e32 v19, v17
	v_cvt_pk_bf16_f32 v17, v14, v15
	v_lshlrev_b32_e32 v14, 16, v145
	v_and_b32_e32 v15, 0xffff0000, v145
	v_mul_f32_e32 v11, v19, v11
	v_mul_f32_e32 v10, v18, v10
	v_mul_f32_e32 v21, v4, v21
	v_mul_f32_e32 v20, v4, v20
	v_mul_f32_e32 v15, v11, v15
	v_mul_f32_e32 v14, v10, v14
	v_cvt_pk_bf16_f32 v13, v20, v21
	v_cvt_pk_bf16_f32 v24, v14, v15
	v_sub_f32_e32 v15, 1.0, v19
	v_sub_f32_e32 v14, 1.0, v18
	v_lshlrev_b32_e32 v18, 16, v164
	v_and_b32_e32 v19, 0xffff0000, v164
	v_mul_f32_e32 v18, 0x3fb8aa3b, v18
	v_mul_f32_e32 v19, 0x3fb8aa3b, v19
	v_exp_f32_e32 v18, v18
	v_exp_f32_e32 v19, v19
	v_rcp_f32_e32 v20, v10
	v_rcp_f32_e32 v21, v11
	v_add_u32_e32 v29, 0x4800, v28
	v_mul_f32_e32 v11, v19, v11
	v_mul_f32_e32 v10, v18, v10
	v_sub_f32_e32 v19, 1.0, v19
	v_sub_f32_e32 v18, 1.0, v18
	v_rcp_f32_e32 v22, v10
	v_rcp_f32_e32 v23, v11
	v_mul_f32_e32 v15, v15, v21
	v_mul_f32_e32 v14, v14, v20
	v_lshlrev_b32_e32 v20, 16, v159
	v_and_b32_e32 v21, 0xffff0000, v159
	v_mul_f32_e32 v21, v11, v21
	v_mul_f32_e32 v20, v10, v20
	v_mul_f32_e32 v19, v19, v23
	v_mul_f32_e32 v18, v18, v22
	v_cvt_pk_bf16_f32 v20, v20, v21
	v_cvt_pk_bf16_f32 v26, v14, v15
	ds_write2_b32 v25, v24, v20 offset0:144 offset1:212
	v_cvt_pk_bf16_f32 v20, v18, v19
	ds_write2_b32 v29, v26, v20 offset0:16 offset1:84
	v_mov_b32_e32 v20, v14
	v_mov_b32_e32 v21, v18
	v_mov_b32_e32 v18, v15
	v_lshlrev_b32_e32 v15, 16, v171
	v_mul_f32_e32 v21, v4, v21
	v_mul_f32_e32 v20, v4, v20
	v_mul_f32_e32 v15, 0x3fb8aa3b, v15
	v_cvt_pk_bf16_f32 v14, v20, v21
	v_exp_f32_e32 v20, v15
	v_and_b32_e32 v15, 0xffff0000, v171
	v_mul_f32_e32 v15, 0x3fb8aa3b, v15
	v_exp_f32_e32 v21, v15
	v_mul_f32_e32 v19, v2, v19
	v_mul_f32_e32 v18, v2, v18
	v_cvt_pk_bf16_f32 v18, v18, v19
	s_waitcnt vmcnt(48)
	v_lshlrev_b32_e32 v22, 16, v184
	v_and_b32_e32 v23, 0xffff0000, v184
	v_mul_f32_e32 v11, v21, v11
	v_mul_f32_e32 v10, v20, v10
	v_lshlrev_b32_e32 v19, 16, v174
	v_mul_f32_e32 v23, v11, v23
	v_mul_f32_e32 v22, v10, v22
	v_mul_f32_e32 v19, 0x3fb8aa3b, v19
	v_cvt_pk_bf16_f32 v15, v22, v23
	v_exp_f32_e32 v22, v19
	v_and_b32_e32 v19, 0xffff0000, v174
	v_mul_f32_e32 v19, 0x3fb8aa3b, v19
	v_exp_f32_e32 v23, v19
	v_rcp_f32_e32 v24, v10
	v_rcp_f32_e32 v25, v11
	v_sub_f32_e32 v21, 1.0, v21
	v_sub_f32_e32 v20, 1.0, v20
	v_mul_f32_e32 v11, v23, v11
	v_mul_f32_e32 v10, v22, v10
	v_mul_f32_e32 v21, v21, v25
	v_mul_f32_e32 v20, v20, v24
	v_lshlrev_b32_e32 v24, 16, v177
	v_and_b32_e32 v25, 0xffff0000, v177
	v_rcp_f32_e32 v26, v10
	v_rcp_f32_e32 v27, v11
	v_mul_f32_e32 v11, v11, v25
	v_mul_f32_e32 v10, v10, v24
	v_cvt_pk_bf16_f32 v19, v20, v21
	v_cvt_pk_bf16_f32 v10, v10, v11
	v_add_u32_e32 v11, 0x2800, v28
	ds_write2_b32 v11, v15, v10 offset0:24 offset1:92
	v_sub_f32_e32 v11, 1.0, v23
	v_sub_f32_e32 v10, 1.0, v22
	v_mov_b32_e32 v22, v20
	v_mul_f32_e32 v11, v11, v27
	v_mul_f32_e32 v10, v10, v26
	s_nop 0
	v_cvt_pk_bf16_f32 v15, v10, v11
	v_mov_b32_e32 v23, v10
	v_mov_b32_e32 v10, v21
	v_mul_f32_e32 v11, v2, v11
	v_mul_f32_e32 v10, v2, v10
	ds_write2_b32 v29, v19, v15 offset0:152 offset1:220
	v_mul_f32_e32 v23, v4, v23
	v_mul_f32_e32 v22, v4, v22
	v_cvt_pk_bf16_f32 v19, v10, v11
	v_mad_u32_u24 v10, v8, s83, 0
	v_lshlrev_b32_e32 v11, 4, v7
	v_cvt_pk_bf16_f32 v15, v22, v23
	v_add_u32_e32 v20, v10, v11
	ds_write_b128 v20, v[12:15] offset:26112
	ds_write_b128 v20, v[16:19] offset:26192
	s_and_saveexec_b64 s[4:5], vcc
	s_cbranch_execz .LBB0_410
	v_mul_f32_e32 v9, 0x3fb8aa3b, v9
	v_mul_f32_e32 v5, 0x3fb8aa3b, v5
	v_exp_f32_e32 v12, v9
	v_exp_f32_e32 v13, v5
	v_mov_b32_e32 v5, v2
	v_mad_i32_i24 v9, v8, s84, v10
	v_mul_f32_e32 v5, v13, v5
	v_mul_f32_e32 v4, v12, v4
	ds_write2st64_b64 v9, v[4:5], v[12:13] offset0:81 offset1:86
; #define LAS __attribute__((address_space(3)))
; template <int SET> DI void h_totals8(const unsigned (&CR)[72], LAS unsigned char* buf, int tgp, int k2) {
;     float lo = 0.f, hi = 0.f;
; #pragma unroll
;     for (int j = 0; j < 8; ++j) { lo += bflo(CR[24 * SET + 8 + j]); hi += bfhi(CR[24 * SET + 8 + j]); }
;     *(LAS f32x2_t*)(buf + H_TOT + (tgp * 128 + 2 * k2) * 4) = (f32x2_t){lo, hi};
; }
; template <int SET> DI void h_prep8(const unsigned (&CR)[72], LAS unsigned char* buf, int tgp, int k2, int v64) {
;     ...
;     { u32x4 w; w.x = (CR[24 * SET + 16] & 0xffffu) | (CR[24 * SET + 17] << 16); w.y = (CR[24 * SET + 18] & 0xffffu) | (CR[24 * SET + 19] << 16);
;       w.z = (CR[24 * SET + 20] & 0xffffu) | (CR[24 * SET + 21] << 16); w.w = (CR[24 * SET + 22] & 0xffffu) | (CR[24 * SET + 23] << 16);
;       *(LAS u32x4*)(buf + H_VT + v64 * 80 + 16 * tgp) = w; }
.LBB0_410:
	s_or_b64 exec, exec, s[4:5]
	s_waitcnt vmcnt(43)
	v_lshlrev_b32_e32 v4, 16, v130
	v_and_b32_e32 v5, 0xffff0000, v130
	v_mul_i32_i24_e32 v2, 0xffffffb0, v8
	s_waitcnt vmcnt(42)
	v_lshlrev_b32_e32 v8, 16, v132
	v_and_b32_e32 v9, 0xffff0000, v132
	v_add_f32_e32 v5, 0, v5
	v_add_f32_e32 v4, 0, v4
	v_lshl_or_b32 v12, v185, 16, v189
	v_lshl_or_b32 v13, v186, 16, v188
	v_lshl_or_b32 v14, v192, 16, v191
	v_lshl_or_b32 v15, v187, 16, v190
	v_add3_u32 v2, v10, v2, v11
	s_waitcnt vmcnt(33)
	v_lshlrev_b32_e32 v10, 16, v141
	v_and_b32_e32 v11, 0xffff0000, v141
	v_add_f32_e32 v5, v5, v9
	v_add_f32_e32 v4, v4, v8
	ds_write_b128 v2, v[12:15] offset:36352
	s_waitcnt vmcnt(32)
	v_lshlrev_b32_e32 v12, 16, v158
	v_and_b32_e32 v13, 0xffff0000, v158
	v_add_f32_e32 v5, v5, v11
	v_add_f32_e32 v4, v4, v10
	v_lshlrev_b32_e32 v14, 16, v156
	v_and_b32_e32 v15, 0xffff0000, v156
	v_add_f32_e32 v5, v5, v13
	v_add_f32_e32 v4, v4, v12
	v_lshlrev_b32_e32 v16, 16, v168
	v_and_b32_e32 v17, 0xffff0000, v168
	v_add_f32_e32 v5, v5, v15
	v_add_f32_e32 v4, v4, v14
	s_waitcnt vmcnt(27)
	v_lshlrev_b32_e32 v18, 16, v173
	v_and_b32_e32 v19, 0xffff0000, v173
	v_add_f32_e32 v5, v5, v17
	v_add_f32_e32 v4, v4, v16
	s_waitcnt vmcnt(26)
	v_lshlrev_b32_e32 v20, 16, v176
	v_and_b32_e32 v21, 0xffff0000, v176
	v_add_f32_e32 v5, v5, v19
	v_add_f32_e32 v4, v4, v18
	v_lshlrev_b32_e32 v2, 9, v7
	v_add_f32_e32 v5, v5, v21
	v_add_f32_e32 v4, v4, v20
	v_add3_u32 v2, s85, v2, v6
	ds_write_b64 v2, v[4:5]

; DI int crow(int reg, int h) { return (reg & 3) + 8 * (reg >> 2) + 4 * h; }
; #define MFMA32(a, b, c) __builtin_amdgcn_mfma_f32_32x32x16_bf16((a), (b), (c), 0, 0, 0)
; DI void h_chain(f32x16& S, f32x16& O, HPacks& K, const HOpsK& P, const bf16x8 (&vt)[2], const u32x4 (&vv)[2], int rq, int hh) {
;     f32x16 X;
;     { f32x16 Se;
; #pragma unroll
;       for (int g = 0; g < 4; ++g) {
; #pragma unroll
;           for (int e = 0; e < 4; ++e) Se[4 * g + e] = S[4 * g + e] * P.ebm[g][e]; }
;       K.sp0 = pack_step(Se, 0); K.sp1 = pack_step(Se, 1); }
; #pragma unroll
;     for (int g = 0; g < 4; ++g) {
; #pragma unroll
;         for (int e = 0; e < 4; ++e) S[4 * g + e] *= P.dec[g][e]; }
; #pragma unroll
;     for (int i = 0; i < 16; ++i) { X[i] = 0.f; O[i] = 0.f; }
;     __builtin_amdgcn_sched_barrier(0);
; #pragma unroll
;     for (int st = 0; st < 2; ++st) X = MFMA32(P.ka[st], P.qb[st], X);
; #pragma unroll
;     for (int i = 0; i < 16; ++i) X[i] = (crow(i, hh) <= rq) ? X[i] : 0.f;
;     K.xp0 = pack_step(X, 0); K.xp1 = pack_step(X, 1);
;     __builtin_amdgcn_sched_barrier(0);
;     O = MFMA32(K.xp0, __builtin_bit_cast(bf16x8, vv[0]), O);
;     O = MFMA32(__builtin_bit_cast(bf16x8, P.qq[0]), K.sp0, O);
;     O = MFMA32(K.xp1, __builtin_bit_cast(bf16x8, vv[1]), O);
;     O = MFMA32(__builtin_bit_cast(bf16x8, P.qq[1]), K.sp1, O);
; #pragma unroll
;     for (int st = 0; st < 2; ++st) S = MFMA32(P.ku[st], vt[st], S);
;     __builtin_amdgcn_sched_barrier(0);
; }
.LBB0_413:
	s_and_b32 s4, s39, 1
	v_mov_b32_e32 v2, v0
	s_mul_i32 s5, s4, 0xb400
	s_add_i32 s62, s5, 0
	v_and_b32_e32 v193, 31, v2
	v_bfe_u32 v2, v2, 5, 1
	v_or_b32_e32 v5, s3, v193
	v_mov_b32_e32 v6, s62
	s_lshl_b32 s4, s4, 14
	v_lshlrev_b32_e32 v4, 8, v2
	v_mad_u32_u24 v5, v5, s86, v6
	v_lshlrev_b32_e32 v226, 4, v2
	v_lshlrev_b32_e32 v218, 3, v2
	s_add_i32 s4, s4, 0
	v_or3_b32 v4, v4, s73, v193
	v_add_u32_e32 v7, v5, v226
	v_add_u32_e32 v5, v5, v218
	v_lshl_add_u32 v242, v4, 2, s4
	v_mov_b32_e32 v4, v193
	v_add_u32_e32 v5, 0x8800, v5
	v_lshlrev_b32_e32 v2, 2, v2
	ds_read2_b64 v[100:103], v5 offset0:192 offset1:194
	ds_read2_b64 v[104:107], v5 offset0:196 offset1:198
	ds_read_b128 v[108:111], v7 offset:36352
	ds_read_b128 v[112:115], v7 offset:36384
	v_or_b32_e32 v5, 2, v2
	v_cmp_gt_i32_e64 s[6:7], v5, v4
	v_or_b32_e32 v5, 3, v2
	v_cmp_gt_i32_e64 s[8:9], v5, v4
	v_or_b32_e32 v5, 8, v2
	v_cmp_gt_i32_e64 s[10:11], v5, v4
	v_or_b32_e32 v5, 9, v2
	v_cmp_gt_i32_e64 s[12:13], v5, v4
	v_or_b32_e32 v5, 10, v2
	v_cmp_gt_i32_e64 s[14:15], v5, v4
	v_or_b32_e32 v5, 11, v2
	v_cmp_gt_i32_e64 s[16:17], v5, v4
	v_or_b32_e32 v5, 16, v2
	v_cmp_gt_i32_e64 s[18:19], v5, v4
	v_or_b32_e32 v5, 17, v2
	v_cmp_gt_i32_e64 s[20:21], v5, v4
	v_or_b32_e32 v5, 18, v2
	v_cmp_gt_i32_e64 s[22:23], v5, v4
	v_or_b32_e32 v5, 19, v2
	v_cmp_gt_i32_e64 s[24:25], v5, v4
	v_or_b32_e32 v5, 24, v2
	v_cmp_gt_i32_e64 s[26:27], v5, v4
	v_or_b32_e32 v5, 25, v2
	v_cmp_gt_i32_e32 vcc, v2, v4
	v_cmp_lt_i32_e64 s[4:5], v2, v4
	v_cmp_gt_i32_e64 s[28:29], v5, v4
	v_or_b32_e32 v5, 26, v2
	v_or_b32_e32 v2, 27, v2
	v_mad_u32_u24 v219, v193, s87, v6
	v_cmp_gt_i32_e64 s[30:31], v5, v4
	v_cmp_gt_i32_e64 s[34:35], v2, v4
	v_or_b32_e32 v4, s63, v218
	v_add_u32_e32 v222, v219, v218
	v_lshl_add_u32 v4, v4, 1, v219
	ds_read_b128 v[84:87], v4 offset:17408
	ds_read_b128 v[88:91], v4 offset:8704
	v_add_u32_e32 v4, s64, v222
	v_add_u32_e32 v4, 0x2000, v4
	v_add_u32_e32 v220, s62, v226
	v_or_b32_e32 v2, s63, v193
	ds_read2_b64 v[92:95], v4 offset0:64 offset1:66
	v_or_b32_e32 v4, s65, v218
	v_mad_u32_u24 v2, v2, s86, v220
	v_lshl_add_u32 v4, v4, 1, v219
	ds_read_b128 v[96:99], v4 offset:17408
	ds_read_b128 v[194:197], v4 offset:8704
	ds_read_b128 v[198:201], v2 offset:26112
	ds_read_b128 v[202:205], v2 offset:26144
	v_add_u32_e32 v2, s66, v222
	v_add_u32_e32 v2, 0x2000, v2
	ds_read2_b64 v[206:209], v2 offset0:64 offset1:66
	v_or_b32_e32 v2, s67, v226
	v_add_u32_e32 v2, s62, v2
	ds_read_b128 v[4:7], v2 offset:41472
	ds_read_b128 v[8:11], v2 offset:41504
	ds_read_b128 v[12:15], v2 offset:44032
	ds_read_b128 v[16:19], v2 offset:44064
	ds_read_b128 v[20:23], v2 offset:41536
	ds_read_b128 v[24:27], v2 offset:41568
	ds_read_b128 v[28:31], v2 offset:44096
	ds_read_b128 v[32:35], v2 offset:44128
	s_waitcnt lgkmcnt(0)
	s_waitcnt lgkmcnt(1)
	v_mul_f32_e32 v29, v61, v29
	v_mul_f32_e32 v28, v60, v28
	v_mul_f32_e32 v31, v63, v31
	v_mul_f32_e32 v30, v62, v30
	s_waitcnt lgkmcnt(0)
	v_mul_f32_e32 v33, v65, v33
	v_mul_f32_e32 v32, v64, v32
	v_mul_f32_e32 v35, v67, v35
	v_mul_f32_e32 v34, v66, v34
	v_mul_f32_e32 v13, v53, v13
	v_mul_f32_e32 v12, v52, v12
	v_mul_f32_e32 v15, v55, v15
	v_mul_f32_e32 v14, v54, v14
	v_mul_f32_e32 v17, v57, v17
	v_mul_f32_e32 v16, v56, v16
	v_mul_f32_e32 v19, v59, v19
	v_mul_f32_e32 v18, v58, v18
	v_cvt_pk_bf16_f32 v214, v28, v29
	v_cvt_pk_bf16_f32 v215, v30, v31
	v_cvt_pk_bf16_f32 v216, v32, v33
	v_cvt_pk_bf16_f32 v217, v34, v35
	v_mul_f32_e32 v35, v67, v27
	v_mul_f32_e32 v34, v66, v26
	v_mul_f32_e32 v31, v63, v23
	v_mul_f32_e32 v30, v62, v22
	v_mul_f32_e32 v27, v59, v11
	v_mul_f32_e32 v26, v58, v10
	v_mul_f32_e32 v23, v55, v7
	v_mul_f32_e32 v22, v54, v6
	v_mul_f32_e32 v33, v65, v25
	v_mul_f32_e32 v32, v64, v24
	v_mul_f32_e32 v29, v61, v21
	v_mul_f32_e32 v28, v60, v20
	v_mul_f32_e32 v25, v57, v9
	v_mul_f32_e32 v24, v56, v8
	v_mul_f32_e32 v21, v53, v5
	v_mul_f32_e32 v20, v52, v4
	v_cvt_pk_bf16_f32 v210, v12, v13
	v_cvt_pk_bf16_f32 v211, v14, v15
	v_cvt_pk_bf16_f32 v212, v16, v17
	v_cvt_pk_bf16_f32 v213, v18, v19
	v_mfma_f32_32x32x16_bf16 v[4:19], v[84:87], v[88:91], 0
	v_mfma_f32_32x32x16_bf16 v[4:19], v[96:99], v[194:197], v[4:19]
	s_nop 11
	v_cndmask_b32_e64 v2, v4, 0, vcc
	v_cndmask_b32_e64 v4, 0, v5, s[4:5]
	v_cndmask_b32_e64 v5, v6, 0, s[6:7]
	v_cndmask_b32_e64 v6, v7, 0, s[8:9]
	v_cndmask_b32_e64 v7, v8, 0, s[10:11]
	v_cndmask_b32_e64 v8, v9, 0, s[12:13]
	v_cndmask_b32_e64 v9, v10, 0, s[14:15]
	v_cndmask_b32_e64 v10, v11, 0, s[16:17]
	v_cndmask_b32_e64 v11, v12, 0, s[18:19]
	v_cndmask_b32_e64 v12, v13, 0, s[20:21]
	v_cndmask_b32_e64 v13, v14, 0, s[22:23]
	v_cndmask_b32_e64 v14, v15, 0, s[24:25]
	v_cndmask_b32_e64 v15, v16, 0, s[26:27]
	v_cndmask_b32_e64 v16, v17, 0, s[28:29]
	v_cndmask_b32_e64 v17, v18, 0, s[30:31]
	v_cndmask_b32_e64 v18, v19, 0, s[34:35]
	v_cvt_pk_bf16_f32 v4, v2, v4
	v_cvt_pk_bf16_f32 v5, v5, v6
	v_cvt_pk_bf16_f32 v6, v7, v8
	v_cvt_pk_bf16_f32 v7, v9, v10
	v_cvt_pk_bf16_f32 v8, v11, v12
	v_cvt_pk_bf16_f32 v9, v13, v14
	v_cvt_pk_bf16_f32 v10, v15, v16
	v_cvt_pk_bf16_f32 v11, v17, v18
	v_mfma_f32_32x32x16_bf16 v[68:83], v[4:7], v[100:103], 0
	v_mfma_f32_32x32x16_bf16 v[68:83], v[92:95], v[210:213], v[68:83]
	v_mfma_f32_32x32x16_bf16 v[20:35], v[198:201], v[108:111], v[20:35]
	v_mfma_f32_32x32x16_bf16 v[68:83], v[8:11], v[104:107], v[68:83]
	v_mfma_f32_32x32x16_bf16 v[20:35], v[202:205], v[112:115], v[20:35]
	v_mfma_f32_32x32x16_bf16 v[68:83], v[206:209], v[214:217], v[68:83]
	s_nop 11
	v_add_f32_e32 v2, v83, v35
	v_mov_b32 v2, v2
	s_nop 0
	v_or_b32_e32 v4, s68, v218
	v_lshl_add_u32 v4, v4, 1, v219
	ds_read_b128 v[194:197], v4 offset:17408
	ds_read_b128 v[198:201], v4 offset:8704
	v_add_u32_e32 v4, s69, v222
	v_add_u32_e32 v4, 0x2000, v4
	v_or_b32_e32 v2, s68, v193
	ds_read2_b64 v[202:205], v4 offset0:64 offset1:66
	v_or_b32_e32 v4, s70, v218
	v_mad_u32_u24 v2, v2, s86, v220
	v_lshl_add_u32 v4, v4, 1, v219
	ds_read_b128 v[206:209], v4 offset:17408
	ds_read_b128 v[210:213], v4 offset:8704
	ds_read_b128 v[214:217], v2 offset:26112
	ds_read_b128 v[218:221], v2 offset:26144
	v_add_u32_e32 v2, s71, v222
	v_add_u32_e32 v2, 0x2000, v2
	ds_read2_b64 v[222:225], v2 offset0:64 offset1:66
	v_or_b32_e32 v2, s72, v226
	v_add_u32_e32 v2, s62, v2
	ds_read_b128 v[4:7], v2 offset:41472
	ds_read_b128 v[8:11], v2 offset:41504
	ds_read_b128 v[12:15], v2 offset:44032
	ds_read_b128 v[16:19], v2 offset:44064
	ds_read_b128 v[84:87], v2 offset:41536
	ds_read_b128 v[88:91], v2 offset:41568
	ds_read_b128 v[92:95], v2 offset:44096
	ds_read_b128 v[96:99], v2 offset:44128
	s_waitcnt lgkmcnt(0)
; DI void h_chain(f32x16& S, f32x16& O, HPacks& K, const HOpsK& P, const bf16x8 (&vt)[2], const u32x4 (&vv)[2], int rq, int hh) {
;     f32x16 X;
;     { f32x16 Se;
; #pragma unroll
;       for (int g = 0; g < 4; ++g) {
; #pragma unroll
;           for (int e = 0; e < 4; ++e) Se[4 * g + e] = S[4 * g + e] * P.ebm[g][e]; }
;       K.sp0 = pack_step(Se, 0); K.sp1 = pack_step(Se, 1); }
; #pragma unroll
;     for (int g = 0; g < 4; ++g) {
; #pragma unroll
;         for (int e = 0; e < 4; ++e) S[4 * g + e] *= P.dec[g][e]; }
; #pragma unroll
;     for (int i = 0; i < 16; ++i) { X[i] = 0.f; O[i] = 0.f; }
;     __builtin_amdgcn_sched_barrier(0);
; #pragma unroll
;     for (int st = 0; st < 2; ++st) X = MFMA32(P.ka[st], P.qb[st], X);
; #pragma unroll
;     for (int i = 0; i < 16; ++i) X[i] = (crow(i, hh) <= rq) ? X[i] : 0.f;
;     K.xp0 = pack_step(X, 0); K.xp1 = pack_step(X, 1);
;     __builtin_amdgcn_sched_barrier(0);
;     O = MFMA32(K.xp0, __builtin_bit_cast(bf16x8, vv[0]), O);
;     O = MFMA32(__builtin_bit_cast(bf16x8, P.qq[0]), K.sp0, O);
;     O = MFMA32(K.xp1, __builtin_bit_cast(bf16x8, vv[1]), O);
;     O = MFMA32(__builtin_bit_cast(bf16x8, P.qq[1]), K.sp1, O);
; #pragma unroll
;     for (int st = 0; st < 2; ++st) S = MFMA32(P.ku[st], vt[st], S);
;     __builtin_amdgcn_sched_barrier(0);
; }
; DI void h_mma2(f32x16& S0, f32x16& S1, LAS unsigned char* buf, LAS unsigned char* red, int kbp, int vb, int r32, int hh) {
;     int rq = r32; asm volatile("" : "+v"(rq));
;     bf16x8 vt[2]; u32x4 vv[2];
; #pragma unroll
;     for (int st = 0; st < 2; ++st) {
;         vt[st] = *(const LAS bf16x8*)(buf + H_VT + (vb * 32 + r32) * 80 + (16 * st + 8 * hh) * 2);
;         const LAS unsigned char* vp = buf + H_VT + (vb * 32 + r32) * 80 + (16 * st + 4 * hh) * 2;
;         const u32x2 v0 = *(const LAS u32x2*)vp, v1 = *(const LAS u32x2*)(vp + 16);
;         vv[st].x = v0.x; vv[st].y = v0.y; vv[st].z = v1.x; vv[st].w = v1.y;
;     }
;     f32x16 Osum;
; #pragma unroll
;     for (int kk = 0; kk < 2; ++kk) {
;         HOpsK P; h_opsk_load(P, buf, 2 * kbp + kk, r32, hh);
;         f32x16& S = (kk == 0) ? S0 : S1; f32x16 O;
;         LDS_WAIT(); __builtin_amdgcn_sched_barrier(0);
;         HPacks K;
;         h_chain(S, O, K, P, vt, vv, rq, hh);
;         { float s_ = S[15] + O[15]; asm volatile("v_mov_b32 %0, %0" : "+v"(s_)); asm volatile("" :: "v"(s_)); }
	s_waitcnt lgkmcnt(5)
	v_mul_f32_e32 v13, v37, v13
	v_mul_f32_e32 v12, v36, v12
	v_mul_f32_e32 v15, v39, v15
	v_mul_f32_e32 v14, v38, v14
	s_waitcnt lgkmcnt(4)
	v_mul_f32_e32 v17, v41, v17
	v_mul_f32_e32 v16, v40, v16
	v_mul_f32_e32 v19, v43, v19
	v_mul_f32_e32 v18, v42, v18
	s_waitcnt lgkmcnt(1)
	v_mul_f32_e32 v93, v45, v93
	v_mul_f32_e32 v92, v44, v92
	v_mul_f32_e32 v95, v47, v95
	v_mul_f32_e32 v94, v46, v94
	s_waitcnt lgkmcnt(0)
	v_mul_f32_e32 v97, v49, v97
	v_mul_f32_e32 v96, v48, v96
	v_mul_f32_e32 v99, v51, v99
	v_mul_f32_e32 v98, v50, v98
	v_cvt_pk_bf16_f32 v226, v12, v13
	v_cvt_pk_bf16_f32 v227, v14, v15
	v_cvt_pk_bf16_f32 v228, v16, v17
	v_cvt_pk_bf16_f32 v229, v18, v19
	v_mul_f32_e32 v19, v51, v91
	v_mul_f32_e32 v18, v50, v90
	v_mul_f32_e32 v15, v47, v87
	v_mul_f32_e32 v14, v46, v86
	v_mul_f32_e32 v11, v43, v11
	v_mul_f32_e32 v10, v42, v10
	v_mul_f32_e32 v7, v39, v7
	v_mul_f32_e32 v6, v38, v6
	v_mul_f32_e32 v17, v49, v89
	v_mul_f32_e32 v16, v48, v88
	v_mul_f32_e32 v13, v45, v85
	v_mul_f32_e32 v12, v44, v84
	v_mul_f32_e32 v9, v41, v9
	v_mul_f32_e32 v8, v40, v8
	v_mul_f32_e32 v5, v37, v5
	v_mul_f32_e32 v4, v36, v4
	v_cvt_pk_bf16_f32 v230, v92, v93
	v_cvt_pk_bf16_f32 v231, v94, v95
	v_cvt_pk_bf16_f32 v232, v96, v97
	v_cvt_pk_bf16_f32 v233, v98, v99
	v_mfma_f32_32x32x16_bf16 v[84:99], v[194:197], v[198:201], 0
	v_mfma_f32_32x32x16_bf16 v[84:99], v[206:209], v[210:213], v[84:99]
	s_nop 11
	v_cndmask_b32_e64 v2, v84, 0, vcc
	v_cndmask_b32_e64 v84, 0, v85, s[4:5]
	v_cndmask_b32_e64 v85, v86, 0, s[6:7]
	v_cndmask_b32_e64 v86, v87, 0, s[8:9]
	v_cndmask_b32_e64 v87, v88, 0, s[10:11]
	v_cndmask_b32_e64 v88, v89, 0, s[12:13]
	v_cndmask_b32_e64 v89, v90, 0, s[14:15]
	v_cndmask_b32_e64 v90, v91, 0, s[16:17]
	v_cndmask_b32_e64 v91, v92, 0, s[18:19]
	v_cndmask_b32_e64 v92, v93, 0, s[20:21]
	v_cndmask_b32_e64 v93, v94, 0, s[22:23]
	v_cndmask_b32_e64 v94, v95, 0, s[24:25]
	v_cndmask_b32_e64 v95, v96, 0, s[26:27]
	v_cndmask_b32_e64 v96, v97, 0, s[28:29]
	v_cndmask_b32_e64 v97, v98, 0, s[30:31]
	v_cndmask_b32_e64 v98, v99, 0, s[34:35]
	v_cvt_pk_bf16_f32 v234, v2, v84
	v_cvt_pk_bf16_f32 v235, v85, v86
	v_cvt_pk_bf16_f32 v236, v87, v88
	v_cvt_pk_bf16_f32 v237, v89, v90
	v_cvt_pk_bf16_f32 v238, v91, v92
	v_cvt_pk_bf16_f32 v239, v93, v94
	v_cvt_pk_bf16_f32 v240, v95, v96
	v_cvt_pk_bf16_f32 v241, v97, v98
	v_mfma_f32_32x32x16_bf16 v[84:99], v[234:237], v[100:103], 0
	v_mfma_f32_32x32x16_bf16 v[84:99], v[202:205], v[226:229], v[84:99]
	v_mfma_f32_32x32x16_bf16 v[4:19], v[214:217], v[108:111], v[4:19]
	v_mfma_f32_32x32x16_bf16 v[84:99], v[238:241], v[104:107], v[84:99]
	v_mfma_f32_32x32x16_bf16 v[4:19], v[218:221], v[112:115], v[4:19]
	v_mfma_f32_32x32x16_bf16 v[84:99], v[222:225], v[230:233], v[84:99]
	s_nop 11
	v_add_f32_e32 v2, v99, v19
	v_mov_b32 v2, v2
	s_nop 0
	v_add_f32_e32 v2, v83, v99
	v_add_f32_e32 v82, v82, v98
	v_add_f32_e32 v81, v81, v97
	v_add_f32_e32 v80, v80, v96
	v_add_f32_e32 v79, v79, v95
	v_add_f32_e32 v78, v78, v94
	v_add_f32_e32 v77, v77, v93
	v_add_f32_e32 v76, v76, v92
	v_add_f32_e32 v75, v75, v91
	v_add_f32_e32 v74, v74, v90
	v_add_f32_e32 v73, v73, v89
	v_add_f32_e32 v72, v72, v88
	v_add_f32_e32 v71, v71, v87
	v_add_f32_e32 v70, v70, v86
	v_add_f32_e32 v69, v69, v85
	v_add_f32_e32 v68, v68, v84
	v_add_u32_e32 v83, 0x16800, v242
	ds_write2st64_b32 v83, v68, v69 offset1:1
	ds_write2st64_b32 v83, v70, v71 offset0:2 offset1:3
	ds_write2st64_b32 v83, v72, v73 offset0:8 offset1:9
	ds_write2st64_b32 v83, v74, v75 offset0:10 offset1:11
	ds_write2st64_b32 v83, v76, v77 offset0:16 offset1:17
	ds_write2st64_b32 v83, v78, v79 offset0:18 offset1:19
	ds_write2st64_b32 v83, v80, v81 offset0:24 offset1:25
	ds_write2st64_b32 v83, v82, v2 offset0:26 offset1:27
	s_mov_b64 s[4:5], 0
.LBB0_414:
	s_andn2_b64 vcc, exec, s[4:5]
	s_cbranch_vccnz .LBB0_420
	v_mov_b32_e32 v4, v0
	s_load_dwordx2 s[4:5], s[40:41], 0x98
	v_lshlrev_b32_e32 v2, 9, v4
	v_and_b32_e32 v6, 63, v4
	v_and_b32_e32 v5, 0x18000, v2
	v_lshl_or_b32 v2, v6, 2, v5
	s_waitcnt lgkmcnt(0)
	v_lshl_add_u64 v[8:9], s[4:5], 0, v[2:3]
	v_lshl_add_u64 v[8:9], v[8:9], 0, s[54:55]
	v_lshl_add_u64 v[12:13], v[8:9], 0, s[56:57]
	v_add_co_u32_e32 v8, vcc, 0xa260000, v12
	v_lshl_or_b32 v2, v6, 1, v5
	s_nop 0
	v_addc_co_u32_e32 v9, vcc, 0, v13, vcc
	v_lshl_add_u64 v[14:15], s[4:5], 0, v[2:3]
	v_add_co_u32_e32 v10, vcc, 0xe260000, v12
	v_lshl_add_u64 v[14:15], v[14:15], 0, v[116:117]
	s_nop 0
	v_addc_co_u32_e32 v11, vcc, 0, v13, vcc
	v_lshl_add_u64 v[14:15], v[14:15], 0, s[56:57]
	v_add_co_u32_e32 v16, vcc, 0x12260000, v14
	s_cmp_eq_u32 s56, 0
	s_nop 0
	v_addc_co_u32_e32 v17, vcc, 0, v15, vcc
	v_add_co_u32_e32 v18, vcc, 0xa261000, v12
	s_nop 1
	v_addc_co_u32_e32 v19, vcc, 0, v13, vcc
	v_add_co_u32_e32 v20, vcc, 0xe261000, v12
	s_nop 1
	v_addc_co_u32_e32 v21, vcc, 0, v13, vcc
	v_add_co_u32_e32 v22, vcc, 0x12261000, v14
	s_nop 1
	v_addc_co_u32_e32 v23, vcc, 0, v15, vcc
	v_add_co_u32_e32 v24, vcc, 0xa262000, v12
	s_nop 1
	v_addc_co_u32_e32 v25, vcc, 0, v13, vcc
	v_add_co_u32_e32 v26, vcc, 0xe262000, v12
	s_nop 1
	v_addc_co_u32_e32 v27, vcc, 0, v13, vcc
	global_load_dword v142, v[8:9], off
	global_load_dword v121, v[10:11], off
	global_load_ushort v7, v[16:17], off
	global_load_dword v124, v[18:19], off
	global_load_dword v122, v[20:21], off
	s_nop 0
	global_load_ushort v8, v[22:23], off
	global_load_dword v123, v[24:25], off
	global_load_dword v133, v[26:27], off
	v_add_co_u32_e32 v10, vcc, 0x12262000, v14
	s_nop 1
	v_addc_co_u32_e32 v11, vcc, 0, v15, vcc
	v_add_co_u32_e32 v16, vcc, 0xa263000, v12
	s_nop 1
	v_addc_co_u32_e32 v17, vcc, 0, v13, vcc
	v_add_co_u32_e32 v18, vcc, 0xe263000, v12
	s_nop 1
; #define LAS __attribute__((address_space(3)))
; DI unsigned pk2(float lo, float hi) { return cvtpk_s(lo, hi); }
; template <int SET> DI void h_prep8(const unsigned (&CR)[72], LAS unsigned char* buf, int tgp, int k2, int v64) {
;     float base0 = 0.f, base1 = 0.f, bm0 = 0.f, bm1 = 0.f, bl0 = 0.f, bl1 = 0.f;
; #pragma unroll
;     for (int g = 0; g < 4; ++g) { const f32x2_t tt = *(const LAS f32x2_t*)(buf + H_TOT + (g * 128 + 2 * k2) * 4);
;         if (g < tgp) { base0 += tt[0]; base1 += tt[1]; } if (g < 2) { bm0 += tt[0]; bm1 += tt[1]; } bl0 += tt[0]; bl1 += tt[1]; }
;     const float ebm0 = __expf(bm0), ebm1 = __expf(bm1), elm0 = __expf(bl0 - bm0), elm1 = __expf(bl1 - bm1);
;     float e20 = __expf(base0 - bm0), e21 = __expf(base1 - bm1); unsigned kup0[4], kup1[4];
; #pragma unroll
;     for (int jp = 0; jp < 4; ++jp) {
;         float ku0[2], ku1[2];
; #pragma unroll
;         for (int jj = 0; jj < 2; ++jj) {
;             const int j = 2 * jp + jj;
;             const unsigned fw = CR[24 * SET + 8 + j], qw = CR[24 * SET + j];
;             const float f0 = __expf(bflo(fw)), f1 = __expf(bfhi(fw)), q0 = bflo(qw), q1 = bfhi(qw);
;             e20 *= f0; e21 *= f1;
;             const float e30 = __builtin_amdgcn_rcpf(e20), e31 = __builtin_amdgcn_rcpf(e21);
;             const float kk0 = 1.0f - f0, kk1 = 1.0f - f1;
; DI void h_reduce_store2(LAS unsigned char* red, bf16_t* op, int c, int pt) {
; #pragma unroll
;     for (int s2 = 0; s2 < 2; ++s2) {
;         const int s = pt + 256 * s2, t = s >> 4, c4 = s & 15;
;         const f32x4 a = *(const LAS f32x4*)(red + ((0 * 32 + t) * 64 + 4 * c4) * 4), b2 = *(const LAS f32x4*)(red + ((1 * 32 + t) * 64 + 4 * c4) * 4);
;         const f32x4 sm = a + b2;
;         u32x2 w; w.x = pk2(sm[0], sm[1]); w.y = pk2(sm[2], sm[3]);
;         *(u32x2*)(op + (size_t)(32 * c + t) * D + 4 * c4) = w;
;     }
; }
	v_addc_co_u32_e32 v19, vcc, 0, v13, vcc
	v_add_co_u32_e32 v20, vcc, 0x12263000, v14
	s_nop 1
	v_addc_co_u32_e32 v21, vcc, 0, v15, vcc
	v_add_co_u32_e32 v22, vcc, 0xa264000, v12
	s_nop 1
	v_addc_co_u32_e32 v23, vcc, 0, v13, vcc
	v_add_co_u32_e32 v24, vcc, 0xe264000, v12
	s_nop 1
	v_addc_co_u32_e32 v25, vcc, 0, v13, vcc
	v_add_co_u32_e32 v26, vcc, 0x12264000, v14
	s_nop 1
	v_addc_co_u32_e32 v27, vcc, 0, v15, vcc
	v_add_co_u32_e32 v28, vcc, 0xa265000, v12
	s_nop 1
	v_addc_co_u32_e32 v29, vcc, 0, v13, vcc
	global_load_ushort v9, v[10:11], off
	global_load_dword v143, v[16:17], off
	global_load_dword v144, v[18:19], off
	s_nop 0
	global_load_ushort v10, v[20:21], off
	global_load_dword v145, v[22:23], off
	global_load_dword v150, v[24:25], off
	global_load_ushort v11, v[26:27], off
	global_load_dword v159, v[28:29], off
	v_add_co_u32_e32 v16, vcc, 0xe265000, v12
	s_nop 1
	v_addc_co_u32_e32 v17, vcc, 0, v13, vcc
	v_add_co_u32_e32 v18, vcc, 0x12265000, v14
	s_nop 1
	v_addc_co_u32_e32 v19, vcc, 0, v15, vcc
	v_add_co_u32_e32 v20, vcc, 0xa266000, v12
	s_nop 1
	v_addc_co_u32_e32 v21, vcc, 0, v13, vcc
	v_add_co_u32_e32 v22, vcc, 0xe266000, v12
	s_nop 1
	v_addc_co_u32_e32 v23, vcc, 0, v13, vcc
	v_add_co_u32_e32 v24, vcc, 0x12266000, v14
	s_nop 1
	v_addc_co_u32_e32 v25, vcc, 0, v15, vcc
	v_add_co_u32_e32 v26, vcc, 0xa267000, v12
	s_nop 1
	v_addc_co_u32_e32 v27, vcc, 0, v13, vcc
	v_add_co_u32_e32 v28, vcc, 0xe267000, v12
	s_nop 1
	v_addc_co_u32_e32 v29, vcc, 0, v13, vcc
	v_add_co_u32_e32 v14, vcc, 0x12267000, v14
	s_nop 1
	v_addc_co_u32_e32 v15, vcc, 0, v15, vcc
	global_load_dword v164, v[16:17], off
	global_load_ushort v12, v[18:19], off
	global_load_dword v184, v[20:21], off
	global_load_dword v171, v[22:23], off
	global_load_ushort v13, v[24:25], off
	global_load_dword v177, v[26:27], off
	global_load_dword v174, v[28:29], off
	s_nop 0
	global_load_ushort v14, v[14:15], off
	s_cbranch_scc1 .LBB0_417
	s_and_b32 s6, s38, 0x4000
	s_add_i32 s6, s6, 0
	s_add_i32 s8, s6, 0x16800
	s_lshl_b64 s[6:7], s[52:53], 1
	s_add_u32 s4, s4, s6
	s_addc_u32 s5, s5, s7
	s_lshl_b32 s6, s96, 1
	v_lshlrev_b32_sdwa v2, v1, v4 dst_sel:DWORD dst_unused:UNUSED_PAD src0_sel:DWORD src1_sel:BYTE_0
	s_add_u32 s4, s4, s6
	v_and_b32_e32 v2, 60, v2
	v_lshrrev_b32_sdwa v15, v118, v4 dst_sel:DWORD dst_unused:UNUSED_PAD src0_sel:DWORD src1_sel:BYTE_0
	s_addc_u32 s5, s5, 0
	s_lshl_b32 s6, s48, 1
	v_lshlrev_b32_e32 v5, 2, v2
	v_lshlrev_b32_e32 v16, 8, v15
	s_add_u32 s4, s4, s6
	v_add3_u32 v5, s8, v5, v16
	s_addc_u32 s5, s5, 0
	v_lshlrev_b32_e32 v2, 1, v2
	ds_read_b128 v[16:19], v5
	ds_read_b128 v[20:23], v5 offset:8192
	v_lshl_add_u64 v[24:25], s[4:5], 0, v[2:3]
	v_lshl_add_u64 v[32:33], v[24:25], 0, s[50:51]
	ds_read_b128 v[24:27], v5 offset:4096
	ds_read_b128 v[28:31], v5 offset:12288
	v_lshl_add_u32 v2, v15, 11, s97
	s_waitcnt lgkmcnt(2)
	v_add_f32_e32 v19, v19, v23
	v_add_f32_e32 v18, v18, v22
	v_add_f32_e32 v17, v17, v21
	v_add_f32_e32 v16, v16, v20
	s_nop 0
	v_cvt_pk_bf16_f32 v16, v16, v17
	v_cvt_pk_bf16_f32 v17, v18, v19
	v_lshl_add_u64 v[18:19], v[2:3], 1, v[32:33]
	global_store_dwordx2 v[18:19], v[16:17], off
	s_waitcnt lgkmcnt(0)
	v_add_f32_e32 v17, v27, v31
	v_add_f32_e32 v16, v26, v30
	v_add_f32_e32 v19, v25, v29
	v_add_f32_e32 v18, v24, v28
	v_add_u32_e32 v2, 0x8000, v2
	v_cvt_pk_bf16_f32 v18, v18, v19
	v_cvt_pk_bf16_f32 v19, v16, v17
	v_lshl_add_u64 v[16:17], v[2:3], 1, v[32:33]
	global_store_dwordx2 v[16:17], v[18:19], off
.LBB0_417:
	s_andn2_b32 s4, 1, s39
	s_mul_i32 s4, s4, 0xb400
	s_add_i32 s8, s4, 0
	v_lshlrev_b32_e32 v15, 3, v6
	v_add_u32_e32 v17, s8, v15
	ds_read2st64_b64 v[18:21], v17 offset0:82 offset1:83
	ds_read2st64_b64 v[22:25], v17 offset0:84 offset1:85
	v_cmp_lt_u32_sdwa s[4:5], v4, v120 src0_sel:BYTE_0 src1_sel:DWORD
	v_cmp_gt_u32_sdwa vcc, v4, s88 src0_sel:BYTE_0 src1_sel:DWORD
	v_lshrrev_b32_sdwa v16, v119, v4 dst_sel:DWORD dst_unused:UNUSED_PAD src0_sel:DWORD src1_sel:BYTE_0
	s_waitcnt lgkmcnt(1)
	v_add_f32_e32 v2, 0, v18
	v_add_f32_e32 v5, 0, v19
	v_cndmask_b32_e64 v19, v2, 0, s[4:5]
	v_cndmask_b32_e64 v18, v5, 0, s[4:5]
	v_add_f32_e32 v26, v20, v19
	v_add_f32_e32 v27, v21, v18
	v_cndmask_b32_e32 v19, v19, v26, vcc
	v_cndmask_b32_e32 v4, v18, v27, vcc
	v_add_f32_e32 v18, v2, v20
	s_waitcnt lgkmcnt(0)
	v_add_f32_e32 v2, v22, v19
	v_cmp_eq_u32_e32 vcc, 3, v16
	v_add_f32_e32 v5, v5, v21
	v_add_f32_e32 v20, v23, v4
	v_cndmask_b32_e32 v19, v19, v2, vcc
	v_add_f32_e32 v2, v18, v22
	v_add_f32_e32 v2, v2, v24
	v_cndmask_b32_e32 v21, v4, v20, vcc
	v_add_f32_e32 v4, v5, v23
	v_sub_f32_e32 v2, v2, v18
	v_sub_f32_e32 v19, v19, v18
	v_add_f32_e32 v20, v4, v25
	v_mul_f32_e32 v2, 0x3fb8aa3b, v2
	v_mul_f32_e32 v19, 0x3fb8aa3b, v19
	v_exp_f32_e32 v4, v2
	v_sub_f32_e32 v2, v20, v5
	v_exp_f32_e32 v20, v19
	v_sub_f32_e32 v19, v21, v5
	v_mul_f32_e32 v19, 0x3fb8aa3b, v19
	v_exp_f32_e32 v21, v19
	s_waitcnt vmcnt(62)
; template <int SET> DI void h_prep8(const unsigned (&CR)[72], LAS unsigned char* buf, int tgp, int k2, int v64) {
;     float base0 = 0.f, base1 = 0.f, bm0 = 0.f, bm1 = 0.f, bl0 = 0.f, bl1 = 0.f;
; #pragma unroll
;     for (int g = 0; g < 4; ++g) { const f32x2_t tt = *(const LAS f32x2_t*)(buf + H_TOT + (g * 128 + 2 * k2) * 4);
;         if (g < tgp) { base0 += tt[0]; base1 += tt[1]; } if (g < 2) { bm0 += tt[0]; bm1 += tt[1]; } bl0 += tt[0]; bl1 += tt[1]; }
;     const float ebm0 = __expf(bm0), ebm1 = __expf(bm1), elm0 = __expf(bl0 - bm0), elm1 = __expf(bl1 - bm1);
;     float e20 = __expf(base0 - bm0), e21 = __expf(base1 - bm1); unsigned kup0[4], kup1[4];
; #pragma unroll
;     for (int jp = 0; jp < 4; ++jp) {
;         float ku0[2], ku1[2];
; #pragma unroll
;         for (int jj = 0; jj < 2; ++jj) {
;             const int j = 2 * jp + jj;
;             const unsigned fw = CR[24 * SET + 8 + j], qw = CR[24 * SET + j];
;             const float f0 = __expf(bflo(fw)), f1 = __expf(bfhi(fw)), q0 = bflo(qw), q1 = bfhi(qw);
;             e20 *= f0; e21 *= f1;
;             const float e30 = __builtin_amdgcn_rcpf(e20), e31 = __builtin_amdgcn_rcpf(e21);
;             const float kk0 = 1.0f - f0, kk1 = 1.0f - f1;
;             const int t = 8 * tgp + j;
;             *(LAS unsigned*)(buf + H_QS + t * 272 + 4 * k2) = pk2(q0 * e20, q1 * e21);
;             *(LAS unsigned*)(buf + H_KS + t * 272 + 4 * k2) = pk2(kk0 * e30, kk1 * e31);
;             ku0[jj] = kk0 * e30 * elm0; ku1[jj] = kk1 * e31 * elm1;
;         }
;         kup0[jp] = pk2(ku0[0], ku0[1]); kup1[jp] = pk2(ku1[0], ku1[1]);
;     }
;     { u32x4 w; w.x = kup0[0]; w.y = kup0[1]; w.z = kup0[2]; w.w = kup0[3]; *(LAS u32x4*)(buf + H_KU + (2 * k2) * 80 + 16 * tgp) = w;
;       w.x = kup1[0]; w.y = kup1[1]; w.z = kup1[2]; w.w = kup1[3]; *(LAS u32x4*)(buf + H_KU + (2 * k2 + 1) * 80 + 16 * tgp) = w; }
;     if (tgp == 0) { *(LAS f32x2_t*)(buf + H_DEC + 8 * k2) = (f32x2_t){ebm0 * elm0, ebm1 * elm1}; *(LAS f32x2_t*)(buf + H_EBM + 8 * k2) = (f32x2_t){ebm0, ebm1}; }
;     { u32x4 w; w.x = (CR[24 * SET + 16] & 0xffffu) | (CR[24 * SET + 17] << 16); w.y = (CR[24 * SET + 18] & 0xffffu) | (CR[24 * SET + 19] << 16);
;       w.z = (CR[24 * SET + 20] & 0xffffu) | (CR[24 * SET + 21] << 16); w.w = (CR[24 * SET + 22] & 0xffffu) | (CR[24 * SET + 23] << 16);
;       *(LAS u32x4*)(buf + H_VT + v64 * 80 + 16 * tgp) = w; }
; }
	v_lshlrev_b32_e32 v19, 16, v130
	v_mul_f32_e32 v19, 0x3fb8aa3b, v19
	v_exp_f32_e32 v22, v19
	v_and_b32_e32 v19, 0xffff0000, v130
	v_mul_f32_e32 v19, 0x3fb8aa3b, v19
	v_exp_f32_e32 v23, v19
	v_lshlrev_b32_e32 v24, 16, v137
	v_and_b32_e32 v25, 0xffff0000, v137
	v_lshlrev_b32_e32 v19, 2, v6
	v_mul_f32_e32 v21, v23, v21
	v_mul_f32_e32 v20, v22, v20
	v_mul_f32_e32 v2, 0x3fb8aa3b, v2
	v_mul_f32_e32 v25, v21, v25
	v_mul_f32_e32 v24, v20, v24
	v_rcp_f32_e32 v26, v20
	v_cvt_pk_bf16_f32 v30, v24, v25
	v_mul_u32_u24_e32 v24, 0x880, v16
	v_add3_u32 v19, s8, v19, v24
	v_lshlrev_b32_e32 v24, 16, v132
	v_and_b32_e32 v25, 0xffff0000, v132
	v_mul_f32_e32 v24, 0x3fb8aa3b, v24
	v_mul_f32_e32 v25, 0x3fb8aa3b, v25
	v_exp_f32_e32 v24, v24
	v_exp_f32_e32 v25, v25
	v_rcp_f32_e32 v27, v21
	v_exp_f32_e32 v2, v2
	v_sub_f32_e32 v23, 1.0, v23
	v_sub_f32_e32 v22, 1.0, v22
	v_mul_f32_e32 v29, v25, v21
	v_mul_f32_e32 v28, v24, v20
	v_sub_f32_e32 v25, 1.0, v25
	v_sub_f32_e32 v24, 1.0, v24
	v_rcp_f32_e32 v20, v28
	v_rcp_f32_e32 v21, v29
	v_mul_f32_e32 v23, v23, v27
	v_mul_f32_e32 v22, v22, v26
	v_lshlrev_b32_e32 v26, 16, v139
	v_cvt_pk_bf16_f32 v31, v22, v23
	v_mul_f32_e32 v21, v25, v21
	v_mul_f32_e32 v20, v24, v20
	v_and_b32_e32 v27, 0xffff0000, v139
	v_cvt_pk_bf16_f32 v24, v20, v21
	v_add_u32_e32 v34, 0x4400, v19
	v_mov_b32_e32 v25, v20
	v_mov_b32_e32 v20, v23
	v_mul_f32_e32 v27, v29, v27
	v_mul_f32_e32 v26, v28, v26
	ds_write2_b32 v34, v31, v24 offset1:68
	v_mov_b32_e32 v24, v22
	v_mul_f32_e32 v23, v2, v21
	v_mul_f32_e32 v22, v2, v20
	s_waitcnt vmcnt(57)
	v_lshlrev_b32_e32 v21, 16, v141
	v_cvt_pk_bf16_f32 v26, v26, v27
	v_add_u32_e32 v27, 0x2000, v19
	v_mul_f32_e32 v21, 0x3fb8aa3b, v21
	ds_write2_b32 v27, v30, v26 offset0:128 offset1:196
	v_exp_f32_e32 v26, v21
	v_and_b32_e32 v21, 0xffff0000, v141
	v_mul_f32_e32 v21, 0x3fb8aa3b, v21
	v_exp_f32_e32 v27, v21
	v_mul_f32_e32 v25, v4, v25
	v_mul_f32_e32 v24, v4, v24
	v_cvt_pk_bf16_f32 v20, v24, v25
	v_cvt_pk_bf16_f32 v24, v22, v23
	v_lshlrev_b32_e32 v22, 16, v136
	v_and_b32_e32 v23, 0xffff0000, v136
	v_mul_f32_e32 v29, v27, v29
	v_mul_f32_e32 v28, v26, v28
	s_waitcnt vmcnt(56)
	v_lshlrev_b32_e32 v25, 16, v158
	v_mul_f32_e32 v23, v29, v23
	v_mul_f32_e32 v22, v28, v22
	v_mul_f32_e32 v25, 0x3fb8aa3b, v25
	v_cvt_pk_bf16_f32 v21, v22, v23
	v_sub_f32_e32 v23, 1.0, v27
	v_sub_f32_e32 v22, 1.0, v26
	v_exp_f32_e32 v26, v25
	v_and_b32_e32 v25, 0xffff0000, v158
	v_mul_f32_e32 v25, 0x3fb8aa3b, v25
	v_exp_f32_e32 v27, v25
	v_rcp_f32_e32 v30, v28
	v_rcp_f32_e32 v31, v29
	v_add_u32_e32 v35, 0x2400, v19
	v_mul_f32_e32 v29, v27, v29
	v_mul_f32_e32 v28, v26, v28
	v_sub_f32_e32 v27, 1.0, v27
	v_sub_f32_e32 v26, 1.0, v26
	v_rcp_f32_e32 v32, v28
	v_rcp_f32_e32 v33, v29
	v_mul_f32_e32 v23, v23, v31
	v_mul_f32_e32 v22, v22, v30
	v_lshlrev_b32_e32 v30, 16, v152
	v_and_b32_e32 v31, 0xffff0000, v152
	v_mul_f32_e32 v31, v29, v31
	v_mul_f32_e32 v30, v28, v30
	v_mul_f32_e32 v27, v27, v33
	v_mul_f32_e32 v26, v26, v32
	v_cvt_pk_bf16_f32 v30, v30, v31
	v_cvt_pk_bf16_f32 v25, v22, v23
	ds_write2_b32 v35, v21, v30 offset0:8 offset1:76
	v_cvt_pk_bf16_f32 v21, v26, v27
	ds_write2_b32 v34, v25, v21 offset0:136 offset1:204
	v_lshlrev_b32_e32 v25, 16, v156
	v_mov_b32_e32 v31, v26
	v_mov_b32_e32 v26, v23
	v_mul_f32_e32 v25, 0x3fb8aa3b, v25
	v_mov_b32_e32 v30, v22
	v_mul_f32_e32 v23, v2, v27
	v_mul_f32_e32 v22, v2, v26
	v_exp_f32_e32 v26, v25
	v_and_b32_e32 v25, 0xffff0000, v156
	v_mul_f32_e32 v25, 0x3fb8aa3b, v25
	v_exp_f32_e32 v27, v25
	v_cvt_pk_bf16_f32 v25, v22, v23
	v_lshlrev_b32_e32 v22, 16, v161
	v_and_b32_e32 v23, 0xffff0000, v161
	v_mul_f32_e32 v29, v27, v29
	v_mul_f32_e32 v28, v26, v28
	v_mul_f32_e32 v31, v4, v31
	v_mul_f32_e32 v30, v4, v30
	v_mul_f32_e32 v23, v29, v23
	v_mul_f32_e32 v22, v28, v22
	v_cvt_pk_bf16_f32 v21, v30, v31
	v_cvt_pk_bf16_f32 v34, v22, v23
	v_sub_f32_e32 v23, 1.0, v27
	v_sub_f32_e32 v22, 1.0, v26
	v_lshlrev_b32_e32 v26, 16, v168
	v_and_b32_e32 v27, 0xffff0000, v168
	v_mul_f32_e32 v26, 0x3fb8aa3b, v26
	v_mul_f32_e32 v27, 0x3fb8aa3b, v27
	v_exp_f32_e32 v26, v26
	v_exp_f32_e32 v27, v27
	v_rcp_f32_e32 v30, v28
	v_rcp_f32_e32 v31, v29
	v_add_u32_e32 v70, 0x4800, v19
	v_mul_f32_e32 v29, v27, v29
	v_mul_f32_e32 v28, v26, v28
	v_sub_f32_e32 v27, 1.0, v27
	v_sub_f32_e32 v26, 1.0, v26
	v_rcp_f32_e32 v32, v28
	v_rcp_f32_e32 v33, v29
	v_mul_f32_e32 v23, v23, v31
	v_mul_f32_e32 v22, v22, v30
	v_lshlrev_b32_e32 v30, 16, v163
	v_and_b32_e32 v31, 0xffff0000, v163
	v_mul_f32_e32 v31, v29, v31
	v_mul_f32_e32 v30, v28, v30
	v_mul_f32_e32 v27, v27, v33
	v_mul_f32_e32 v26, v26, v32
	v_cvt_pk_bf16_f32 v30, v30, v31
	v_cvt_pk_bf16_f32 v68, v22, v23
	ds_write2_b32 v35, v34, v30 offset0:144 offset1:212
	v_cvt_pk_bf16_f32 v30, v26, v27
	ds_write2_b32 v70, v68, v30 offset0:16 offset1:84
	v_mov_b32_e32 v30, v22
	v_mov_b32_e32 v31, v26
	v_mov_b32_e32 v26, v23
	s_waitcnt vmcnt(51)
	v_lshlrev_b32_e32 v23, 16, v173
	v_mul_f32_e32 v31, v4, v31
	v_mul_f32_e32 v30, v4, v30
	v_mul_f32_e32 v23, 0x3fb8aa3b, v23
	v_cvt_pk_bf16_f32 v22, v30, v31
	v_exp_f32_e32 v30, v23
	v_and_b32_e32 v23, 0xffff0000, v173
	v_mul_f32_e32 v23, 0x3fb8aa3b, v23
	v_exp_f32_e32 v31, v23
	v_mul_f32_e32 v27, v2, v27
	v_mul_f32_e32 v26, v2, v26
	v_cvt_pk_bf16_f32 v26, v26, v27
	s_waitcnt vmcnt(49)
	v_lshlrev_b32_e32 v32, 16, v179
	v_and_b32_e32 v33, 0xffff0000, v179
	v_mul_f32_e32 v29, v31, v29
	v_mul_f32_e32 v28, v30, v28
	v_lshlrev_b32_e32 v27, 16, v176
	v_mul_f32_e32 v33, v29, v33
	v_mul_f32_e32 v32, v28, v32
	v_mul_f32_e32 v27, 0x3fb8aa3b, v27
	v_cvt_pk_bf16_f32 v23, v32, v33
	v_exp_f32_e32 v32, v27
	v_and_b32_e32 v27, 0xffff0000, v176
	v_mul_f32_e32 v27, 0x3fb8aa3b, v27
	v_exp_f32_e32 v33, v27
	v_rcp_f32_e32 v34, v28
	v_rcp_f32_e32 v35, v29
	v_sub_f32_e32 v31, 1.0, v31
	v_sub_f32_e32 v30, 1.0, v30
	v_mul_f32_e32 v29, v33, v29
	v_mul_f32_e32 v28, v32, v28
	v_add_u32_e32 v19, 0x2800, v19
	v_mul_f32_e32 v31, v31, v35
	v_mul_f32_e32 v30, v30, v34
	s_waitcnt vmcnt(48)
	v_lshlrev_b32_e32 v34, 16, v183
	v_and_b32_e32 v35, 0xffff0000, v183
	v_rcp_f32_e32 v68, v28
	v_rcp_f32_e32 v69, v29
	v_mul_f32_e32 v29, v29, v35
	v_mul_f32_e32 v28, v28, v34
	v_cvt_pk_bf16_f32 v27, v30, v31
	v_cvt_pk_bf16_f32 v28, v28, v29
	ds_write2_b32 v19, v23, v28 offset0:24 offset1:92
	v_sub_f32_e32 v29, 1.0, v33
	v_sub_f32_e32 v28, 1.0, v32
	v_mov_b32_e32 v32, v30
	v_mul_f32_e32 v29, v29, v69
	v_mul_f32_e32 v28, v28, v68
	s_nop 0
	v_cvt_pk_bf16_f32 v19, v28, v29
	v_mov_b32_e32 v33, v28
	v_mov_b32_e32 v28, v31
	v_mul_f32_e32 v29, v2, v29
	v_mul_f32_e32 v28, v2, v28
	ds_write2_b32 v70, v27, v19 offset0:152 offset1:220
	v_mul_f32_e32 v33, v4, v33
	v_mul_f32_e32 v32, v4, v32
	v_cvt_pk_bf16_f32 v27, v28, v29
	v_mul_u32_u24_e32 v28, 0xa0, v6
	v_lshlrev_b32_e32 v19, 4, v16
	v_cvt_pk_bf16_f32 v23, v32, v33
	v_add3_u32 v28, s8, v28, v19
	ds_write_b128 v28, v[20:23] offset:26112
	ds_write_b128 v28, v[24:27] offset:26192
	s_and_saveexec_b64 s[6:7], s[4:5]
	s_cbranch_execz .LBB0_419
; #define LAS __attribute__((address_space(3)))
; template <int SET> DI void h_totals8(const unsigned (&CR)[72], LAS unsigned char* buf, int tgp, int k2) {
;     float lo = 0.f, hi = 0.f;
; #pragma unroll
;     for (int j = 0; j < 8; ++j) { lo += bflo(CR[24 * SET + 8 + j]); hi += bfhi(CR[24 * SET + 8 + j]); }
;     *(LAS f32x2_t*)(buf + H_TOT + (tgp * 128 + 2 * k2) * 4) = (f32x2_t){lo, hi};
; }
; template <int SET> DI void h_prep8(const unsigned (&CR)[72], LAS unsigned char* buf, int tgp, int k2, int v64) {
;     ...
;     if (tgp == 0) { *(LAS f32x2_t*)(buf + H_DEC + 8 * k2) = (f32x2_t){ebm0 * elm0, ebm1 * elm1}; *(LAS f32x2_t*)(buf + H_EBM + 8 * k2) = (f32x2_t){ebm0, ebm1}; }
;     { u32x4 w; w.x = (CR[24 * SET + 16] & 0xffffu) | (CR[24 * SET + 17] << 16); w.y = (CR[24 * SET + 18] & 0xffffu) | (CR[24 * SET + 19] << 16);
;       w.z = (CR[24 * SET + 20] & 0xffffu) | (CR[24 * SET + 21] << 16); w.w = (CR[24 * SET + 22] & 0xffffu) | (CR[24 * SET + 23] << 16);
;       *(LAS u32x4*)(buf + H_VT + v64 * 80 + 16 * tgp) = w; }
	v_mul_f32_e32 v18, 0x3fb8aa3b, v18
	v_mul_f32_e32 v5, 0x3fb8aa3b, v5
	v_exp_f32_e32 v20, v18
	v_exp_f32_e32 v21, v5
	v_mov_b32_e32 v5, v2
	v_mul_f32_e32 v5, v21, v5
	v_mul_f32_e32 v4, v20, v4
	ds_write2st64_b64 v17, v[4:5], v[20:21] offset0:81 offset1:86
.LBB0_419:
	s_or_b64 exec, exec, s[6:7]
	v_mul_u32_u24_e32 v2, 0x50, v6
	s_waitcnt vmcnt(43)
	v_lshlrev_b32_e32 v4, 16, v129
	v_and_b32_e32 v5, 0xffff0000, v129
	s_waitcnt vmcnt(21)
	v_and_b32_e32 v189, 0xffff, v7
	s_waitcnt vmcnt(18)
	v_and_b32_e32 v185, 0xffff, v8
	s_waitcnt vmcnt(15)
	v_and_b32_e32 v188, 0xffff, v9
	s_waitcnt vmcnt(12)
	v_and_b32_e32 v186, 0xffff, v10
	s_waitcnt vmcnt(9)
	v_and_b32_e32 v191, 0xffff, v11
	v_lshl_add_u32 v8, v128, 16, v126
	v_lshl_add_u32 v9, v149, 16, v147
	v_lshl_add_u32 v10, v166, 16, v154
	v_lshl_add_u32 v11, v181, 16, v170
	v_add3_u32 v2, s8, v2, v19
	v_lshlrev_b32_e32 v6, 16, v131
	v_and_b32_e32 v7, 0xffff0000, v131
	v_add_f32_e32 v5, 0, v5
	v_add_f32_e32 v4, 0, v4
	ds_write_b128 v2, v[8:11] offset:36352
	v_lshlrev_b32_e32 v8, 16, v140
	v_and_b32_e32 v9, 0xffff0000, v140
	v_add_f32_e32 v5, v5, v7
	v_add_f32_e32 v4, v4, v6
	v_lshlrev_b32_e32 v10, 16, v157
	v_and_b32_e32 v11, 0xffff0000, v157
	v_add_f32_e32 v5, v5, v9
	v_add_f32_e32 v4, v4, v8
	s_waitcnt vmcnt(6)
	v_and_b32_e32 v192, 0xffff, v12
	s_waitcnt vmcnt(3)
	v_and_b32_e32 v190, 0xffff, v13
	v_lshlrev_b32_e32 v12, 16, v155
	v_and_b32_e32 v13, 0xffff0000, v155
	v_add_f32_e32 v5, v5, v11
	v_add_f32_e32 v4, v4, v10
	s_bitcmp1_b32 s39, 0
	v_lshlrev_b32_e32 v18, 16, v167
	v_and_b32_e32 v19, 0xffff0000, v167
	v_add_f32_e32 v5, v5, v13
	v_add_f32_e32 v4, v4, v12
	s_cselect_b32 s4, 0xb400, 0
	v_lshlrev_b32_e32 v20, 16, v172
	v_and_b32_e32 v21, 0xffff0000, v172
	v_add_f32_e32 v5, v5, v19
	v_add_f32_e32 v4, v4, v18
	s_add_i32 s4, s4, 0
	v_lshlrev_b32_e32 v22, 16, v175
	v_and_b32_e32 v23, 0xffff0000, v175
	v_add_f32_e32 v5, v5, v21
	v_add_f32_e32 v4, v4, v20
	v_lshlrev_b32_e32 v2, 9, v16
	v_add_f32_e32 v5, v5, v23
	v_add_f32_e32 v4, v4, v22
	v_add3_u32 v2, s4, v2, v15
	s_waitcnt vmcnt(0)
	v_and_b32_e32 v187, 0xffff, v14
	ds_write_b64 v2, v[4:5] offset:41984
	v_mov_b64_e32 v[4:5], v[36:37]
	v_mov_b64_e32 v[20:21], v[52:53]
	v_mov_b64_e32 v[6:7], v[38:39]
	v_mov_b64_e32 v[8:9], v[40:41]
	v_mov_b64_e32 v[10:11], v[42:43]
	v_mov_b64_e32 v[12:13], v[44:45]
	v_mov_b64_e32 v[14:15], v[46:47]
	v_mov_b64_e32 v[16:17], v[48:49]
	v_mov_b64_e32 v[18:19], v[50:51]
	v_mov_b64_e32 v[22:23], v[54:55]
	v_mov_b64_e32 v[24:25], v[56:57]
	v_mov_b64_e32 v[26:27], v[58:59]
	v_mov_b64_e32 v[28:29], v[60:61]
	v_mov_b64_e32 v[30:31], v[62:63]
	v_mov_b64_e32 v[32:33], v[64:65]
	v_mov_b64_e32 v[34:35], v[66:67]
.LBB0_420:
	s_mov_b64 s[4:5], -1
	s_and_b64 vcc, exec, s[42:43]
	s_waitcnt lgkmcnt(0)
	s_barrier
	s_cbranch_vccz .LBB0_422
	s_andn2_b32 s4, 1, s39
	v_mov_b32_e32 v2, v0
	s_mul_i32 s5, s4, 0xb400
	s_add_i32 s62, s5, 0
	v_and_b32_e32 v193, 31, v2
	v_bfe_u32 v2, v2, 5, 1
	v_or_b32_e32 v37, s3, v193
	v_mov_b32_e32 v38, s62
	s_lshl_b32 s4, s4, 14
	v_lshlrev_b32_e32 v36, 8, v2
	v_mad_u32_u24 v37, v37, s86, v38
	v_lshlrev_b32_e32 v226, 4, v2
	v_lshlrev_b32_e32 v210, 3, v2
	s_add_i32 s4, s4, 0
	v_or3_b32 v36, v36, s73, v193
	v_add_u32_e32 v39, v37, v226
	v_add_u32_e32 v37, v37, v210
	v_lshl_add_u32 v242, v36, 2, s4
	v_mov_b32_e32 v36, v193
	v_add_u32_e32 v37, 0x8800, v37
	v_lshlrev_b32_e32 v2, 2, v2
	ds_read2_b64 v[100:103], v37 offset0:192 offset1:194
	ds_read2_b64 v[104:107], v37 offset0:196 offset1:198
	ds_read_b128 v[108:111], v39 offset:36352
	ds_read_b128 v[112:115], v39 offset:36384
	v_or_b32_e32 v37, 2, v2
	v_cmp_gt_i32_e64 s[6:7], v37, v36
	v_or_b32_e32 v37, 3, v2
	v_cmp_gt_i32_e64 s[8:9], v37, v36
	v_or_b32_e32 v37, 8, v2
	v_cmp_gt_i32_e64 s[10:11], v37, v36
	v_or_b32_e32 v37, 9, v2
	v_cmp_gt_i32_e64 s[12:13], v37, v36
	v_or_b32_e32 v37, 10, v2
	v_cmp_gt_i32_e64 s[14:15], v37, v36
	v_or_b32_e32 v37, 11, v2
	v_cmp_gt_i32_e64 s[16:17], v37, v36
	v_or_b32_e32 v37, 16, v2
	v_cmp_gt_i32_e64 s[18:19], v37, v36
	v_or_b32_e32 v37, 17, v2
	v_cmp_gt_i32_e64 s[20:21], v37, v36
	v_or_b32_e32 v37, 18, v2
	v_cmp_gt_i32_e64 s[22:23], v37, v36
	v_or_b32_e32 v37, 19, v2
	v_cmp_gt_i32_e64 s[24:25], v37, v36
	v_or_b32_e32 v37, 24, v2
	v_cmp_gt_i32_e64 s[26:27], v37, v36
	v_or_b32_e32 v37, 25, v2
	v_cmp_gt_i32_e32 vcc, v2, v36
	v_cmp_lt_i32_e64 s[4:5], v2, v36
	v_cmp_gt_i32_e64 s[28:29], v37, v36
	v_or_b32_e32 v37, 26, v2
	v_or_b32_e32 v2, 27, v2
	v_mad_u32_u24 v211, v193, s87, v38
	v_cmp_gt_i32_e64 s[30:31], v37, v36
	v_cmp_gt_i32_e64 s[34:35], v2, v36
	v_or_b32_e32 v36, s63, v210
	v_add_u32_e32 v222, v211, v210
	v_lshl_add_u32 v36, v36, 1, v211
	ds_read_b128 v[68:71], v36 offset:17408
	ds_read_b128 v[72:75], v36 offset:8704
	v_add_u32_e32 v36, s64, v222
	v_add_u32_e32 v36, 0x2000, v36
	v_add_u32_e32 v212, s62, v226
	v_or_b32_e32 v2, s63, v193
	ds_read2_b64 v[76:79], v36 offset0:64 offset1:66
	v_or_b32_e32 v36, s65, v210
	v_mad_u32_u24 v2, v2, s86, v212
	v_lshl_add_u32 v36, v36, 1, v211
	ds_read_b128 v[80:83], v36 offset:17408
	ds_read_b128 v[84:87], v36 offset:8704
	ds_read_b128 v[88:91], v2 offset:26112
	ds_read_b128 v[92:95], v2 offset:26144
	v_add_u32_e32 v2, s66, v222
	v_add_u32_e32 v2, 0x2000, v2
	ds_read2_b64 v[96:99], v2 offset0:64 offset1:66
	v_or_b32_e32 v2, s67, v226
	v_add_u32_e32 v2, s62, v2
	ds_read_b128 v[36:39], v2 offset:41472
	ds_read_b128 v[40:43], v2 offset:41504
	ds_read_b128 v[44:47], v2 offset:44032
	ds_read_b128 v[48:51], v2 offset:44064
	ds_read_b128 v[52:55], v2 offset:41536
	ds_read_b128 v[56:59], v2 offset:41568
	ds_read_b128 v[60:63], v2 offset:44096
	ds_read_b128 v[64:67], v2 offset:44128
	s_waitcnt lgkmcnt(0)
; DI int crow(int reg, int h) { return (reg & 3) + 8 * (reg >> 2) + 4 * h; }
; #define MFMA32(a, b, c) __builtin_amdgcn_mfma_f32_32x32x16_bf16((a), (b), (c), 0, 0, 0)
; DI void h_chain(f32x16& S, f32x16& O, HPacks& K, const HOpsK& P, const bf16x8 (&vt)[2], const u32x4 (&vv)[2], int rq, int hh) {
;     f32x16 X;
;     { f32x16 Se;
; #pragma unroll
;       for (int g = 0; g < 4; ++g) {
; #pragma unroll
;           for (int e = 0; e < 4; ++e) Se[4 * g + e] = S[4 * g + e] * P.ebm[g][e]; }
;       K.sp0 = pack_step(Se, 0); K.sp1 = pack_step(Se, 1); }
; #pragma unroll
;     for (int g = 0; g < 4; ++g) {
; #pragma unroll
;         for (int e = 0; e < 4; ++e) S[4 * g + e] *= P.dec[g][e]; }
; #pragma unroll
;     for (int i = 0; i < 16; ++i) { X[i] = 0.f; O[i] = 0.f; }
;     __builtin_amdgcn_sched_barrier(0);
; #pragma unroll
;     for (int st = 0; st < 2; ++st) X = MFMA32(P.ka[st], P.qb[st], X);
; #pragma unroll
;     for (int i = 0; i < 16; ++i) X[i] = (crow(i, hh) <= rq) ? X[i] : 0.f;
;     K.xp0 = pack_step(X, 0); K.xp1 = pack_step(X, 1);
;     __builtin_amdgcn_sched_barrier(0);
;     O = MFMA32(K.xp0, __builtin_bit_cast(bf16x8, vv[0]), O);
;     O = MFMA32(__builtin_bit_cast(bf16x8, P.qq[0]), K.sp0, O);
;     O = MFMA32(K.xp1, __builtin_bit_cast(bf16x8, vv[1]), O);
;     O = MFMA32(__builtin_bit_cast(bf16x8, P.qq[1]), K.sp1, O);
; #pragma unroll
;     for (int st = 0; st < 2; ++st) S = MFMA32(P.ku[st], vt[st], S);
;     __builtin_amdgcn_sched_barrier(0);
; }
	s_waitcnt lgkmcnt(5)
	v_mul_f32_e32 v45, v21, v45
	v_mul_f32_e32 v44, v20, v44
	v_mul_f32_e32 v47, v23, v47
	v_mul_f32_e32 v46, v22, v46
	s_waitcnt lgkmcnt(4)
	v_mul_f32_e32 v49, v25, v49
	v_mul_f32_e32 v48, v24, v48
	v_mul_f32_e32 v51, v27, v51
	v_mul_f32_e32 v50, v26, v50
	s_waitcnt lgkmcnt(1)
	v_mul_f32_e32 v61, v29, v61
	v_mul_f32_e32 v60, v28, v60
	v_mul_f32_e32 v63, v31, v63
	v_mul_f32_e32 v62, v30, v62
	s_waitcnt lgkmcnt(0)
	v_mul_f32_e32 v65, v33, v65
	v_mul_f32_e32 v64, v32, v64
	v_mul_f32_e32 v67, v35, v67
	v_mul_f32_e32 v66, v34, v66
	v_cvt_pk_bf16_f32 v194, v44, v45
	v_cvt_pk_bf16_f32 v195, v46, v47
	v_cvt_pk_bf16_f32 v196, v48, v49
	v_cvt_pk_bf16_f32 v197, v50, v51
	v_mul_f32_e32 v51, v35, v59
	v_mul_f32_e32 v50, v34, v58
	v_mul_f32_e32 v47, v31, v55
	v_mul_f32_e32 v46, v30, v54
	v_mul_f32_e32 v43, v27, v43
	v_mul_f32_e32 v42, v26, v42
	v_mul_f32_e32 v39, v23, v39
	v_mul_f32_e32 v38, v22, v38
	v_mul_f32_e32 v49, v33, v57
	v_mul_f32_e32 v48, v32, v56
	v_mul_f32_e32 v45, v29, v53
	v_mul_f32_e32 v44, v28, v52
	v_mul_f32_e32 v41, v25, v41
	v_mul_f32_e32 v40, v24, v40
	v_mul_f32_e32 v37, v21, v37
	v_mul_f32_e32 v36, v20, v36
	v_cvt_pk_bf16_f32 v198, v60, v61
	v_cvt_pk_bf16_f32 v199, v62, v63
	v_cvt_pk_bf16_f32 v200, v64, v65
	v_cvt_pk_bf16_f32 v201, v66, v67
	v_mfma_f32_32x32x16_bf16 v[52:67], v[68:71], v[72:75], 0
	v_mfma_f32_32x32x16_bf16 v[52:67], v[80:83], v[84:87], v[52:67]
	s_nop 11
	v_cndmask_b32_e64 v2, v52, 0, vcc
	v_cndmask_b32_e64 v52, 0, v53, s[4:5]
	v_cndmask_b32_e64 v53, v54, 0, s[6:7]
	v_cndmask_b32_e64 v54, v55, 0, s[8:9]
	v_cndmask_b32_e64 v55, v56, 0, s[10:11]
	v_cndmask_b32_e64 v56, v57, 0, s[12:13]
	v_cndmask_b32_e64 v57, v58, 0, s[14:15]
	v_cndmask_b32_e64 v58, v59, 0, s[16:17]
	v_cndmask_b32_e64 v59, v60, 0, s[18:19]
	v_cndmask_b32_e64 v60, v61, 0, s[20:21]
	v_cndmask_b32_e64 v61, v62, 0, s[22:23]
	v_cndmask_b32_e64 v62, v63, 0, s[24:25]
	v_cndmask_b32_e64 v63, v64, 0, s[26:27]
	v_cndmask_b32_e64 v64, v65, 0, s[28:29]
	v_cndmask_b32_e64 v65, v66, 0, s[30:31]
	v_cndmask_b32_e64 v66, v67, 0, s[34:35]
	v_cvt_pk_bf16_f32 v202, v2, v52
	v_cvt_pk_bf16_f32 v203, v53, v54
	v_cvt_pk_bf16_f32 v204, v55, v56
	v_cvt_pk_bf16_f32 v205, v57, v58
	v_cvt_pk_bf16_f32 v206, v59, v60
	v_cvt_pk_bf16_f32 v207, v61, v62
	v_cvt_pk_bf16_f32 v208, v63, v64
	v_cvt_pk_bf16_f32 v209, v65, v66
	v_mfma_f32_32x32x16_bf16 v[52:67], v[202:205], v[100:103], 0
	v_mfma_f32_32x32x16_bf16 v[52:67], v[76:79], v[194:197], v[52:67]
	v_mfma_f32_32x32x16_bf16 v[36:51], v[88:91], v[108:111], v[36:51]
	v_mfma_f32_32x32x16_bf16 v[52:67], v[206:209], v[104:107], v[52:67]
	v_mfma_f32_32x32x16_bf16 v[36:51], v[92:95], v[112:115], v[36:51]
	v_mfma_f32_32x32x16_bf16 v[52:67], v[96:99], v[198:201], v[52:67]
	s_nop 11
	v_add_f32_e32 v2, v67, v51
	v_mov_b32 v2, v2
	s_nop 0
	v_or_b32_e32 v68, s68, v210
	v_lshl_add_u32 v68, v68, 1, v211
	ds_read_b128 v[194:197], v68 offset:17408
	ds_read_b128 v[198:201], v68 offset:8704
	v_add_u32_e32 v68, s69, v222
	v_add_u32_e32 v68, 0x2000, v68
	v_or_b32_e32 v2, s68, v193
	ds_read2_b64 v[202:205], v68 offset0:64 offset1:66
	v_or_b32_e32 v68, s70, v210
	v_mad_u32_u24 v2, v2, s86, v212
	v_lshl_add_u32 v68, v68, 1, v211
	ds_read_b128 v[206:209], v68 offset:17408
	ds_read_b128 v[210:213], v68 offset:8704
	ds_read_b128 v[214:217], v2 offset:26112
	ds_read_b128 v[218:221], v2 offset:26144
	v_add_u32_e32 v2, s71, v222
	v_add_u32_e32 v2, 0x2000, v2
	ds_read2_b64 v[222:225], v2 offset0:64 offset1:66
	v_or_b32_e32 v2, s72, v226
	v_add_u32_e32 v2, s62, v2
	ds_read_b128 v[68:71], v2 offset:41472
	ds_read_b128 v[72:75], v2 offset:41504
	ds_read_b128 v[76:79], v2 offset:44032
	ds_read_b128 v[80:83], v2 offset:44064
	ds_read_b128 v[84:87], v2 offset:41536
	ds_read_b128 v[88:91], v2 offset:41568
	ds_read_b128 v[92:95], v2 offset:44096
	ds_read_b128 v[96:99], v2 offset:44128
	s_waitcnt lgkmcnt(0)
; DI void h_chain(f32x16& S, f32x16& O, HPacks& K, const HOpsK& P, const bf16x8 (&vt)[2], const u32x4 (&vv)[2], int rq, int hh) {
;     f32x16 X;
;     { f32x16 Se;
; #pragma unroll
;       for (int g = 0; g < 4; ++g) {
; #pragma unroll
;           for (int e = 0; e < 4; ++e) Se[4 * g + e] = S[4 * g + e] * P.ebm[g][e]; }
;       K.sp0 = pack_step(Se, 0); K.sp1 = pack_step(Se, 1); }
; #pragma unroll
;     for (int g = 0; g < 4; ++g) {
; #pragma unroll
;         for (int e = 0; e < 4; ++e) S[4 * g + e] *= P.dec[g][e]; }
; #pragma unroll
;     for (int i = 0; i < 16; ++i) { X[i] = 0.f; O[i] = 0.f; }
;     __builtin_amdgcn_sched_barrier(0);
; #pragma unroll
;     for (int st = 0; st < 2; ++st) X = MFMA32(P.ka[st], P.qb[st], X);
; #pragma unroll
;     for (int i = 0; i < 16; ++i) X[i] = (crow(i, hh) <= rq) ? X[i] : 0.f;
;     K.xp0 = pack_step(X, 0); K.xp1 = pack_step(X, 1);
;     __builtin_amdgcn_sched_barrier(0);
;     O = MFMA32(K.xp0, __builtin_bit_cast(bf16x8, vv[0]), O);
;     O = MFMA32(__builtin_bit_cast(bf16x8, P.qq[0]), K.sp0, O);
;     O = MFMA32(K.xp1, __builtin_bit_cast(bf16x8, vv[1]), O);
;     O = MFMA32(__builtin_bit_cast(bf16x8, P.qq[1]), K.sp1, O);
; #pragma unroll
;     for (int st = 0; st < 2; ++st) S = MFMA32(P.ku[st], vt[st], S);
;     __builtin_amdgcn_sched_barrier(0);
; }
; DI void h_mma2(f32x16& S0, f32x16& S1, LAS unsigned char* buf, LAS unsigned char* red, int kbp, int vb, int r32, int hh) {
;     int rq = r32; asm volatile("" : "+v"(rq));
;     bf16x8 vt[2]; u32x4 vv[2];
; #pragma unroll
;     for (int st = 0; st < 2; ++st) {
;         vt[st] = *(const LAS bf16x8*)(buf + H_VT + (vb * 32 + r32) * 80 + (16 * st + 8 * hh) * 2);
;         const LAS unsigned char* vp = buf + H_VT + (vb * 32 + r32) * 80 + (16 * st + 4 * hh) * 2;
;         const u32x2 v0 = *(const LAS u32x2*)vp, v1 = *(const LAS u32x2*)(vp + 16);
;         vv[st].x = v0.x; vv[st].y = v0.y; vv[st].z = v1.x; vv[st].w = v1.y;
;     }
;     f32x16 Osum;
; #pragma unroll
;     for (int kk = 0; kk < 2; ++kk) {
;         HOpsK P; h_opsk_load(P, buf, 2 * kbp + kk, r32, hh);
;         f32x16& S = (kk == 0) ? S0 : S1; f32x16 O;
;         LDS_WAIT(); __builtin_amdgcn_sched_barrier(0);
;         HPacks K;
;         h_chain(S, O, K, P, vt, vv, rq, hh);
;         { float s_ = S[15] + O[15]; asm volatile("v_mov_b32 %0, %0" : "+v"(s_)); asm volatile("" :: "v"(s_)); }
	s_waitcnt lgkmcnt(5)
	v_mul_f32_e32 v77, v5, v77
	v_mul_f32_e32 v76, v4, v76
	v_mul_f32_e32 v79, v7, v79
	v_mul_f32_e32 v78, v6, v78
	s_waitcnt lgkmcnt(4)
	v_mul_f32_e32 v81, v9, v81
	v_mul_f32_e32 v80, v8, v80
	v_mul_f32_e32 v83, v11, v83
	v_mul_f32_e32 v82, v10, v82
	s_waitcnt lgkmcnt(1)
	v_mul_f32_e32 v93, v13, v93
	v_mul_f32_e32 v92, v12, v92
	v_mul_f32_e32 v95, v15, v95
	v_mul_f32_e32 v94, v14, v94
	s_waitcnt lgkmcnt(0)
	v_mul_f32_e32 v97, v17, v97
	v_mul_f32_e32 v96, v16, v96
	v_mul_f32_e32 v99, v19, v99
	v_mul_f32_e32 v98, v18, v98
	v_cvt_pk_bf16_f32 v226, v76, v77
	v_cvt_pk_bf16_f32 v227, v78, v79
	v_cvt_pk_bf16_f32 v228, v80, v81
	v_cvt_pk_bf16_f32 v229, v82, v83
	v_mul_f32_e32 v83, v19, v91
	v_mul_f32_e32 v82, v18, v90
	v_mul_f32_e32 v79, v15, v87
	v_mul_f32_e32 v78, v14, v86
	v_mul_f32_e32 v75, v11, v75
	v_mul_f32_e32 v74, v10, v74
	v_mul_f32_e32 v71, v7, v71
	v_mul_f32_e32 v70, v6, v70
	v_mul_f32_e32 v81, v17, v89
	v_mul_f32_e32 v80, v16, v88
	v_mul_f32_e32 v77, v13, v85
	v_mul_f32_e32 v76, v12, v84
	v_mul_f32_e32 v73, v9, v73
	v_mul_f32_e32 v72, v8, v72
	v_mul_f32_e32 v69, v5, v69
	v_mul_f32_e32 v68, v4, v68
	v_cvt_pk_bf16_f32 v230, v92, v93
	v_cvt_pk_bf16_f32 v231, v94, v95
	v_cvt_pk_bf16_f32 v232, v96, v97
	v_cvt_pk_bf16_f32 v233, v98, v99
	v_mfma_f32_32x32x16_bf16 v[84:99], v[194:197], v[198:201], 0
	v_mfma_f32_32x32x16_bf16 v[84:99], v[206:209], v[210:213], v[84:99]
	s_nop 11
	v_cndmask_b32_e64 v2, v84, 0, vcc
	v_cndmask_b32_e64 v84, 0, v85, s[4:5]
	v_cndmask_b32_e64 v85, v86, 0, s[6:7]
	v_cndmask_b32_e64 v86, v87, 0, s[8:9]
	v_cndmask_b32_e64 v87, v88, 0, s[10:11]
	v_cndmask_b32_e64 v88, v89, 0, s[12:13]
	v_cndmask_b32_e64 v89, v90, 0, s[14:15]
	v_cndmask_b32_e64 v90, v91, 0, s[16:17]
	v_cndmask_b32_e64 v91, v92, 0, s[18:19]
	v_cndmask_b32_e64 v92, v93, 0, s[20:21]
	v_cndmask_b32_e64 v93, v94, 0, s[22:23]
	v_cndmask_b32_e64 v94, v95, 0, s[24:25]
	v_cndmask_b32_e64 v95, v96, 0, s[26:27]
	v_cndmask_b32_e64 v96, v97, 0, s[28:29]
	v_cndmask_b32_e64 v97, v98, 0, s[30:31]
	v_cndmask_b32_e64 v98, v99, 0, s[34:35]
	v_cvt_pk_bf16_f32 v234, v2, v84
	v_cvt_pk_bf16_f32 v235, v85, v86
	v_cvt_pk_bf16_f32 v236, v87, v88
	v_cvt_pk_bf16_f32 v237, v89, v90
	v_cvt_pk_bf16_f32 v238, v91, v92
	v_cvt_pk_bf16_f32 v239, v93, v94
	v_cvt_pk_bf16_f32 v240, v95, v96
	v_cvt_pk_bf16_f32 v241, v97, v98
	v_mfma_f32_32x32x16_bf16 v[84:99], v[234:237], v[100:103], 0
	v_mfma_f32_32x32x16_bf16 v[84:99], v[202:205], v[226:229], v[84:99]
	v_mfma_f32_32x32x16_bf16 v[68:83], v[214:217], v[108:111], v[68:83]
	v_mfma_f32_32x32x16_bf16 v[84:99], v[238:241], v[104:107], v[84:99]
	v_mfma_f32_32x32x16_bf16 v[68:83], v[218:221], v[112:115], v[68:83]
	v_mfma_f32_32x32x16_bf16 v[84:99], v[222:225], v[230:233], v[84:99]
	s_nop 11
	v_add_f32_e32 v2, v99, v83
	v_mov_b32 v2, v2
	s_nop 0
	v_add_f32_e32 v2, v67, v99
	v_add_f32_e32 v66, v66, v98
	v_add_f32_e32 v65, v65, v97
	v_add_f32_e32 v64, v64, v96
	v_add_f32_e32 v63, v63, v95
	v_add_f32_e32 v62, v62, v94
	v_add_f32_e32 v61, v61, v93
	v_add_f32_e32 v60, v60, v92
	v_add_f32_e32 v59, v59, v91
	v_add_f32_e32 v58, v58, v90
	v_add_f32_e32 v57, v57, v89
	v_add_f32_e32 v56, v56, v88
	v_add_f32_e32 v55, v55, v87
	v_add_f32_e32 v54, v54, v86
	v_add_f32_e32 v53, v53, v85
	v_add_f32_e32 v52, v52, v84
	v_add_u32_e32 v67, 0x16800, v242
	ds_write2st64_b32 v67, v52, v53 offset1:1
	ds_write2st64_b32 v67, v54, v55 offset0:2 offset1:3
	ds_write2st64_b32 v67, v56, v57 offset0:8 offset1:9
	ds_write2st64_b32 v67, v58, v59 offset0:10 offset1:11
	ds_write2st64_b32 v67, v60, v61 offset0:16 offset1:17
	ds_write2st64_b32 v67, v62, v63 offset0:18 offset1:19
	ds_write2st64_b32 v67, v64, v65 offset0:24 offset1:25
	ds_write2st64_b32 v67, v66, v2 offset0:26 offset1:27
	s_mov_b64 s[4:5], 0

; #define LAS __attribute__((address_space(3)))
; DI unsigned pk2(float lo, float hi) { return cvtpk_s(lo, hi); }
; template <int SET> DI void h_prep8(const unsigned (&CR)[72], LAS unsigned char* buf, int tgp, int k2, int v64) {
;     float base0 = 0.f, base1 = 0.f, bm0 = 0.f, bm1 = 0.f, bl0 = 0.f, bl1 = 0.f;
; #pragma unroll
;     for (int g = 0; g < 4; ++g) { const f32x2_t tt = *(const LAS f32x2_t*)(buf + H_TOT + (g * 128 + 2 * k2) * 4);
;         if (g < tgp) { base0 += tt[0]; base1 += tt[1]; } if (g < 2) { bm0 += tt[0]; bm1 += tt[1]; } bl0 += tt[0]; bl1 += tt[1]; }
;     const float ebm0 = __expf(bm0), ebm1 = __expf(bm1), elm0 = __expf(bl0 - bm0), elm1 = __expf(bl1 - bm1);
;     float e20 = __expf(base0 - bm0), e21 = __expf(base1 - bm1); unsigned kup0[4], kup1[4];
; #pragma unroll
;     for (int jp = 0; jp < 4; ++jp) {
;         float ku0[2], ku1[2];
; #pragma unroll
;         for (int jj = 0; jj < 2; ++jj) {
;             const int j = 2 * jp + jj;
;             const unsigned fw = CR[24 * SET + 8 + j], qw = CR[24 * SET + j];
;             const float f0 = __expf(bflo(fw)), f1 = __expf(bfhi(fw)), q0 = bflo(qw), q1 = bfhi(qw);
;             e20 *= f0; e21 *= f1;
;             const float e30 = __builtin_amdgcn_rcpf(e20), e31 = __builtin_amdgcn_rcpf(e21);
;             const float kk0 = 1.0f - f0, kk1 = 1.0f - f1;
;             const int t = 8 * tgp + j;
;             *(LAS unsigned*)(buf + H_QS + t * 272 + 4 * k2) = pk2(q0 * e20, q1 * e21);
;             *(LAS unsigned*)(buf + H_KS + t * 272 + 4 * k2) = pk2(kk0 * e30, kk1 * e31);
;             ku0[jj] = kk0 * e30 * elm0; ku1[jj] = kk1 * e31 * elm1;
;         }
;         kup0[jp] = pk2(ku0[0], ku0[1]); kup1[jp] = pk2(ku1[0], ku1[1]);
;     }
;     { u32x4 w; w.x = kup0[0]; w.y = kup0[1]; w.z = kup0[2]; w.w = kup0[3]; *(LAS u32x4*)(buf + H_KU + (2 * k2) * 80 + 16 * tgp) = w;
; DI void h_reduce_store2(LAS unsigned char* red, bf16_t* op, int c, int pt) {
; #pragma unroll
;     for (int s2 = 0; s2 < 2; ++s2) {
;         const int s = pt + 256 * s2, t = s >> 4, c4 = s & 15;
;         const f32x4 a = *(const LAS f32x4*)(red + ((0 * 32 + t) * 64 + 4 * c4) * 4), b2 = *(const LAS f32x4*)(red + ((1 * 32 + t) * 64 + 4 * c4) * 4);
;         const f32x4 sm = a + b2;
;         u32x2 w; w.x = pk2(sm[0], sm[1]); w.y = pk2(sm[2], sm[3]);
;         *(u32x2*)(op + (size_t)(32 * c + t) * D + 4 * c4) = w;
;     }
; }
.LBB0_425:
	s_add_i32 s6, s38, 0x4000
	s_and_b32 s6, s6, 0x4000
	s_add_i32 s6, s6, 0
	s_add_i32 s8, s39, 1
	s_add_i32 s9, s6, 0x16800
	s_lshl_b64 s[6:7], s[52:53], 1
	s_waitcnt lgkmcnt(0)
	s_add_u32 s4, s4, s6
	s_addc_u32 s5, s5, s7
	s_lshl_b32 s6, s96, 1
	v_lshlrev_b32_e32 v2, 2, v36
	s_add_u32 s4, s4, s6
	v_and_b32_e32 v2, 60, v2
	v_bfe_u32 v58, v36, 4, 4
	s_addc_u32 s5, s5, 0
	s_lshl_b32 s6, s48, 1
	v_lshlrev_b32_e32 v37, 2, v2
	v_lshlrev_b32_e32 v40, 8, v58
	s_add_u32 s4, s4, s6
	v_add3_u32 v37, s9, v37, v40
	s_addc_u32 s5, s5, 0
	v_lshlrev_b32_e32 v2, 1, v2
	ds_read_b128 v[40:43], v37
	ds_read_b128 v[44:47], v37 offset:8192
	v_lshl_add_u64 v[48:49], s[4:5], 0, v[2:3]
	v_lshl_add_u64 v[56:57], v[48:49], 0, s[50:51]
	ds_read_b128 v[48:51], v37 offset:4096
	ds_read_b128 v[52:55], v37 offset:12288
	v_lshl_add_u32 v37, v58, 11, s97
	s_waitcnt lgkmcnt(2)
	v_add_f32_e32 v43, v43, v47
	v_add_f32_e32 v42, v42, v46
	v_add_f32_e32 v41, v41, v45
	v_add_f32_e32 v40, v40, v44
	v_add_u32_e32 v2, 0x10000, v37
	v_cvt_pk_bf16_f32 v40, v40, v41
	v_cvt_pk_bf16_f32 v41, v42, v43
	v_lshl_add_u64 v[42:43], v[2:3], 1, v[56:57]
	s_andn2_b32 s4, 1, s8
	global_store_dwordx2 v[42:43], v[40:41], off
	s_waitcnt lgkmcnt(0)
	v_add_f32_e32 v41, v51, v55
	v_add_f32_e32 v40, v50, v54
	s_mul_i32 s4, s4, 0xb400
	v_cvt_pk_bf16_f32 v47, v40, v41
	s_add_i32 s9, s4, 0
	v_lshlrev_b32_e32 v40, 3, v38
	v_add_f32_e32 v43, v49, v53
	v_add_f32_e32 v42, v48, v52
	v_add_u32_e32 v41, s9, v40
	v_cvt_pk_bf16_f32 v46, v42, v43
	ds_read2st64_b64 v[42:45], v41 offset0:82 offset1:83
	v_add_u32_e32 v2, 0x18000, v37
	v_lshl_add_u64 v[48:49], v[2:3], 1, v[56:57]
	global_store_dwordx2 v[48:49], v[46:47], off
	ds_read2st64_b64 v[46:49], v41 offset0:84 offset1:85
	s_waitcnt lgkmcnt(1)
	v_add_f32_e32 v2, 0, v42
	v_cmp_lt_u32_sdwa s[4:5], v36, v120 src0_sel:BYTE_0 src1_sel:DWORD
	v_add_f32_e32 v37, 0, v43
	v_cmp_gt_u32_sdwa vcc, v36, s88 src0_sel:BYTE_0 src1_sel:DWORD
	v_cndmask_b32_e64 v43, v2, 0, s[4:5]
	v_cndmask_b32_e64 v42, v37, 0, s[4:5]
	v_add_f32_e32 v50, v44, v43
	v_bfe_u32 v39, v36, 6, 2
	v_add_f32_e32 v51, v45, v42
	v_cndmask_b32_e32 v43, v43, v50, vcc
	v_cndmask_b32_e32 v36, v42, v51, vcc
	v_add_f32_e32 v42, v2, v44
	s_waitcnt lgkmcnt(0)
	v_add_f32_e32 v2, v46, v43
	v_cmp_eq_u32_e32 vcc, 3, v39
	v_add_f32_e32 v37, v37, v45
	v_add_f32_e32 v44, v47, v36
	v_cndmask_b32_e32 v43, v43, v2, vcc
	v_add_f32_e32 v2, v42, v46
	v_add_f32_e32 v2, v2, v48
	v_cndmask_b32_e32 v45, v36, v44, vcc
	v_add_f32_e32 v36, v37, v47
	v_sub_f32_e32 v2, v2, v42
	v_sub_f32_e32 v43, v43, v42
	v_add_f32_e32 v44, v36, v49
	v_mul_f32_e32 v2, 0x3fb8aa3b, v2
	v_mul_f32_e32 v43, 0x3fb8aa3b, v43
	v_exp_f32_e32 v36, v2
	v_sub_f32_e32 v2, v44, v37
	v_exp_f32_e32 v44, v43
	v_sub_f32_e32 v43, v45, v37
	v_mul_f32_e32 v43, 0x3fb8aa3b, v43
	v_exp_f32_e32 v45, v43
	s_waitcnt vmcnt(21)
	v_lshlrev_b32_e32 v43, 16, v129
	v_mul_f32_e32 v43, 0x3fb8aa3b, v43
	v_exp_f32_e32 v46, v43
	v_and_b32_e32 v43, 0xffff0000, v129
	v_mul_f32_e32 v43, 0x3fb8aa3b, v43
	v_exp_f32_e32 v47, v43
	s_waitcnt vmcnt(19)
	v_lshlrev_b32_e32 v48, 16, v135
	v_and_b32_e32 v49, 0xffff0000, v135
	v_lshlrev_b32_e32 v43, 2, v38
	v_mul_f32_e32 v45, v47, v45
	v_mul_f32_e32 v44, v46, v44
	v_mul_f32_e32 v2, 0x3fb8aa3b, v2
	v_mul_f32_e32 v49, v45, v49
	v_mul_f32_e32 v48, v44, v48
	v_rcp_f32_e32 v50, v44
	v_cvt_pk_bf16_f32 v54, v48, v49
	v_mul_u32_u24_e32 v48, 0x880, v39
	v_add3_u32 v43, s9, v43, v48
	v_lshlrev_b32_e32 v48, 16, v131
	v_and_b32_e32 v49, 0xffff0000, v131
	v_mul_f32_e32 v48, 0x3fb8aa3b, v48
	v_mul_f32_e32 v49, 0x3fb8aa3b, v49
	v_exp_f32_e32 v48, v48
	v_exp_f32_e32 v49, v49
	v_rcp_f32_e32 v51, v45
	v_exp_f32_e32 v2, v2
	v_sub_f32_e32 v47, 1.0, v47
	v_sub_f32_e32 v46, 1.0, v46
	v_mul_f32_e32 v53, v49, v45
	v_mul_f32_e32 v52, v48, v44
	v_sub_f32_e32 v49, 1.0, v49
	v_sub_f32_e32 v48, 1.0, v48
	v_rcp_f32_e32 v44, v52
	v_rcp_f32_e32 v45, v53
	v_mul_f32_e32 v47, v47, v51
	v_mul_f32_e32 v46, v46, v50
	s_waitcnt vmcnt(18)
	v_lshlrev_b32_e32 v50, 16, v138
	v_cvt_pk_bf16_f32 v55, v46, v47
	v_mul_f32_e32 v45, v49, v45
	v_mul_f32_e32 v44, v48, v44
	v_and_b32_e32 v51, 0xffff0000, v138
	v_cvt_pk_bf16_f32 v48, v44, v45
	v_add_u32_e32 v58, 0x4400, v43
	v_mov_b32_e32 v49, v44
	v_mov_b32_e32 v44, v47
	v_mul_f32_e32 v51, v53, v51
	v_mul_f32_e32 v50, v52, v50
	ds_write2_b32 v58, v55, v48 offset1:68
	v_mov_b32_e32 v48, v46
	v_mul_f32_e32 v47, v2, v45
	v_mul_f32_e32 v46, v2, v44
	s_waitcnt vmcnt(11)
	v_lshlrev_b32_e32 v45, 16, v140
	v_cvt_pk_bf16_f32 v50, v50, v51
	v_add_u32_e32 v51, 0x2000, v43
	v_mul_f32_e32 v45, 0x3fb8aa3b, v45
	ds_write2_b32 v51, v54, v50 offset0:128 offset1:196
	v_exp_f32_e32 v50, v45
	v_and_b32_e32 v45, 0xffff0000, v140
	v_mul_f32_e32 v45, 0x3fb8aa3b, v45
	v_exp_f32_e32 v51, v45
	v_mul_f32_e32 v49, v36, v49
	v_mul_f32_e32 v48, v36, v48
	v_cvt_pk_bf16_f32 v44, v48, v49
	v_cvt_pk_bf16_f32 v48, v46, v47
	v_lshlrev_b32_e32 v46, 16, v134
	v_and_b32_e32 v47, 0xffff0000, v134
	v_mul_f32_e32 v53, v51, v53
	v_mul_f32_e32 v52, v50, v52
	s_waitcnt vmcnt(10)
; #define LAS __attribute__((address_space(3)))
; DI unsigned pk2(float lo, float hi) { return cvtpk_s(lo, hi); }
; template <int SET> DI void h_totals8(const unsigned (&CR)[72], LAS unsigned char* buf, int tgp, int k2) {
;     float lo = 0.f, hi = 0.f;
; #pragma unroll
;     for (int j = 0; j < 8; ++j) { lo += bflo(CR[24 * SET + 8 + j]); hi += bfhi(CR[24 * SET + 8 + j]); }
;     *(LAS f32x2_t*)(buf + H_TOT + (tgp * 128 + 2 * k2) * 4) = (f32x2_t){lo, hi};
; }
; template <int SET> DI void h_prep8(const unsigned (&CR)[72], LAS unsigned char* buf, int tgp, int k2, int v64) {
;     ...
;     float e20 = __expf(base0 - bm0), e21 = __expf(base1 - bm1); unsigned kup0[4], kup1[4];
; #pragma unroll
;     for (int jp = 0; jp < 4; ++jp) {
;         float ku0[2], ku1[2];
; #pragma unroll
;         for (int jj = 0; jj < 2; ++jj) {
;             const int j = 2 * jp + jj;
;             const unsigned fw = CR[24 * SET + 8 + j], qw = CR[24 * SET + j];
;             const float f0 = __expf(bflo(fw)), f1 = __expf(bfhi(fw)), q0 = bflo(qw), q1 = bfhi(qw);
;             e20 *= f0; e21 *= f1;
;             const float e30 = __builtin_amdgcn_rcpf(e20), e31 = __builtin_amdgcn_rcpf(e21);
;             const float kk0 = 1.0f - f0, kk1 = 1.0f - f1;
;             const int t = 8 * tgp + j;
;             *(LAS unsigned*)(buf + H_QS + t * 272 + 4 * k2) = pk2(q0 * e20, q1 * e21);
;             *(LAS unsigned*)(buf + H_KS + t * 272 + 4 * k2) = pk2(kk0 * e30, kk1 * e31);
;             ku0[jj] = kk0 * e30 * elm0; ku1[jj] = kk1 * e31 * elm1;
;         }
;         kup0[jp] = pk2(ku0[0], ku0[1]); kup1[jp] = pk2(ku1[0], ku1[1]);
;     }
;     { u32x4 w; w.x = kup0[0]; w.y = kup0[1]; w.z = kup0[2]; w.w = kup0[3]; *(LAS u32x4*)(buf + H_KU + (2 * k2) * 80 + 16 * tgp) = w;
;       w.x = kup1[0]; w.y = kup1[1]; w.z = kup1[2]; w.w = kup1[3]; *(LAS u32x4*)(buf + H_KU + (2 * k2 + 1) * 80 + 16 * tgp) = w; }
;     if (tgp == 0) { *(LAS f32x2_t*)(buf + H_DEC + 8 * k2) = (f32x2_t){ebm0 * elm0, ebm1 * elm1}; *(LAS f32x2_t*)(buf + H_EBM + 8 * k2) = (f32x2_t){ebm0, ebm1}; }
;     { u32x4 w; w.x = (CR[24 * SET + 16] & 0xffffu) | (CR[24 * SET + 17] << 16); w.y = (CR[24 * SET + 18] & 0xffffu) | (CR[24 * SET + 19] << 16);
;       w.z = (CR[24 * SET + 20] & 0xffffu) | (CR[24 * SET + 21] << 16); w.w = (CR[24 * SET + 22] & 0xffffu) | (CR[24 * SET + 23] << 16);
;       *(LAS u32x4*)(buf + H_VT + v64 * 80 + 16 * tgp) = w; }
; }
	v_lshlrev_b32_e32 v49, 16, v157
	v_mul_f32_e32 v47, v53, v47
	v_mul_f32_e32 v46, v52, v46
	v_mul_f32_e32 v49, 0x3fb8aa3b, v49
	v_cvt_pk_bf16_f32 v45, v46, v47
	v_sub_f32_e32 v47, 1.0, v51
	v_sub_f32_e32 v46, 1.0, v50
	v_exp_f32_e32 v50, v49
	v_and_b32_e32 v49, 0xffff0000, v157
	v_mul_f32_e32 v49, 0x3fb8aa3b, v49
	v_exp_f32_e32 v51, v49
	v_rcp_f32_e32 v54, v52
	v_rcp_f32_e32 v55, v53
	v_add_u32_e32 v59, 0x2400, v43
	v_mul_f32_e32 v53, v51, v53
	v_mul_f32_e32 v52, v50, v52
	v_sub_f32_e32 v51, 1.0, v51
	v_sub_f32_e32 v50, 1.0, v50
	v_rcp_f32_e32 v56, v52
	v_rcp_f32_e32 v57, v53
	v_mul_f32_e32 v47, v47, v55
	v_mul_f32_e32 v46, v46, v54
	v_lshlrev_b32_e32 v54, 16, v151
	v_and_b32_e32 v55, 0xffff0000, v151
	v_mul_f32_e32 v55, v53, v55
	v_mul_f32_e32 v54, v52, v54
	v_mul_f32_e32 v51, v51, v57
	v_mul_f32_e32 v50, v50, v56
	v_cvt_pk_bf16_f32 v54, v54, v55
	v_cvt_pk_bf16_f32 v49, v46, v47
	ds_write2_b32 v59, v45, v54 offset0:8 offset1:76
	v_cvt_pk_bf16_f32 v45, v50, v51
	ds_write2_b32 v58, v49, v45 offset0:136 offset1:204
	v_lshlrev_b32_e32 v49, 16, v155
	v_mov_b32_e32 v55, v50
	v_mov_b32_e32 v50, v47
	v_mul_f32_e32 v49, 0x3fb8aa3b, v49
	v_mov_b32_e32 v54, v46
	v_mul_f32_e32 v47, v2, v51
	v_mul_f32_e32 v46, v2, v50
	v_exp_f32_e32 v50, v49
	v_and_b32_e32 v49, 0xffff0000, v155
	v_mul_f32_e32 v49, 0x3fb8aa3b, v49
	v_exp_f32_e32 v51, v49
	v_cvt_pk_bf16_f32 v49, v46, v47
	v_lshlrev_b32_e32 v46, 16, v160
	v_and_b32_e32 v47, 0xffff0000, v160
	v_mul_f32_e32 v53, v51, v53
	v_mul_f32_e32 v52, v50, v52
	v_mul_f32_e32 v55, v36, v55
	v_mul_f32_e32 v54, v36, v54
	v_mul_f32_e32 v47, v53, v47
	v_mul_f32_e32 v46, v52, v46
	v_cvt_pk_bf16_f32 v45, v54, v55
	v_cvt_pk_bf16_f32 v58, v46, v47
	v_sub_f32_e32 v47, 1.0, v51
	v_sub_f32_e32 v46, 1.0, v50
	v_lshlrev_b32_e32 v50, 16, v167
	v_and_b32_e32 v51, 0xffff0000, v167
	v_mul_f32_e32 v50, 0x3fb8aa3b, v50
	v_mul_f32_e32 v51, 0x3fb8aa3b, v51
	v_exp_f32_e32 v50, v50
	v_exp_f32_e32 v51, v51
	v_rcp_f32_e32 v54, v52
	v_rcp_f32_e32 v55, v53
	v_add_u32_e32 v62, 0x4800, v43
	v_mul_f32_e32 v53, v51, v53
	v_mul_f32_e32 v52, v50, v52
	v_sub_f32_e32 v51, 1.0, v51
	v_sub_f32_e32 v50, 1.0, v50
	v_rcp_f32_e32 v56, v52
	v_rcp_f32_e32 v57, v53
	v_mul_f32_e32 v47, v47, v55
	v_mul_f32_e32 v46, v46, v54
	v_lshlrev_b32_e32 v54, 16, v162
	v_and_b32_e32 v55, 0xffff0000, v162
	v_mul_f32_e32 v55, v53, v55
	v_mul_f32_e32 v54, v52, v54
	v_mul_f32_e32 v51, v51, v57
	v_mul_f32_e32 v50, v50, v56
	v_cvt_pk_bf16_f32 v54, v54, v55
	v_cvt_pk_bf16_f32 v60, v46, v47
	ds_write2_b32 v59, v58, v54 offset0:144 offset1:212
	v_cvt_pk_bf16_f32 v54, v50, v51
	ds_write2_b32 v62, v60, v54 offset0:16 offset1:84
	v_mov_b32_e32 v54, v46
	v_mov_b32_e32 v55, v50
	v_mov_b32_e32 v50, v47
	s_waitcnt vmcnt(5)
	v_lshlrev_b32_e32 v47, 16, v172
	v_mul_f32_e32 v55, v36, v55
	v_mul_f32_e32 v54, v36, v54
	v_mul_f32_e32 v47, 0x3fb8aa3b, v47
	v_cvt_pk_bf16_f32 v46, v54, v55
	v_exp_f32_e32 v54, v47
	v_and_b32_e32 v47, 0xffff0000, v172
	v_mul_f32_e32 v47, 0x3fb8aa3b, v47
	v_exp_f32_e32 v55, v47
	v_mul_f32_e32 v51, v2, v51
	v_mul_f32_e32 v50, v2, v50
	v_cvt_pk_bf16_f32 v50, v50, v51
	s_waitcnt vmcnt(3)
	v_lshlrev_b32_e32 v56, 16, v178
	v_and_b32_e32 v57, 0xffff0000, v178
	v_mul_f32_e32 v53, v55, v53
	v_mul_f32_e32 v52, v54, v52
	v_lshlrev_b32_e32 v51, 16, v175
	v_mul_f32_e32 v57, v53, v57
	v_mul_f32_e32 v56, v52, v56
	v_mul_f32_e32 v51, 0x3fb8aa3b, v51
	v_cvt_pk_bf16_f32 v47, v56, v57
	v_exp_f32_e32 v56, v51
	v_and_b32_e32 v51, 0xffff0000, v175
	v_mul_f32_e32 v51, 0x3fb8aa3b, v51
	v_exp_f32_e32 v57, v51
	v_rcp_f32_e32 v58, v52
	v_rcp_f32_e32 v59, v53
	v_sub_f32_e32 v55, 1.0, v55
	v_sub_f32_e32 v54, 1.0, v54
	v_mul_f32_e32 v53, v57, v53
	v_mul_f32_e32 v52, v56, v52
	v_add_u32_e32 v43, 0x2800, v43
	v_mul_f32_e32 v55, v55, v59
	v_mul_f32_e32 v54, v54, v58
	s_waitcnt vmcnt(2)
	v_lshlrev_b32_e32 v58, 16, v182
	v_and_b32_e32 v59, 0xffff0000, v182
	v_rcp_f32_e32 v60, v52
	v_rcp_f32_e32 v61, v53
	v_mul_f32_e32 v53, v53, v59
	v_mul_f32_e32 v52, v52, v58
	v_cvt_pk_bf16_f32 v51, v54, v55
	v_cvt_pk_bf16_f32 v52, v52, v53
	ds_write2_b32 v43, v47, v52 offset0:24 offset1:92
	v_sub_f32_e32 v53, 1.0, v57
	v_sub_f32_e32 v52, 1.0, v56
	v_mov_b32_e32 v56, v54
	v_mul_f32_e32 v53, v53, v61
	v_mul_f32_e32 v52, v52, v60
	s_nop 0
	v_cvt_pk_bf16_f32 v43, v52, v53
	v_mov_b32_e32 v57, v52
	v_mov_b32_e32 v52, v55
	v_mul_f32_e32 v53, v2, v53
	v_mul_f32_e32 v52, v2, v52
	ds_write2_b32 v62, v51, v43 offset0:152 offset1:220
	v_mul_f32_e32 v57, v36, v57
	v_mul_f32_e32 v56, v36, v56
	v_cvt_pk_bf16_f32 v51, v52, v53
	v_mul_u32_u24_e32 v52, 0xa0, v38
	v_lshlrev_b32_e32 v43, 4, v39
	v_cvt_pk_bf16_f32 v47, v56, v57
	v_add3_u32 v52, s9, v52, v43
	ds_write_b128 v52, v[44:47] offset:26112
	ds_write_b128 v52, v[48:51] offset:26192
	s_and_saveexec_b64 s[6:7], s[4:5]
	s_cbranch_execz .LBB0_427
	v_mul_f32_e32 v42, 0x3fb8aa3b, v42
	v_mul_f32_e32 v37, 0x3fb8aa3b, v37
	v_exp_f32_e32 v44, v42
	v_exp_f32_e32 v45, v37
	v_mov_b32_e32 v37, v2
	v_mul_f32_e32 v37, v45, v37
	v_mul_f32_e32 v36, v44, v36
	ds_write2st64_b64 v41, v[36:37], v[44:45] offset0:81 offset1:86
.LBB0_427:
	s_or_b64 exec, exec, s[6:7]
	v_mul_u32_u24_e32 v2, 0x50, v38
	v_lshlrev_b32_e32 v36, 16, v121
	v_and_b32_e32 v37, 0xffff0000, v121
	v_lshl_add_u32 v44, v127, 16, v125
	v_lshl_add_u32 v45, v148, 16, v146
	v_lshl_add_u32 v46, v165, 16, v153
	v_lshl_add_u32 v47, v180, 16, v169
	v_add3_u32 v2, s9, v2, v43
	v_lshlrev_b32_e32 v42, 16, v122
	v_and_b32_e32 v43, 0xffff0000, v122
	v_add_f32_e32 v37, 0, v37
	v_add_f32_e32 v36, 0, v36
	ds_write_b128 v2, v[44:47] offset:36352
	v_lshlrev_b32_e32 v44, 16, v133
	v_and_b32_e32 v45, 0xffff0000, v133
	v_add_f32_e32 v37, v37, v43
	v_add_f32_e32 v36, v36, v42
	v_lshlrev_b32_e32 v46, 16, v144
	v_and_b32_e32 v47, 0xffff0000, v144
	v_add_f32_e32 v37, v37, v45
	v_add_f32_e32 v36, v36, v44
	v_lshlrev_b32_e32 v48, 16, v150
	v_and_b32_e32 v49, 0xffff0000, v150
	v_add_f32_e32 v37, v37, v47
	v_add_f32_e32 v36, v36, v46
	s_bitcmp1_b32 s8, 0
	v_lshlrev_b32_e32 v50, 16, v164
	v_and_b32_e32 v51, 0xffff0000, v164
	v_add_f32_e32 v37, v37, v49
	v_add_f32_e32 v36, v36, v48
	s_cselect_b32 s4, 0xb400, 0
	v_lshlrev_b32_e32 v52, 16, v171
	v_and_b32_e32 v53, 0xffff0000, v171
	v_add_f32_e32 v37, v37, v51
	v_add_f32_e32 v36, v36, v50
	s_add_i32 s4, s4, 0
	v_lshlrev_b32_e32 v54, 16, v174
	v_and_b32_e32 v55, 0xffff0000, v174
	v_add_f32_e32 v37, v37, v53
	v_add_f32_e32 v36, v36, v52
	v_lshlrev_b32_e32 v2, 9, v39
	v_add_f32_e32 v37, v37, v55
	v_add_f32_e32 v36, v36, v54
	v_add3_u32 v2, s4, v2, v40
	ds_write_b64 v2, v[36:37] offset:41984
	s_branch .LBB0_429

; DI int crow(int reg, int h) { return (reg & 3) + 8 * (reg >> 2) + 4 * h; }
; #define MFMA32(a, b, c) __builtin_amdgcn_mfma_f32_32x32x16_bf16((a), (b), (c), 0, 0, 0)
; DI void h_chain(f32x16& S, f32x16& O, HPacks& K, const HOpsK& P, const bf16x8 (&vt)[2], const u32x4 (&vv)[2], int rq, int hh) {
;     f32x16 X;
;     { f32x16 Se;
; #pragma unroll
;       for (int g = 0; g < 4; ++g) {
; #pragma unroll
;           for (int e = 0; e < 4; ++e) Se[4 * g + e] = S[4 * g + e] * P.ebm[g][e]; }
;       K.sp0 = pack_step(Se, 0); K.sp1 = pack_step(Se, 1); }
; #pragma unroll
;     for (int g = 0; g < 4; ++g) {
; #pragma unroll
;         for (int e = 0; e < 4; ++e) S[4 * g + e] *= P.dec[g][e]; }
; #pragma unroll
;     for (int i = 0; i < 16; ++i) { X[i] = 0.f; O[i] = 0.f; }
;     __builtin_amdgcn_sched_barrier(0);
; #pragma unroll
;     for (int st = 0; st < 2; ++st) X = MFMA32(P.ka[st], P.qb[st], X);
; #pragma unroll
;     for (int i = 0; i < 16; ++i) X[i] = (crow(i, hh) <= rq) ? X[i] : 0.f;
;     K.xp0 = pack_step(X, 0); K.xp1 = pack_step(X, 1);
;     __builtin_amdgcn_sched_barrier(0);
;     O = MFMA32(K.xp0, __builtin_bit_cast(bf16x8, vv[0]), O);
;     O = MFMA32(__builtin_bit_cast(bf16x8, P.qq[0]), K.sp0, O);
;     O = MFMA32(K.xp1, __builtin_bit_cast(bf16x8, vv[1]), O);
;     O = MFMA32(__builtin_bit_cast(bf16x8, P.qq[1]), K.sp1, O);
; #pragma unroll
;     for (int st = 0; st < 2; ++st) S = MFMA32(P.ku[st], vt[st], S);
;     __builtin_amdgcn_sched_barrier(0);
; }
.LBB0_429:
	s_mov_b64 s[4:5], -1
	s_and_b64 vcc, exec, s[42:43]
	s_waitcnt lgkmcnt(0)
	s_barrier
	s_cbranch_vccz .LBB0_431
	s_and_b32 s4, s39, 1
	v_mov_b32_e32 v2, v0
	s_mul_i32 s5, s4, 0xb400
	s_add_i32 s62, s5, 0
	v_and_b32_e32 v193, 31, v2
	v_bfe_u32 v2, v2, 5, 1
	v_or_b32_e32 v37, s3, v193
	v_mov_b32_e32 v38, s62
	s_lshl_b32 s4, s4, 14
	v_lshlrev_b32_e32 v36, 8, v2
	v_mad_u32_u24 v37, v37, s86, v38
	v_lshlrev_b32_e32 v226, 4, v2
	v_lshlrev_b32_e32 v210, 3, v2
	s_add_i32 s4, s4, 0
	v_or3_b32 v36, v36, s73, v193
	v_add_u32_e32 v39, v37, v226
	v_add_u32_e32 v37, v37, v210
	v_lshl_add_u32 v242, v36, 2, s4
	v_mov_b32_e32 v36, v193
	v_add_u32_e32 v37, 0x8800, v37
	v_lshlrev_b32_e32 v2, 2, v2
	ds_read2_b64 v[100:103], v37 offset0:192 offset1:194
	ds_read2_b64 v[104:107], v37 offset0:196 offset1:198
	ds_read_b128 v[108:111], v39 offset:36352
	ds_read_b128 v[112:115], v39 offset:36384
	v_or_b32_e32 v37, 2, v2
	v_cmp_gt_i32_e64 s[6:7], v37, v36
	v_or_b32_e32 v37, 3, v2
	v_cmp_gt_i32_e64 s[8:9], v37, v36
	v_or_b32_e32 v37, 8, v2
	v_cmp_gt_i32_e64 s[10:11], v37, v36
	v_or_b32_e32 v37, 9, v2
	v_cmp_gt_i32_e64 s[12:13], v37, v36
	v_or_b32_e32 v37, 10, v2
	v_cmp_gt_i32_e64 s[14:15], v37, v36
	v_or_b32_e32 v37, 11, v2
	v_cmp_gt_i32_e64 s[16:17], v37, v36
	v_or_b32_e32 v37, 16, v2
	v_cmp_gt_i32_e64 s[18:19], v37, v36
	v_or_b32_e32 v37, 17, v2
	v_cmp_gt_i32_e64 s[20:21], v37, v36
	v_or_b32_e32 v37, 18, v2
	v_cmp_gt_i32_e64 s[22:23], v37, v36
	v_or_b32_e32 v37, 19, v2
	v_cmp_gt_i32_e64 s[24:25], v37, v36
	v_or_b32_e32 v37, 24, v2
	v_cmp_gt_i32_e64 s[26:27], v37, v36
	v_or_b32_e32 v37, 25, v2
	v_cmp_gt_i32_e32 vcc, v2, v36
	v_cmp_lt_i32_e64 s[4:5], v2, v36
	v_cmp_gt_i32_e64 s[28:29], v37, v36
	v_or_b32_e32 v37, 26, v2
	v_or_b32_e32 v2, 27, v2
	v_mad_u32_u24 v211, v193, s87, v38
	v_cmp_gt_i32_e64 s[30:31], v37, v36
	v_cmp_gt_i32_e64 s[34:35], v2, v36
	v_or_b32_e32 v36, s63, v210
	v_add_u32_e32 v222, v211, v210
	v_lshl_add_u32 v36, v36, 1, v211
	ds_read_b128 v[68:71], v36 offset:17408
	ds_read_b128 v[72:75], v36 offset:8704
	v_add_u32_e32 v36, s64, v222
	v_add_u32_e32 v36, 0x2000, v36
	v_add_u32_e32 v212, s62, v226
	v_or_b32_e32 v2, s63, v193
	ds_read2_b64 v[76:79], v36 offset0:64 offset1:66
	v_or_b32_e32 v36, s65, v210
	v_mad_u32_u24 v2, v2, s86, v212
	v_lshl_add_u32 v36, v36, 1, v211
	ds_read_b128 v[80:83], v36 offset:17408
	ds_read_b128 v[84:87], v36 offset:8704
	ds_read_b128 v[88:91], v2 offset:26112
	ds_read_b128 v[92:95], v2 offset:26144
	v_add_u32_e32 v2, s66, v222
	v_add_u32_e32 v2, 0x2000, v2
	ds_read2_b64 v[96:99], v2 offset0:64 offset1:66
	v_or_b32_e32 v2, s67, v226
	v_add_u32_e32 v2, s62, v2
	ds_read_b128 v[36:39], v2 offset:41472
	ds_read_b128 v[40:43], v2 offset:41504
	ds_read_b128 v[44:47], v2 offset:44032
	ds_read_b128 v[48:51], v2 offset:44064
	ds_read_b128 v[52:55], v2 offset:41536
	ds_read_b128 v[56:59], v2 offset:41568
	ds_read_b128 v[60:63], v2 offset:44096
	ds_read_b128 v[64:67], v2 offset:44128
	s_waitcnt lgkmcnt(0)
	s_waitcnt lgkmcnt(5)
	v_mul_f32_e32 v45, v21, v45
	v_mul_f32_e32 v44, v20, v44
	v_mul_f32_e32 v47, v23, v47
	v_mul_f32_e32 v46, v22, v46
	s_waitcnt lgkmcnt(4)
	v_mul_f32_e32 v49, v25, v49
	v_mul_f32_e32 v48, v24, v48
	v_mul_f32_e32 v51, v27, v51
	v_mul_f32_e32 v50, v26, v50
	s_waitcnt lgkmcnt(1)
	v_mul_f32_e32 v61, v29, v61
	v_mul_f32_e32 v60, v28, v60
	v_mul_f32_e32 v63, v31, v63
	v_mul_f32_e32 v62, v30, v62
	s_waitcnt lgkmcnt(0)
	v_mul_f32_e32 v65, v33, v65
	v_mul_f32_e32 v64, v32, v64
	v_mul_f32_e32 v67, v35, v67
	v_mul_f32_e32 v66, v34, v66
	v_cvt_pk_bf16_f32 v194, v44, v45
	v_cvt_pk_bf16_f32 v195, v46, v47
	v_cvt_pk_bf16_f32 v196, v48, v49
	v_cvt_pk_bf16_f32 v197, v50, v51
	v_mul_f32_e32 v51, v35, v59
	v_mul_f32_e32 v50, v34, v58
	v_mul_f32_e32 v47, v31, v55
	v_mul_f32_e32 v46, v30, v54
	v_mul_f32_e32 v43, v27, v43
	v_mul_f32_e32 v42, v26, v42
	v_mul_f32_e32 v39, v23, v39
	v_mul_f32_e32 v38, v22, v38
	v_mul_f32_e32 v49, v33, v57
	v_mul_f32_e32 v48, v32, v56
	v_mul_f32_e32 v45, v29, v53
	v_mul_f32_e32 v44, v28, v52
	v_mul_f32_e32 v41, v25, v41
	v_mul_f32_e32 v40, v24, v40
	v_mul_f32_e32 v37, v21, v37
	v_mul_f32_e32 v36, v20, v36
	v_cvt_pk_bf16_f32 v198, v60, v61
	v_cvt_pk_bf16_f32 v199, v62, v63
	v_cvt_pk_bf16_f32 v200, v64, v65
	v_cvt_pk_bf16_f32 v201, v66, v67
	v_mfma_f32_32x32x16_bf16 v[52:67], v[68:71], v[72:75], 0
	v_mfma_f32_32x32x16_bf16 v[52:67], v[80:83], v[84:87], v[52:67]
	s_nop 11
	v_cndmask_b32_e64 v2, v52, 0, vcc
	v_cndmask_b32_e64 v52, 0, v53, s[4:5]
	v_cndmask_b32_e64 v53, v54, 0, s[6:7]
	v_cndmask_b32_e64 v54, v55, 0, s[8:9]
	v_cndmask_b32_e64 v55, v56, 0, s[10:11]
	v_cndmask_b32_e64 v56, v57, 0, s[12:13]
	v_cndmask_b32_e64 v57, v58, 0, s[14:15]
	v_cndmask_b32_e64 v58, v59, 0, s[16:17]
	v_cndmask_b32_e64 v59, v60, 0, s[18:19]
	v_cndmask_b32_e64 v60, v61, 0, s[20:21]
	v_cndmask_b32_e64 v61, v62, 0, s[22:23]
	v_cndmask_b32_e64 v62, v63, 0, s[24:25]
	v_cndmask_b32_e64 v63, v64, 0, s[26:27]
	v_cndmask_b32_e64 v64, v65, 0, s[28:29]
	v_cndmask_b32_e64 v65, v66, 0, s[30:31]
	v_cndmask_b32_e64 v66, v67, 0, s[34:35]
	v_cvt_pk_bf16_f32 v202, v2, v52
	v_cvt_pk_bf16_f32 v203, v53, v54
	v_cvt_pk_bf16_f32 v204, v55, v56
	v_cvt_pk_bf16_f32 v205, v57, v58
	v_cvt_pk_bf16_f32 v206, v59, v60
	v_cvt_pk_bf16_f32 v207, v61, v62
	v_cvt_pk_bf16_f32 v208, v63, v64
	v_cvt_pk_bf16_f32 v209, v65, v66
	v_mfma_f32_32x32x16_bf16 v[52:67], v[202:205], v[100:103], 0
	v_mfma_f32_32x32x16_bf16 v[52:67], v[76:79], v[194:197], v[52:67]
	v_mfma_f32_32x32x16_bf16 v[36:51], v[88:91], v[108:111], v[36:51]
	v_mfma_f32_32x32x16_bf16 v[52:67], v[206:209], v[104:107], v[52:67]
	v_mfma_f32_32x32x16_bf16 v[36:51], v[92:95], v[112:115], v[36:51]
	v_mfma_f32_32x32x16_bf16 v[52:67], v[96:99], v[198:201], v[52:67]
	s_nop 11
	v_add_f32_e32 v2, v67, v51
	v_mov_b32 v2, v2
	s_nop 0
	v_or_b32_e32 v68, s68, v210
	v_lshl_add_u32 v68, v68, 1, v211
	ds_read_b128 v[194:197], v68 offset:17408
	ds_read_b128 v[198:201], v68 offset:8704
	v_add_u32_e32 v68, s69, v222
	v_add_u32_e32 v68, 0x2000, v68
	v_or_b32_e32 v2, s68, v193
	ds_read2_b64 v[202:205], v68 offset0:64 offset1:66
	v_or_b32_e32 v68, s70, v210
	v_mad_u32_u24 v2, v2, s86, v212
	v_lshl_add_u32 v68, v68, 1, v211
	ds_read_b128 v[206:209], v68 offset:17408
	ds_read_b128 v[210:213], v68 offset:8704
	ds_read_b128 v[214:217], v2 offset:26112
	ds_read_b128 v[218:221], v2 offset:26144
	v_add_u32_e32 v2, s71, v222
	v_add_u32_e32 v2, 0x2000, v2
	ds_read2_b64 v[222:225], v2 offset0:64 offset1:66
	v_or_b32_e32 v2, s72, v226
	v_add_u32_e32 v2, s62, v2
	ds_read_b128 v[68:71], v2 offset:41472
	ds_read_b128 v[72:75], v2 offset:41504
	ds_read_b128 v[76:79], v2 offset:44032
	ds_read_b128 v[80:83], v2 offset:44064
	ds_read_b128 v[84:87], v2 offset:41536
	ds_read_b128 v[88:91], v2 offset:41568
	ds_read_b128 v[92:95], v2 offset:44096
	ds_read_b128 v[96:99], v2 offset:44128
	s_waitcnt lgkmcnt(0)
; DI void h_chain(f32x16& S, f32x16& O, HPacks& K, const HOpsK& P, const bf16x8 (&vt)[2], const u32x4 (&vv)[2], int rq, int hh) {
;     f32x16 X;
;     { f32x16 Se;
; #pragma unroll
;       for (int g = 0; g < 4; ++g) {
; #pragma unroll
;           for (int e = 0; e < 4; ++e) Se[4 * g + e] = S[4 * g + e] * P.ebm[g][e]; }
;       K.sp0 = pack_step(Se, 0); K.sp1 = pack_step(Se, 1); }
; #pragma unroll
;     for (int g = 0; g < 4; ++g) {
; #pragma unroll
;         for (int e = 0; e < 4; ++e) S[4 * g + e] *= P.dec[g][e]; }
; #pragma unroll
;     for (int i = 0; i < 16; ++i) { X[i] = 0.f; O[i] = 0.f; }
;     __builtin_amdgcn_sched_barrier(0);
; #pragma unroll
;     for (int st = 0; st < 2; ++st) X = MFMA32(P.ka[st], P.qb[st], X);
; #pragma unroll
;     for (int i = 0; i < 16; ++i) X[i] = (crow(i, hh) <= rq) ? X[i] : 0.f;
;     K.xp0 = pack_step(X, 0); K.xp1 = pack_step(X, 1);
;     __builtin_amdgcn_sched_barrier(0);
;     O = MFMA32(K.xp0, __builtin_bit_cast(bf16x8, vv[0]), O);
;     O = MFMA32(__builtin_bit_cast(bf16x8, P.qq[0]), K.sp0, O);
;     O = MFMA32(K.xp1, __builtin_bit_cast(bf16x8, vv[1]), O);
;     O = MFMA32(__builtin_bit_cast(bf16x8, P.qq[1]), K.sp1, O);
; #pragma unroll
;     for (int st = 0; st < 2; ++st) S = MFMA32(P.ku[st], vt[st], S);
;     __builtin_amdgcn_sched_barrier(0);
; }
; DI void h_mma2(f32x16& S0, f32x16& S1, LAS unsigned char* buf, LAS unsigned char* red, int kbp, int vb, int r32, int hh) {
;     int rq = r32; asm volatile("" : "+v"(rq));
;     bf16x8 vt[2]; u32x4 vv[2];
; #pragma unroll
;     for (int st = 0; st < 2; ++st) {
;         vt[st] = *(const LAS bf16x8*)(buf + H_VT + (vb * 32 + r32) * 80 + (16 * st + 8 * hh) * 2);
;         const LAS unsigned char* vp = buf + H_VT + (vb * 32 + r32) * 80 + (16 * st + 4 * hh) * 2;
;         const u32x2 v0 = *(const LAS u32x2*)vp, v1 = *(const LAS u32x2*)(vp + 16);
;         vv[st].x = v0.x; vv[st].y = v0.y; vv[st].z = v1.x; vv[st].w = v1.y;
;     }
;     f32x16 Osum;
; #pragma unroll
;     for (int kk = 0; kk < 2; ++kk) {
;         HOpsK P; h_opsk_load(P, buf, 2 * kbp + kk, r32, hh);
;         f32x16& S = (kk == 0) ? S0 : S1; f32x16 O;
;         LDS_WAIT(); __builtin_amdgcn_sched_barrier(0);
;         HPacks K;
;         h_chain(S, O, K, P, vt, vv, rq, hh);
;         { float s_ = S[15] + O[15]; asm volatile("v_mov_b32 %0, %0" : "+v"(s_)); asm volatile("" :: "v"(s_)); }
	s_waitcnt lgkmcnt(5)
	v_mul_f32_e32 v77, v5, v77
	v_mul_f32_e32 v76, v4, v76
	v_mul_f32_e32 v79, v7, v79
	v_mul_f32_e32 v78, v6, v78
	s_waitcnt lgkmcnt(4)
	v_mul_f32_e32 v81, v9, v81
	v_mul_f32_e32 v80, v8, v80
	v_mul_f32_e32 v83, v11, v83
	v_mul_f32_e32 v82, v10, v82
	s_waitcnt lgkmcnt(1)
	v_mul_f32_e32 v93, v13, v93
	v_mul_f32_e32 v92, v12, v92
	v_mul_f32_e32 v95, v15, v95
	v_mul_f32_e32 v94, v14, v94
	s_waitcnt lgkmcnt(0)
	v_mul_f32_e32 v97, v17, v97
	v_mul_f32_e32 v96, v16, v96
	v_mul_f32_e32 v99, v19, v99
	v_mul_f32_e32 v98, v18, v98
	v_cvt_pk_bf16_f32 v226, v76, v77
	v_cvt_pk_bf16_f32 v227, v78, v79
	v_cvt_pk_bf16_f32 v228, v80, v81
	v_cvt_pk_bf16_f32 v229, v82, v83
	v_mul_f32_e32 v83, v19, v91
	v_mul_f32_e32 v82, v18, v90
	v_mul_f32_e32 v79, v15, v87
	v_mul_f32_e32 v78, v14, v86
	v_mul_f32_e32 v75, v11, v75
	v_mul_f32_e32 v74, v10, v74
	v_mul_f32_e32 v71, v7, v71
	v_mul_f32_e32 v70, v6, v70
	v_mul_f32_e32 v81, v17, v89
	v_mul_f32_e32 v80, v16, v88
	v_mul_f32_e32 v77, v13, v85
	v_mul_f32_e32 v76, v12, v84
	v_mul_f32_e32 v73, v9, v73
	v_mul_f32_e32 v72, v8, v72
	v_mul_f32_e32 v69, v5, v69
	v_mul_f32_e32 v68, v4, v68
	v_cvt_pk_bf16_f32 v230, v92, v93
	v_cvt_pk_bf16_f32 v231, v94, v95
	v_cvt_pk_bf16_f32 v232, v96, v97
	v_cvt_pk_bf16_f32 v233, v98, v99
	v_mfma_f32_32x32x16_bf16 v[84:99], v[194:197], v[198:201], 0
	v_mfma_f32_32x32x16_bf16 v[84:99], v[206:209], v[210:213], v[84:99]
	s_nop 11
	v_cndmask_b32_e64 v2, v84, 0, vcc
	v_cndmask_b32_e64 v84, 0, v85, s[4:5]
	v_cndmask_b32_e64 v85, v86, 0, s[6:7]
	v_cndmask_b32_e64 v86, v87, 0, s[8:9]
	v_cndmask_b32_e64 v87, v88, 0, s[10:11]
	v_cndmask_b32_e64 v88, v89, 0, s[12:13]
	v_cndmask_b32_e64 v89, v90, 0, s[14:15]
	v_cndmask_b32_e64 v90, v91, 0, s[16:17]
	v_cndmask_b32_e64 v91, v92, 0, s[18:19]
	v_cndmask_b32_e64 v92, v93, 0, s[20:21]
	v_cndmask_b32_e64 v93, v94, 0, s[22:23]
	v_cndmask_b32_e64 v94, v95, 0, s[24:25]
	v_cndmask_b32_e64 v95, v96, 0, s[26:27]
	v_cndmask_b32_e64 v96, v97, 0, s[28:29]
	v_cndmask_b32_e64 v97, v98, 0, s[30:31]
	v_cndmask_b32_e64 v98, v99, 0, s[34:35]
	v_cvt_pk_bf16_f32 v234, v2, v84
	v_cvt_pk_bf16_f32 v235, v85, v86
	v_cvt_pk_bf16_f32 v236, v87, v88
	v_cvt_pk_bf16_f32 v237, v89, v90
	v_cvt_pk_bf16_f32 v238, v91, v92
	v_cvt_pk_bf16_f32 v239, v93, v94
	v_cvt_pk_bf16_f32 v240, v95, v96
	v_cvt_pk_bf16_f32 v241, v97, v98
	v_mfma_f32_32x32x16_bf16 v[84:99], v[234:237], v[100:103], 0
	v_mfma_f32_32x32x16_bf16 v[84:99], v[202:205], v[226:229], v[84:99]
	v_mfma_f32_32x32x16_bf16 v[68:83], v[214:217], v[108:111], v[68:83]
	v_mfma_f32_32x32x16_bf16 v[84:99], v[238:241], v[104:107], v[84:99]
	v_mfma_f32_32x32x16_bf16 v[68:83], v[218:221], v[112:115], v[68:83]
	v_mfma_f32_32x32x16_bf16 v[84:99], v[222:225], v[230:233], v[84:99]
	s_nop 11
	v_add_f32_e32 v2, v99, v83
	v_mov_b32 v2, v2
	s_nop 0
	v_add_f32_e32 v2, v67, v99
	v_add_f32_e32 v66, v66, v98
	v_add_f32_e32 v65, v65, v97
	v_add_f32_e32 v64, v64, v96
	v_add_f32_e32 v63, v63, v95
	v_add_f32_e32 v62, v62, v94
	v_add_f32_e32 v61, v61, v93
	v_add_f32_e32 v60, v60, v92
	v_add_f32_e32 v59, v59, v91
	v_add_f32_e32 v58, v58, v90
	v_add_f32_e32 v57, v57, v89
	v_add_f32_e32 v56, v56, v88
	v_add_f32_e32 v55, v55, v87
	v_add_f32_e32 v54, v54, v86
	v_add_f32_e32 v53, v53, v85
	v_add_f32_e32 v52, v52, v84
	v_add_u32_e32 v67, 0x16800, v242
	ds_write2st64_b32 v67, v52, v53 offset1:1
	ds_write2st64_b32 v67, v54, v55 offset0:2 offset1:3
	ds_write2st64_b32 v67, v56, v57 offset0:8 offset1:9
	ds_write2st64_b32 v67, v58, v59 offset0:10 offset1:11
	ds_write2st64_b32 v67, v60, v61 offset0:16 offset1:17
	ds_write2st64_b32 v67, v62, v63 offset0:18 offset1:19
	ds_write2st64_b32 v67, v64, v65 offset0:24 offset1:25
	ds_write2st64_b32 v67, v66, v2 offset0:26 offset1:27
	s_mov_b64 s[4:5], 0

; #define LAS __attribute__((address_space(3)))
; DI unsigned pk2(float lo, float hi) { return cvtpk_s(lo, hi); }
; template <int SET> DI void h_prep8(const unsigned (&CR)[72], LAS unsigned char* buf, int tgp, int k2, int v64) {
;     float base0 = 0.f, base1 = 0.f, bm0 = 0.f, bm1 = 0.f, bl0 = 0.f, bl1 = 0.f;
; #pragma unroll
;     for (int g = 0; g < 4; ++g) { const f32x2_t tt = *(const LAS f32x2_t*)(buf + H_TOT + (g * 128 + 2 * k2) * 4);
;         if (g < tgp) { base0 += tt[0]; base1 += tt[1]; } if (g < 2) { bm0 += tt[0]; bm1 += tt[1]; } bl0 += tt[0]; bl1 += tt[1]; }
;     const float ebm0 = __expf(bm0), ebm1 = __expf(bm1), elm0 = __expf(bl0 - bm0), elm1 = __expf(bl1 - bm1);
;     float e20 = __expf(base0 - bm0), e21 = __expf(base1 - bm1); unsigned kup0[4], kup1[4];
; #pragma unroll
;     for (int jp = 0; jp < 4; ++jp) {
;         float ku0[2], ku1[2];
; #pragma unroll
;         for (int jj = 0; jj < 2; ++jj) {
;             const int j = 2 * jp + jj;
;             const unsigned fw = CR[24 * SET + 8 + j], qw = CR[24 * SET + j];
;             const float f0 = __expf(bflo(fw)), f1 = __expf(bfhi(fw)), q0 = bflo(qw), q1 = bfhi(qw);
;             e20 *= f0; e21 *= f1;
;             const float e30 = __builtin_amdgcn_rcpf(e20), e31 = __builtin_amdgcn_rcpf(e21);
;             const float kk0 = 1.0f - f0, kk1 = 1.0f - f1;
;             const int t = 8 * tgp + j;
;             *(LAS unsigned*)(buf + H_QS + t * 272 + 4 * k2) = pk2(q0 * e20, q1 * e21);
;             *(LAS unsigned*)(buf + H_KS + t * 272 + 4 * k2) = pk2(kk0 * e30, kk1 * e31);
;             ku0[jj] = kk0 * e30 * elm0; ku1[jj] = kk1 * e31 * elm1;
;         }
;         kup0[jp] = pk2(ku0[0], ku0[1]); kup1[jp] = pk2(ku1[0], ku1[1]);
;     }
;     { u32x4 w; w.x = kup0[0]; w.y = kup0[1]; w.z = kup0[2]; w.w = kup0[3]; *(LAS u32x4*)(buf + H_KU + (2 * k2) * 80 + 16 * tgp) = w;
; DI void h_reduce_store2(LAS unsigned char* red, bf16_t* op, int c, int pt) {
; #pragma unroll
;     for (int s2 = 0; s2 < 2; ++s2) {
;         const int s = pt + 256 * s2, t = s >> 4, c4 = s & 15;
;         const f32x4 a = *(const LAS f32x4*)(red + ((0 * 32 + t) * 64 + 4 * c4) * 4), b2 = *(const LAS f32x4*)(red + ((1 * 32 + t) * 64 + 4 * c4) * 4);
;         const f32x4 sm = a + b2;
;         u32x2 w; w.x = pk2(sm[0], sm[1]); w.y = pk2(sm[2], sm[3]);
;         *(u32x2*)(op + (size_t)(32 * c + t) * D + 4 * c4) = w;
;     }
; }
.LBB0_434:
	s_add_i32 s6, s38, 0x8000
	s_and_b32 s6, s6, 0x4000
	s_add_i32 s6, s6, 0
	s_add_i32 s8, s6, 0x16800
	s_lshl_b64 s[6:7], s[52:53], 1
	s_waitcnt lgkmcnt(0)
	s_add_u32 s4, s4, s6
	s_addc_u32 s5, s5, s7
	s_lshl_b32 s6, s96, 1
	v_lshlrev_b32_e32 v2, 2, v36
	s_add_u32 s4, s4, s6
	v_and_b32_e32 v2, 60, v2
	v_bfe_u32 v58, v36, 4, 4
	s_addc_u32 s5, s5, 0
	s_lshl_b32 s6, s48, 1
	v_lshlrev_b32_e32 v37, 2, v2
	v_lshlrev_b32_e32 v40, 8, v58
	s_add_u32 s4, s4, s6
	v_add3_u32 v37, s8, v37, v40
	s_addc_u32 s5, s5, 0
	v_lshlrev_b32_e32 v2, 1, v2
	ds_read_b128 v[40:43], v37
	ds_read_b128 v[44:47], v37 offset:8192
	v_lshl_add_u64 v[48:49], s[4:5], 0, v[2:3]
	v_lshl_add_u64 v[56:57], v[48:49], 0, s[50:51]
	ds_read_b128 v[48:51], v37 offset:4096
	ds_read_b128 v[52:55], v37 offset:12288
	v_lshl_add_u32 v37, v58, 11, s97
	s_waitcnt lgkmcnt(2)
	v_add_f32_e32 v43, v43, v47
	v_add_f32_e32 v42, v42, v46
	v_add_f32_e32 v41, v41, v45
	v_add_f32_e32 v40, v40, v44
	v_add_u32_e32 v2, 0x20000, v37
	v_cvt_pk_bf16_f32 v40, v40, v41
	v_cvt_pk_bf16_f32 v41, v42, v43
	v_lshl_add_u64 v[42:43], v[2:3], 1, v[56:57]
	s_andn2_b32 s4, 1, s39
	global_store_dwordx2 v[42:43], v[40:41], off
	s_waitcnt lgkmcnt(0)
	v_add_f32_e32 v41, v51, v55
	v_add_f32_e32 v40, v50, v54
	s_mul_i32 s4, s4, 0xb400
	v_cvt_pk_bf16_f32 v47, v40, v41
	s_add_i32 s8, s4, 0
	v_lshlrev_b32_e32 v40, 3, v38
	v_add_f32_e32 v43, v49, v53
	v_add_f32_e32 v42, v48, v52
	v_add_u32_e32 v41, s8, v40
	v_cvt_pk_bf16_f32 v46, v42, v43
	ds_read2st64_b64 v[42:45], v41 offset0:82 offset1:83
	v_add_u32_e32 v2, 0x28000, v37
	v_lshl_add_u64 v[48:49], v[2:3], 1, v[56:57]
	global_store_dwordx2 v[48:49], v[46:47], off
	ds_read2st64_b64 v[46:49], v41 offset0:84 offset1:85
	s_waitcnt lgkmcnt(1)
	v_add_f32_e32 v2, 0, v42
	v_cmp_lt_u32_sdwa s[4:5], v36, v120 src0_sel:BYTE_0 src1_sel:DWORD
	v_add_f32_e32 v37, 0, v43
	v_cmp_gt_u32_sdwa vcc, v36, s88 src0_sel:BYTE_0 src1_sel:DWORD
	v_cndmask_b32_e64 v43, v2, 0, s[4:5]
	v_cndmask_b32_e64 v42, v37, 0, s[4:5]
	v_add_f32_e32 v50, v44, v43
	v_bfe_u32 v39, v36, 6, 2
	v_add_f32_e32 v51, v45, v42
	v_cndmask_b32_e32 v43, v43, v50, vcc
	v_cndmask_b32_e32 v36, v42, v51, vcc
	v_add_f32_e32 v42, v2, v44
	s_waitcnt lgkmcnt(0)
	v_add_f32_e32 v2, v46, v43
	v_cmp_eq_u32_e32 vcc, 3, v39
	v_add_f32_e32 v37, v37, v45
	v_add_f32_e32 v44, v47, v36
	v_cndmask_b32_e32 v43, v43, v2, vcc
	v_add_f32_e32 v2, v42, v46
	v_add_f32_e32 v2, v2, v48
	v_cndmask_b32_e32 v45, v36, v44, vcc
	v_add_f32_e32 v36, v37, v47
	v_sub_f32_e32 v2, v2, v42
	v_sub_f32_e32 v43, v43, v42
	v_add_f32_e32 v44, v36, v49
	v_mul_f32_e32 v2, 0x3fb8aa3b, v2
	v_mul_f32_e32 v43, 0x3fb8aa3b, v43
	v_exp_f32_e32 v36, v2
	v_sub_f32_e32 v2, v44, v37
	v_exp_f32_e32 v44, v43
	v_sub_f32_e32 v43, v45, v37
	v_mul_f32_e32 v43, 0x3fb8aa3b, v43
	v_exp_f32_e32 v45, v43
	v_lshlrev_b32_e32 v43, 16, v121
	v_mul_f32_e32 v43, 0x3fb8aa3b, v43
	v_exp_f32_e32 v46, v43
	v_and_b32_e32 v43, 0xffff0000, v121
	v_mul_f32_e32 v43, 0x3fb8aa3b, v43
	v_exp_f32_e32 v47, v43
	s_waitcnt vmcnt(54)
	v_lshlrev_b32_e32 v48, 16, v142
	v_and_b32_e32 v49, 0xffff0000, v142
	v_lshlrev_b32_e32 v43, 2, v38
	v_mul_f32_e32 v45, v47, v45
	v_mul_f32_e32 v44, v46, v44
	v_mul_f32_e32 v2, 0x3fb8aa3b, v2
	v_mul_f32_e32 v49, v45, v49
	v_mul_f32_e32 v48, v44, v48
	v_rcp_f32_e32 v50, v44
	v_cvt_pk_bf16_f32 v54, v48, v49
	v_mul_u32_u24_e32 v48, 0x880, v39
	v_add3_u32 v43, s8, v43, v48
	v_lshlrev_b32_e32 v48, 16, v122
	v_and_b32_e32 v49, 0xffff0000, v122
	v_mul_f32_e32 v48, 0x3fb8aa3b, v48
	v_mul_f32_e32 v49, 0x3fb8aa3b, v49
	v_exp_f32_e32 v48, v48
	v_exp_f32_e32 v49, v49
	v_rcp_f32_e32 v51, v45
	v_exp_f32_e32 v2, v2
	v_sub_f32_e32 v47, 1.0, v47
	v_sub_f32_e32 v46, 1.0, v46
	v_mul_f32_e32 v53, v49, v45
	v_mul_f32_e32 v52, v48, v44
	v_sub_f32_e32 v49, 1.0, v49
	v_sub_f32_e32 v48, 1.0, v48
	v_rcp_f32_e32 v44, v52
	v_rcp_f32_e32 v45, v53
	v_mul_f32_e32 v47, v47, v51
	v_mul_f32_e32 v46, v46, v50
	v_lshlrev_b32_e32 v50, 16, v124
	v_cvt_pk_bf16_f32 v55, v46, v47
	v_mul_f32_e32 v45, v49, v45
	v_mul_f32_e32 v44, v48, v44
	v_and_b32_e32 v51, 0xffff0000, v124
	v_cvt_pk_bf16_f32 v48, v44, v45
	v_add_u32_e32 v58, 0x4400, v43
	v_mov_b32_e32 v49, v44
	v_mov_b32_e32 v44, v47
	v_mul_f32_e32 v51, v53, v51
	v_mul_f32_e32 v50, v52, v50
	ds_write2_b32 v58, v55, v48 offset1:68
	v_mov_b32_e32 v48, v46
	v_mul_f32_e32 v47, v2, v45
	v_mul_f32_e32 v46, v2, v44
	v_lshlrev_b32_e32 v45, 16, v133
	v_cvt_pk_bf16_f32 v50, v50, v51
	v_add_u32_e32 v51, 0x2000, v43
	v_mul_f32_e32 v45, 0x3fb8aa3b, v45
	ds_write2_b32 v51, v54, v50 offset0:128 offset1:196
	v_exp_f32_e32 v50, v45
	v_and_b32_e32 v45, 0xffff0000, v133
	v_mul_f32_e32 v45, 0x3fb8aa3b, v45
	v_exp_f32_e32 v51, v45
	v_mul_f32_e32 v49, v36, v49
	v_mul_f32_e32 v48, v36, v48
	v_cvt_pk_bf16_f32 v44, v48, v49
	v_cvt_pk_bf16_f32 v48, v46, v47
	v_lshlrev_b32_e32 v46, 16, v123
	v_and_b32_e32 v47, 0xffff0000, v123
	v_mul_f32_e32 v53, v51, v53
	v_mul_f32_e32 v52, v50, v52
	v_lshlrev_b32_e32 v49, 16, v144
	v_mul_f32_e32 v47, v53, v47
	v_mul_f32_e32 v46, v52, v46
	v_mul_f32_e32 v49, 0x3fb8aa3b, v49
	v_cvt_pk_bf16_f32 v45, v46, v47
	v_sub_f32_e32 v47, 1.0, v51
	v_sub_f32_e32 v46, 1.0, v50
	v_exp_f32_e32 v50, v49
	v_and_b32_e32 v49, 0xffff0000, v144
	v_mul_f32_e32 v49, 0x3fb8aa3b, v49
	v_exp_f32_e32 v51, v49
	v_rcp_f32_e32 v54, v52
	v_rcp_f32_e32 v55, v53
	v_add_u32_e32 v59, 0x2400, v43
	v_mul_f32_e32 v53, v51, v53
	v_mul_f32_e32 v52, v50, v52
	v_sub_f32_e32 v51, 1.0, v51
	v_sub_f32_e32 v50, 1.0, v50
	v_rcp_f32_e32 v56, v52
	v_rcp_f32_e32 v57, v53
	v_mul_f32_e32 v47, v47, v55
	v_mul_f32_e32 v46, v46, v54
	v_lshlrev_b32_e32 v54, 16, v143
	v_and_b32_e32 v55, 0xffff0000, v143
; #define LAS __attribute__((address_space(3)))
; DI unsigned pk2(float lo, float hi) { return cvtpk_s(lo, hi); }
; template <int SET> DI void h_totals8(const unsigned (&CR)[72], LAS unsigned char* buf, int tgp, int k2) {
;     float lo = 0.f, hi = 0.f;
; #pragma unroll
;     for (int j = 0; j < 8; ++j) { lo += bflo(CR[24 * SET + 8 + j]); hi += bfhi(CR[24 * SET + 8 + j]); }
;     *(LAS f32x2_t*)(buf + H_TOT + (tgp * 128 + 2 * k2) * 4) = (f32x2_t){lo, hi};
; }
; template <int SET> DI void h_prep8(const unsigned (&CR)[72], LAS unsigned char* buf, int tgp, int k2, int v64) {
;     ...
;     float e20 = __expf(base0 - bm0), e21 = __expf(base1 - bm1); unsigned kup0[4], kup1[4];
; #pragma unroll
;     for (int jp = 0; jp < 4; ++jp) {
;         float ku0[2], ku1[2];
; #pragma unroll
;         for (int jj = 0; jj < 2; ++jj) {
;             const int j = 2 * jp + jj;
;             const unsigned fw = CR[24 * SET + 8 + j], qw = CR[24 * SET + j];
;             const float f0 = __expf(bflo(fw)), f1 = __expf(bfhi(fw)), q0 = bflo(qw), q1 = bfhi(qw);
;             e20 *= f0; e21 *= f1;
;             const float e30 = __builtin_amdgcn_rcpf(e20), e31 = __builtin_amdgcn_rcpf(e21);
;             const float kk0 = 1.0f - f0, kk1 = 1.0f - f1;
;             const int t = 8 * tgp + j;
;             *(LAS unsigned*)(buf + H_QS + t * 272 + 4 * k2) = pk2(q0 * e20, q1 * e21);
;             *(LAS unsigned*)(buf + H_KS + t * 272 + 4 * k2) = pk2(kk0 * e30, kk1 * e31);
;             ku0[jj] = kk0 * e30 * elm0; ku1[jj] = kk1 * e31 * elm1;
;         }
;         kup0[jp] = pk2(ku0[0], ku0[1]); kup1[jp] = pk2(ku1[0], ku1[1]);
;     }
;     { u32x4 w; w.x = kup0[0]; w.y = kup0[1]; w.z = kup0[2]; w.w = kup0[3]; *(LAS u32x4*)(buf + H_KU + (2 * k2) * 80 + 16 * tgp) = w;
;       w.x = kup1[0]; w.y = kup1[1]; w.z = kup1[2]; w.w = kup1[3]; *(LAS u32x4*)(buf + H_KU + (2 * k2 + 1) * 80 + 16 * tgp) = w; }
;     if (tgp == 0) { *(LAS f32x2_t*)(buf + H_DEC + 8 * k2) = (f32x2_t){ebm0 * elm0, ebm1 * elm1}; *(LAS f32x2_t*)(buf + H_EBM + 8 * k2) = (f32x2_t){ebm0, ebm1}; }
;     { u32x4 w; w.x = (CR[24 * SET + 16] & 0xffffu) | (CR[24 * SET + 17] << 16); w.y = (CR[24 * SET + 18] & 0xffffu) | (CR[24 * SET + 19] << 16);
;       w.z = (CR[24 * SET + 20] & 0xffffu) | (CR[24 * SET + 21] << 16); w.w = (CR[24 * SET + 22] & 0xffffu) | (CR[24 * SET + 23] << 16);
;       *(LAS u32x4*)(buf + H_VT + v64 * 80 + 16 * tgp) = w; }
; }
	v_mul_f32_e32 v55, v53, v55
	v_mul_f32_e32 v54, v52, v54
	v_mul_f32_e32 v51, v51, v57
	v_mul_f32_e32 v50, v50, v56
	v_cvt_pk_bf16_f32 v54, v54, v55
	v_cvt_pk_bf16_f32 v49, v46, v47
	ds_write2_b32 v59, v45, v54 offset0:8 offset1:76
	v_cvt_pk_bf16_f32 v45, v50, v51
	ds_write2_b32 v58, v49, v45 offset0:136 offset1:204
	v_lshlrev_b32_e32 v49, 16, v150
	v_mov_b32_e32 v55, v50
	v_mov_b32_e32 v50, v47
	v_mul_f32_e32 v49, 0x3fb8aa3b, v49
	v_mov_b32_e32 v54, v46
	v_mul_f32_e32 v47, v2, v51
	v_mul_f32_e32 v46, v2, v50
	v_exp_f32_e32 v50, v49
	v_and_b32_e32 v49, 0xffff0000, v150
	v_mul_f32_e32 v49, 0x3fb8aa3b, v49
	v_exp_f32_e32 v51, v49
	v_cvt_pk_bf16_f32 v49, v46, v47
	v_lshlrev_b32_e32 v46, 16, v145
	v_and_b32_e32 v47, 0xffff0000, v145
	v_mul_f32_e32 v53, v51, v53
	v_mul_f32_e32 v52, v50, v52
	v_mul_f32_e32 v55, v36, v55
	v_mul_f32_e32 v54, v36, v54
	v_mul_f32_e32 v47, v53, v47
	v_mul_f32_e32 v46, v52, v46
	v_cvt_pk_bf16_f32 v45, v54, v55
	v_cvt_pk_bf16_f32 v58, v46, v47
	v_sub_f32_e32 v47, 1.0, v51
	v_sub_f32_e32 v46, 1.0, v50
	v_lshlrev_b32_e32 v50, 16, v164
	v_and_b32_e32 v51, 0xffff0000, v164
	v_mul_f32_e32 v50, 0x3fb8aa3b, v50
	v_mul_f32_e32 v51, 0x3fb8aa3b, v51
	v_exp_f32_e32 v50, v50
	v_exp_f32_e32 v51, v51
	v_rcp_f32_e32 v54, v52
	v_rcp_f32_e32 v55, v53
	v_add_u32_e32 v62, 0x4800, v43
	v_mul_f32_e32 v53, v51, v53
	v_mul_f32_e32 v52, v50, v52
	v_sub_f32_e32 v51, 1.0, v51
	v_sub_f32_e32 v50, 1.0, v50
	v_rcp_f32_e32 v56, v52
	v_rcp_f32_e32 v57, v53
	v_mul_f32_e32 v47, v47, v55
	v_mul_f32_e32 v46, v46, v54
	v_lshlrev_b32_e32 v54, 16, v159
	v_and_b32_e32 v55, 0xffff0000, v159
	v_mul_f32_e32 v55, v53, v55
	v_mul_f32_e32 v54, v52, v54
	v_mul_f32_e32 v51, v51, v57
	v_mul_f32_e32 v50, v50, v56
	v_cvt_pk_bf16_f32 v54, v54, v55
	v_cvt_pk_bf16_f32 v60, v46, v47
	ds_write2_b32 v59, v58, v54 offset0:144 offset1:212
	v_cvt_pk_bf16_f32 v54, v50, v51
	ds_write2_b32 v62, v60, v54 offset0:16 offset1:84
	v_mov_b32_e32 v54, v46
	v_mov_b32_e32 v55, v50
	v_mov_b32_e32 v50, v47
	v_lshlrev_b32_e32 v47, 16, v171
	v_mul_f32_e32 v55, v36, v55
	v_mul_f32_e32 v54, v36, v54
	v_mul_f32_e32 v47, 0x3fb8aa3b, v47
	v_cvt_pk_bf16_f32 v46, v54, v55
	v_exp_f32_e32 v54, v47
	v_and_b32_e32 v47, 0xffff0000, v171
	v_mul_f32_e32 v47, 0x3fb8aa3b, v47
	v_exp_f32_e32 v55, v47
	v_mul_f32_e32 v51, v2, v51
	v_mul_f32_e32 v50, v2, v50
	v_cvt_pk_bf16_f32 v50, v50, v51
	s_waitcnt vmcnt(50)
	v_lshlrev_b32_e32 v56, 16, v184
	v_and_b32_e32 v57, 0xffff0000, v184
	v_mul_f32_e32 v53, v55, v53
	v_mul_f32_e32 v52, v54, v52
	v_lshlrev_b32_e32 v51, 16, v174
	v_mul_f32_e32 v57, v53, v57
	v_mul_f32_e32 v56, v52, v56
	v_mul_f32_e32 v51, 0x3fb8aa3b, v51
	v_cvt_pk_bf16_f32 v47, v56, v57
	v_exp_f32_e32 v56, v51
	v_and_b32_e32 v51, 0xffff0000, v174
	v_mul_f32_e32 v51, 0x3fb8aa3b, v51
	v_exp_f32_e32 v57, v51
	v_rcp_f32_e32 v58, v52
	v_rcp_f32_e32 v59, v53
	v_sub_f32_e32 v55, 1.0, v55
	v_sub_f32_e32 v54, 1.0, v54
	v_mul_f32_e32 v53, v57, v53
	v_mul_f32_e32 v52, v56, v52
	v_add_u32_e32 v43, 0x2800, v43
	v_mul_f32_e32 v55, v55, v59
	v_mul_f32_e32 v54, v54, v58
	v_lshlrev_b32_e32 v58, 16, v177
	v_and_b32_e32 v59, 0xffff0000, v177
	v_rcp_f32_e32 v60, v52
	v_rcp_f32_e32 v61, v53
	v_mul_f32_e32 v53, v53, v59
	v_mul_f32_e32 v52, v52, v58
	v_cvt_pk_bf16_f32 v51, v54, v55
	v_cvt_pk_bf16_f32 v52, v52, v53
	ds_write2_b32 v43, v47, v52 offset0:24 offset1:92
	v_sub_f32_e32 v53, 1.0, v57
	v_sub_f32_e32 v52, 1.0, v56
	v_mov_b32_e32 v56, v54
	v_mul_f32_e32 v53, v53, v61
	v_mul_f32_e32 v52, v52, v60
	s_nop 0
	v_cvt_pk_bf16_f32 v43, v52, v53
	v_mov_b32_e32 v57, v52
	v_mov_b32_e32 v52, v55
	v_mul_f32_e32 v53, v2, v53
	v_mul_f32_e32 v52, v2, v52
	ds_write2_b32 v62, v51, v43 offset0:152 offset1:220
	v_mul_f32_e32 v57, v36, v57
	v_mul_f32_e32 v56, v36, v56
	v_cvt_pk_bf16_f32 v51, v52, v53
	v_mul_u32_u24_e32 v52, 0xa0, v38
	v_lshlrev_b32_e32 v43, 4, v39
	v_cvt_pk_bf16_f32 v47, v56, v57
	v_add3_u32 v52, s8, v52, v43
	ds_write_b128 v52, v[44:47] offset:26112
	ds_write_b128 v52, v[48:51] offset:26192
	s_and_saveexec_b64 s[6:7], s[4:5]
	s_cbranch_execz .LBB0_436
	v_mul_f32_e32 v42, 0x3fb8aa3b, v42
	v_mul_f32_e32 v37, 0x3fb8aa3b, v37
	v_exp_f32_e32 v44, v42
	v_exp_f32_e32 v45, v37
	v_mov_b32_e32 v37, v2
	v_mul_f32_e32 v37, v45, v37
	v_mul_f32_e32 v36, v44, v36
	ds_write2st64_b64 v41, v[36:37], v[44:45] offset0:81 offset1:86
.LBB0_436:
	s_or_b64 exec, exec, s[6:7]
	v_mul_u32_u24_e32 v2, 0x50, v38
	v_lshl_add_u32 v44, v185, 16, v189
	v_lshl_add_u32 v45, v186, 16, v188
	v_lshl_add_u32 v46, v192, 16, v191
	v_lshl_add_u32 v47, v187, 16, v190
	v_add3_u32 v2, s8, v2, v43
	s_cmp_gt_u32 s39, 59
	ds_write_b128 v2, v[44:47] offset:36352
	s_cbranch_scc1 .LBB0_439
	s_waitcnt vmcnt(45)
	v_lshlrev_b32_e32 v36, 16, v130
	v_and_b32_e32 v37, 0xffff0000, v130
	s_waitcnt vmcnt(44)
	v_lshlrev_b32_e32 v42, 16, v132
	v_and_b32_e32 v43, 0xffff0000, v132
	v_add_f32_e32 v37, 0, v37
	v_add_f32_e32 v36, 0, v36
	s_waitcnt vmcnt(35)
	v_lshlrev_b32_e32 v44, 16, v141
	v_and_b32_e32 v45, 0xffff0000, v141
	v_add_f32_e32 v37, v37, v43
	v_add_f32_e32 v36, v36, v42
	s_waitcnt vmcnt(34)
	v_lshlrev_b32_e32 v46, 16, v158
	v_and_b32_e32 v47, 0xffff0000, v158
	v_add_f32_e32 v37, v37, v45
	v_add_f32_e32 v36, v36, v44
	v_lshlrev_b32_e32 v48, 16, v156
	v_and_b32_e32 v49, 0xffff0000, v156
	v_add_f32_e32 v37, v37, v47
	v_add_f32_e32 v36, v36, v46
	s_bitcmp1_b32 s39, 0
	v_lshlrev_b32_e32 v50, 16, v168
	v_and_b32_e32 v51, 0xffff0000, v168
	v_add_f32_e32 v37, v37, v49
	v_add_f32_e32 v36, v36, v48
	s_cselect_b32 s4, 0xb400, 0
	s_waitcnt vmcnt(29)
	v_lshlrev_b32_e32 v52, 16, v173
	v_and_b32_e32 v53, 0xffff0000, v173
	v_add_f32_e32 v37, v37, v51
	v_add_f32_e32 v36, v36, v50
	s_add_i32 s4, s4, 0
	s_waitcnt vmcnt(28)
	v_lshlrev_b32_e32 v54, 16, v176
	v_and_b32_e32 v55, 0xffff0000, v176
	v_add_f32_e32 v37, v37, v53
	v_add_f32_e32 v36, v36, v52
	v_lshlrev_b32_e32 v2, 9, v39
	v_add_f32_e32 v37, v37, v55
	v_add_f32_e32 v36, v36, v54
	v_add3_u32 v2, s4, v2, v40
	ds_write_b64 v2, v[36:37] offset:41984
	s_branch .LBB0_439

; DI int crow(int reg, int h) { return (reg & 3) + 8 * (reg >> 2) + 4 * h; }
; #define MFMA32(a, b, c) __builtin_amdgcn_mfma_f32_32x32x16_bf16((a), (b), (c), 0, 0, 0)
; #define HSTEP2(cc, RF, RN, RNN) do { if (prep) h_prep_step<RF, RN, RNN>(CR, A, lds, (cc), rb, h, vhalf); else h_mma_step(S0, S1, lds, (cc), F.wave); __syncthreads(); } while (0)
; DI void h_chain(f32x16& S, f32x16& O, HPacks& K, const HOpsK& P, const bf16x8 (&vt)[2], const u32x4 (&vv)[2], int rq, int hh) {
;     f32x16 X;
;     { f32x16 Se;
; #pragma unroll
;       for (int g = 0; g < 4; ++g) {
; #pragma unroll
;           for (int e = 0; e < 4; ++e) Se[4 * g + e] = S[4 * g + e] * P.ebm[g][e]; }
;       K.sp0 = pack_step(Se, 0); K.sp1 = pack_step(Se, 1); }
; #pragma unroll
;     for (int g = 0; g < 4; ++g) {
; #pragma unroll
;         for (int e = 0; e < 4; ++e) S[4 * g + e] *= P.dec[g][e]; }
; #pragma unroll
;     for (int i = 0; i < 16; ++i) { X[i] = 0.f; O[i] = 0.f; }
;     __builtin_amdgcn_sched_barrier(0);
; #pragma unroll
;     for (int st = 0; st < 2; ++st) X = MFMA32(P.ka[st], P.qb[st], X);
; #pragma unroll
;     for (int i = 0; i < 16; ++i) X[i] = (crow(i, hh) <= rq) ? X[i] : 0.f;
;     K.xp0 = pack_step(X, 0); K.xp1 = pack_step(X, 1);
;     __builtin_amdgcn_sched_barrier(0);
;     O = MFMA32(K.xp0, __builtin_bit_cast(bf16x8, vv[0]), O);
;     O = MFMA32(__builtin_bit_cast(bf16x8, P.qq[0]), K.sp0, O);
;     O = MFMA32(K.xp1, __builtin_bit_cast(bf16x8, vv[1]), O);
;     O = MFMA32(__builtin_bit_cast(bf16x8, P.qq[1]), K.sp1, O);
; #pragma unroll
;     for (int st = 0; st < 2; ++st) S = MFMA32(P.ku[st], vt[st], S);
;     __builtin_amdgcn_sched_barrier(0);
; }
; DI void p2_hgrn_roles(Frame& F, ArgsP A) {
;     ...
;         for (int c = 0; c < 63; c += 3) { HSTEP2(c, 0, 1, 2); HSTEP2(c + 1, 1, 2, 0); HSTEP2(c + 2, 2, 0, 1); }
;         HSTEP2(63, 0, 1, 2);
.LBB0_439:
	s_add_i32 s4, s39, 3
	s_add_u32 s56, s56, 0x60000
	s_addc_u32 s57, s57, 0
	s_add_i32 s97, s97, 0x30000
	s_add_i32 s38, s38, 0xc000
	s_cmp_gt_u32 s39, 59
	s_waitcnt lgkmcnt(0)
	s_barrier
	s_cbranch_scc0 .LBB0_412
	s_mov_b64 s[4:5], -1
	s_and_b64 vcc, exec, s[42:43]
	s_cbranch_vccz .LBB0_442
	v_mov_b32_e32 v2, v0
	v_mov_b32_e32 v38, s89
	v_and_b32_e32 v121, 31, v2
	v_bfe_u32 v2, v2, 5, 1
	v_or_b32_e32 v37, s3, v121
	v_mad_u32_u24 v37, v37, s86, v38
	s_waitcnt vmcnt(46)
	v_lshlrev_b32_e32 v128, 4, v2
	s_waitcnt vmcnt(19)
	v_lshlrev_b32_e32 v129, 3, v2
	v_mov_b32_e32 v36, v121
	v_add_u32_e32 v38, v37, v128
	v_add_u32_e32 v37, v37, v129
	ds_read2_b64 v[52:55], v37 offset1:2
	ds_read2_b64 v[56:59], v37 offset0:4 offset1:6
	ds_read_b128 v[60:63], v38
	ds_read_b128 v[64:67], v38 offset:32
	v_lshlrev_b32_e32 v37, 2, v2
	v_or_b32_e32 v38, 2, v37
	v_cmp_gt_i32_e64 s[6:7], v38, v36
	v_or_b32_e32 v38, 3, v37
	v_cmp_gt_i32_e64 s[8:9], v38, v36
	v_or_b32_e32 v38, 8, v37
	v_cmp_gt_i32_e64 s[10:11], v38, v36
	v_or_b32_e32 v38, 9, v37
	v_cmp_gt_i32_e64 s[12:13], v38, v36
	v_or_b32_e32 v38, 10, v37
	v_cmp_gt_i32_e64 s[14:15], v38, v36
	v_or_b32_e32 v38, 11, v37
	v_cmp_gt_i32_e64 s[16:17], v38, v36
	v_or_b32_e32 v38, 16, v37
	v_cmp_gt_i32_e64 s[18:19], v38, v36
	v_or_b32_e32 v38, 17, v37
	v_cmp_gt_i32_e64 s[20:21], v38, v36
	v_or_b32_e32 v38, 18, v37
	v_cmp_gt_i32_e64 s[22:23], v38, v36
	v_or_b32_e32 v38, 19, v37
	v_cmp_gt_i32_e64 s[24:25], v38, v36
	v_or_b32_e32 v38, 24, v37
	v_cmp_gt_i32_e64 s[26:27], v38, v36
	v_or_b32_e32 v38, 25, v37
	v_cmp_gt_i32_e32 vcc, v37, v36
	v_cmp_lt_i32_e64 s[4:5], v37, v36
	v_cmp_gt_i32_e64 s[28:29], v38, v36
	v_or_b32_e32 v38, 26, v37
	v_or_b32_e32 v37, 27, v37
	v_mad_u32_u24 v130, v121, s87, 0
	v_cmp_gt_i32_e64 s[34:35], v37, v36
	v_or_b32_e32 v37, s63, v129
	s_waitcnt vmcnt(18)
	v_add_u32_e32 v131, v130, v129
	v_lshl_add_u32 v37, v37, 1, v130
	ds_read_b128 v[68:71], v37 offset:63488
	ds_read_b128 v[72:75], v37 offset:54784
	v_add_u32_e32 v37, s64, v131
	v_add_u32_e32 v37, 0xd000, v37
	v_add_u32_e32 v132, s90, v128
	v_cmp_gt_i32_e64 s[30:31], v38, v36
	v_or_b32_e32 v36, s63, v121
	ds_read2_b64 v[76:79], v37 offset0:192 offset1:194
	v_or_b32_e32 v37, s65, v129
	v_mad_u32_u24 v36, v36, s86, v132
	v_lshl_add_u32 v37, v37, 1, v130
	ds_read_b128 v[80:83], v37 offset:63488
	ds_read_b128 v[84:87], v37 offset:54784
	ds_read_b128 v[88:91], v36
	ds_read_b128 v[92:95], v36 offset:32
	v_add_u32_e32 v36, s66, v131
	v_add_u32_e32 v36, 0xd000, v36
	v_or_b32_e32 v108, s67, v128
	ds_read2_b64 v[96:99], v36 offset0:192 offset1:194
	v_add_u32_e32 v36, s91, v108
	v_add_u32_e32 v40, s92, v108
	v_or_b32_e32 v44, 32, v108
	v_or_b32_e32 v48, 64, v108
	v_or_b32_e32 v108, 0x60, v108
	v_add_u32_e32 v45, s91, v44
	v_add_u32_e32 v44, s92, v44
	v_add_u32_e32 v49, s91, v48
	v_add_u32_e32 v48, s92, v48
	v_add_u32_e32 v109, s91, v108
	v_add_u32_e32 v112, s92, v108
	ds_read_b128 v[36:39], v36
	ds_read_b128 v[40:43], v40
	ds_read_b128 v[100:103], v45
	ds_read_b128 v[44:47], v44
	ds_read_b128 v[104:107], v49
	ds_read_b128 v[48:51], v48
	ds_read_b128 v[108:111], v109
	ds_read_b128 v[112:115], v112
	s_waitcnt lgkmcnt(0)
	s_waitcnt lgkmcnt(6)
	v_mul_f32_e32 v41, v21, v41
	v_mul_f32_e32 v40, v20, v40
	v_mul_f32_e32 v43, v23, v43
	v_mul_f32_e32 v42, v22, v42
	s_waitcnt lgkmcnt(4)
	v_mul_f32_e32 v45, v25, v45
	v_mul_f32_e32 v44, v24, v44
	v_mul_f32_e32 v47, v27, v47
	v_mul_f32_e32 v46, v26, v46
	s_waitcnt lgkmcnt(2)
	v_mul_f32_e32 v49, v29, v49
	v_mul_f32_e32 v48, v28, v48
	v_mul_f32_e32 v51, v31, v51
	v_mul_f32_e32 v50, v30, v50
	s_waitcnt lgkmcnt(0)
	v_mul_f32_e32 v117, v33, v113
	v_mul_f32_e32 v116, v32, v112
	v_mul_f32_e32 v127, v35, v115
	v_mul_f32_e32 v126, v34, v114
	v_cvt_pk_bf16_f32 v112, v40, v41
	v_cvt_pk_bf16_f32 v113, v42, v43
	v_cvt_pk_bf16_f32 v114, v44, v45
	v_cvt_pk_bf16_f32 v115, v46, v47
	v_cvt_pk_bf16_f32 v122, v48, v49
	v_cvt_pk_bf16_f32 v123, v50, v51
	v_cvt_pk_bf16_f32 v124, v116, v117
	v_cvt_pk_bf16_f32 v125, v126, v127
	v_mul_f32_e32 v39, v23, v39
	v_mul_f32_e32 v38, v22, v38
	v_mul_f32_e32 v51, v35, v111
	v_mul_f32_e32 v50, v34, v110
	v_mul_f32_e32 v47, v31, v107
	v_mul_f32_e32 v46, v30, v106
	v_mul_f32_e32 v43, v27, v103
	v_mul_f32_e32 v42, v26, v102
	v_mul_f32_e32 v37, v21, v37
	v_mul_f32_e32 v36, v20, v36
	v_mul_f32_e32 v49, v33, v109
	v_mul_f32_e32 v48, v32, v108
	v_mul_f32_e32 v45, v29, v105
	v_mul_f32_e32 v44, v28, v104
	v_mul_f32_e32 v41, v25, v101
	v_mul_f32_e32 v40, v24, v100
	v_mfma_f32_32x32x16_bf16 v[20:35], v[68:71], v[72:75], 0
	v_mfma_f32_32x32x16_bf16 v[20:35], v[80:83], v[84:87], v[20:35]
	s_nop 11
	v_cndmask_b32_e64 v20, v20, 0, vcc
	v_cndmask_b32_e64 v21, 0, v21, s[4:5]
	v_cndmask_b32_e64 v22, v22, 0, s[6:7]
	v_cndmask_b32_e64 v23, v23, 0, s[8:9]
	v_cndmask_b32_e64 v24, v24, 0, s[10:11]
	v_cndmask_b32_e64 v25, v25, 0, s[12:13]
	v_cndmask_b32_e64 v26, v26, 0, s[14:15]
	v_cndmask_b32_e64 v27, v27, 0, s[16:17]
	v_cndmask_b32_e64 v28, v28, 0, s[18:19]
	v_cndmask_b32_e64 v29, v29, 0, s[20:21]
	v_cndmask_b32_e64 v30, v30, 0, s[22:23]
	v_cndmask_b32_e64 v31, v31, 0, s[24:25]
	v_cndmask_b32_e64 v32, v32, 0, s[26:27]
	v_cndmask_b32_e64 v33, v33, 0, s[28:29]
	v_cndmask_b32_e64 v34, v34, 0, s[30:31]
	v_cndmask_b32_e64 v35, v35, 0, s[34:35]
	v_cvt_pk_bf16_f32 v100, v20, v21
	v_cvt_pk_bf16_f32 v101, v22, v23
	v_cvt_pk_bf16_f32 v102, v24, v25
	v_cvt_pk_bf16_f32 v103, v26, v27
	v_cvt_pk_bf16_f32 v104, v28, v29
	v_cvt_pk_bf16_f32 v105, v30, v31
	v_cvt_pk_bf16_f32 v106, v32, v33
	v_cvt_pk_bf16_f32 v107, v34, v35
	v_mfma_f32_32x32x16_bf16 v[20:35], v[100:103], v[52:55], 0
	v_mfma_f32_32x32x16_bf16 v[20:35], v[76:79], v[112:115], v[20:35]
; DI void h_chain(f32x16& S, f32x16& O, HPacks& K, const HOpsK& P, const bf16x8 (&vt)[2], const u32x4 (&vv)[2], int rq, int hh) {
;     f32x16 X;
;     { f32x16 Se;
; #pragma unroll
;       for (int g = 0; g < 4; ++g) {
; #pragma unroll
;           for (int e = 0; e < 4; ++e) Se[4 * g + e] = S[4 * g + e] * P.ebm[g][e]; }
;       K.sp0 = pack_step(Se, 0); K.sp1 = pack_step(Se, 1); }
; #pragma unroll
;     for (int g = 0; g < 4; ++g) {
; #pragma unroll
;         for (int e = 0; e < 4; ++e) S[4 * g + e] *= P.dec[g][e]; }
; #pragma unroll
;     for (int i = 0; i < 16; ++i) { X[i] = 0.f; O[i] = 0.f; }
;     __builtin_amdgcn_sched_barrier(0);
; #pragma unroll
;     for (int st = 0; st < 2; ++st) X = MFMA32(P.ka[st], P.qb[st], X);
; #pragma unroll
;     for (int i = 0; i < 16; ++i) X[i] = (crow(i, hh) <= rq) ? X[i] : 0.f;
;     K.xp0 = pack_step(X, 0); K.xp1 = pack_step(X, 1);
;     __builtin_amdgcn_sched_barrier(0);
;     O = MFMA32(K.xp0, __builtin_bit_cast(bf16x8, vv[0]), O);
;     O = MFMA32(__builtin_bit_cast(bf16x8, P.qq[0]), K.sp0, O);
;     O = MFMA32(K.xp1, __builtin_bit_cast(bf16x8, vv[1]), O);
;     O = MFMA32(__builtin_bit_cast(bf16x8, P.qq[1]), K.sp1, O);
; #pragma unroll
;     for (int st = 0; st < 2; ++st) S = MFMA32(P.ku[st], vt[st], S);
;     __builtin_amdgcn_sched_barrier(0);
; }
; DI void h_mma2(f32x16& S0, f32x16& S1, LAS unsigned char* buf, LAS unsigned char* red, int kbp, int vb, int r32, int hh) {
;     int rq = r32; asm volatile("" : "+v"(rq));
;     bf16x8 vt[2]; u32x4 vv[2];
; #pragma unroll
;     for (int st = 0; st < 2; ++st) {
;         vt[st] = *(const LAS bf16x8*)(buf + H_VT + (vb * 32 + r32) * 80 + (16 * st + 8 * hh) * 2);
;         const LAS unsigned char* vp = buf + H_VT + (vb * 32 + r32) * 80 + (16 * st + 4 * hh) * 2;
;         const u32x2 v0 = *(const LAS u32x2*)vp, v1 = *(const LAS u32x2*)(vp + 16);
;         vv[st].x = v0.x; vv[st].y = v0.y; vv[st].z = v1.x; vv[st].w = v1.y;
;     }
;     f32x16 Osum;
; #pragma unroll
;     for (int kk = 0; kk < 2; ++kk) {
;         HOpsK P; h_opsk_load(P, buf, 2 * kbp + kk, r32, hh);
;         f32x16& S = (kk == 0) ? S0 : S1; f32x16 O;
;         LDS_WAIT(); __builtin_amdgcn_sched_barrier(0);
;         HPacks K;
;         h_chain(S, O, K, P, vt, vv, rq, hh);
;         { float s_ = S[15] + O[15]; asm volatile("v_mov_b32 %0, %0" : "+v"(s_)); asm volatile("" :: "v"(s_)); }
	v_mfma_f32_32x32x16_bf16 v[20:35], v[104:107], v[56:59], v[20:35]
	v_mfma_f32_32x32x16_bf16 v[36:51], v[88:91], v[60:63], v[36:51]
	v_mfma_f32_32x32x16_bf16 v[20:35], v[96:99], v[122:125], v[20:35]
	v_mfma_f32_32x32x16_bf16 v[36:51], v[92:95], v[64:67], v[36:51]
	s_nop 11
	v_add_f32_e32 v36, v35, v51
	v_mov_b32 v36, v36
	s_nop 0
	v_or_b32_e32 v37, s68, v129
	v_lshl_add_u32 v37, v37, 1, v130
	ds_read_b128 v[68:71], v37 offset:63488
	ds_read_b128 v[72:75], v37 offset:54784
	v_add_u32_e32 v37, s69, v131
	v_add_u32_e32 v37, 0xd000, v37
	v_or_b32_e32 v36, s68, v121
	ds_read2_b64 v[76:79], v37 offset0:192 offset1:194
	v_or_b32_e32 v37, s70, v129
	v_mad_u32_u24 v36, v36, s86, v132
	v_lshl_add_u32 v37, v37, 1, v130
	ds_read_b128 v[80:83], v37 offset:63488
	ds_read_b128 v[84:87], v37 offset:54784
	ds_read_b128 v[88:91], v36
	ds_read_b128 v[92:95], v36 offset:32
	v_add_u32_e32 v36, s71, v131
	v_add_u32_e32 v36, 0xd000, v36
	v_or_b32_e32 v108, s72, v128
	ds_read2_b64 v[96:99], v36 offset0:192 offset1:194
	v_add_u32_e32 v36, s91, v108
	v_add_u32_e32 v40, s92, v108
	v_or_b32_e32 v44, 32, v108
	v_or_b32_e32 v100, 64, v108
	v_or_b32_e32 v108, 0x60, v108
	v_add_u32_e32 v45, s91, v44
	v_add_u32_e32 v48, s92, v44
	v_add_u32_e32 v101, s91, v100
	v_add_u32_e32 v104, s92, v100
	v_add_u32_e32 v109, s91, v108
	v_add_u32_e32 v112, s92, v108
	ds_read_b128 v[36:39], v36
	ds_read_b128 v[40:43], v40
	ds_read_b128 v[44:47], v45
	ds_read_b128 v[48:51], v48
	ds_read_b128 v[100:103], v101
	ds_read_b128 v[104:107], v104
	ds_read_b128 v[108:111], v109
	ds_read_b128 v[112:115], v112
	s_waitcnt lgkmcnt(0)
	s_waitcnt lgkmcnt(6)
	v_mul_f32_e32 v41, v5, v41
	v_mul_f32_e32 v40, v4, v40
	v_mul_f32_e32 v43, v7, v43
	v_mul_f32_e32 v42, v6, v42
	s_waitcnt lgkmcnt(4)
	v_mul_f32_e32 v49, v9, v49
	v_mul_f32_e32 v48, v8, v48
	v_mul_f32_e32 v51, v11, v51
	v_mul_f32_e32 v50, v10, v50
	s_waitcnt lgkmcnt(2)
	v_mul_f32_e32 v117, v13, v105
	v_mul_f32_e32 v116, v12, v104
	v_mul_f32_e32 v123, v15, v107
	v_mul_f32_e32 v122, v14, v106
	s_waitcnt lgkmcnt(0)
	v_mul_f32_e32 v125, v17, v113
	v_mul_f32_e32 v124, v16, v112
	v_mul_f32_e32 v127, v19, v115
	v_mul_f32_e32 v126, v18, v114
	v_cvt_pk_bf16_f32 v104, v40, v41
	v_cvt_pk_bf16_f32 v105, v42, v43
	v_cvt_pk_bf16_f32 v106, v48, v49
	v_cvt_pk_bf16_f32 v107, v50, v51
	v_cvt_pk_bf16_f32 v112, v116, v117
	v_cvt_pk_bf16_f32 v113, v122, v123
	v_cvt_pk_bf16_f32 v114, v124, v125
	v_cvt_pk_bf16_f32 v115, v126, v127
	v_mul_f32_e32 v19, v19, v111
	v_mul_f32_e32 v18, v18, v110
	v_mul_f32_e32 v15, v15, v103
	v_mul_f32_e32 v14, v14, v102
	v_mul_f32_e32 v11, v11, v47
	v_mul_f32_e32 v10, v10, v46
	v_mul_f32_e32 v7, v7, v39
	v_mul_f32_e32 v6, v6, v38
	v_mul_f32_e32 v17, v17, v109
	v_mul_f32_e32 v16, v16, v108
	v_mul_f32_e32 v13, v13, v101
	v_mul_f32_e32 v12, v12, v100
	v_mul_f32_e32 v9, v9, v45
	v_mul_f32_e32 v8, v8, v44
	v_mul_f32_e32 v5, v5, v37
	v_mul_f32_e32 v4, v4, v36
	v_mfma_f32_32x32x16_bf16 v[36:51], v[68:71], v[72:75], 0
	v_mfma_f32_32x32x16_bf16 v[36:51], v[80:83], v[84:87], v[36:51]
	s_nop 11
	v_cndmask_b32_e64 v36, v36, 0, vcc
	v_cndmask_b32_e64 v37, 0, v37, s[4:5]
	v_cndmask_b32_e64 v38, v38, 0, s[6:7]
	v_cndmask_b32_e64 v39, v39, 0, s[8:9]
	v_cndmask_b32_e64 v40, v40, 0, s[10:11]
	v_cndmask_b32_e64 v41, v41, 0, s[12:13]
	v_cndmask_b32_e64 v42, v42, 0, s[14:15]
	v_cndmask_b32_e64 v43, v43, 0, s[16:17]
	v_cndmask_b32_e64 v44, v44, 0, s[18:19]
	v_cndmask_b32_e64 v45, v45, 0, s[20:21]
	v_cndmask_b32_e64 v46, v46, 0, s[22:23]
	v_cndmask_b32_e64 v47, v47, 0, s[24:25]
	v_cndmask_b32_e64 v48, v48, 0, s[26:27]
	v_cndmask_b32_e64 v49, v49, 0, s[28:29]
	v_cndmask_b32_e64 v50, v50, 0, s[30:31]
	v_cndmask_b32_e64 v51, v51, 0, s[34:35]
	v_cvt_pk_bf16_f32 v100, v36, v37
	v_cvt_pk_bf16_f32 v101, v38, v39
	v_cvt_pk_bf16_f32 v102, v40, v41
	v_cvt_pk_bf16_f32 v103, v42, v43
	v_cvt_pk_bf16_f32 v108, v44, v45
	v_cvt_pk_bf16_f32 v109, v46, v47
	v_cvt_pk_bf16_f32 v110, v48, v49
	v_cvt_pk_bf16_f32 v111, v50, v51
	v_mfma_f32_32x32x16_bf16 v[36:51], v[100:103], v[52:55], 0
	v_mfma_f32_32x32x16_bf16 v[36:51], v[76:79], v[104:107], v[36:51]
	v_mfma_f32_32x32x16_bf16 v[36:51], v[108:111], v[56:59], v[36:51]
	v_mfma_f32_32x32x16_bf16 v[4:19], v[88:91], v[60:63], v[4:19]
	v_mfma_f32_32x32x16_bf16 v[36:51], v[96:99], v[112:115], v[36:51]
	v_mfma_f32_32x32x16_bf16 v[4:19], v[92:95], v[64:67], v[4:19]
	s_nop 11
	v_add_f32_e32 v4, v51, v19
	v_mov_b32 v4, v4
	s_nop 0
	v_add_f32_e32 v4, v35, v51
	v_add_f32_e32 v5, v34, v50
	v_add_f32_e32 v6, v33, v49
	v_add_f32_e32 v7, v32, v48
	v_add_f32_e32 v8, v31, v47
	v_add_f32_e32 v9, v30, v46
	v_add_f32_e32 v10, v29, v45
	v_add_f32_e32 v11, v28, v44
	v_add_f32_e32 v12, v27, v43
	v_add_f32_e32 v13, v26, v42
	v_add_f32_e32 v14, v25, v41
	v_add_f32_e32 v15, v24, v40
	v_add_f32_e32 v16, v23, v39
	v_add_f32_e32 v17, v22, v38
	v_add_f32_e32 v18, v21, v37
	v_add_f32_e32 v19, v20, v36
	v_lshlrev_b32_e32 v2, 8, v2
	v_or3_b32 v2, v2, s73, v121
	v_lshl_add_u32 v2, v2, 2, 0
	v_add_u32_e32 v2, 0x1a800, v2
	ds_write2st64_b32 v2, v19, v18 offset1:1
	ds_write2st64_b32 v2, v17, v16 offset0:2 offset1:3
	ds_write2st64_b32 v2, v15, v14 offset0:8 offset1:9
	ds_write2st64_b32 v2, v13, v12 offset0:10 offset1:11
	ds_write2st64_b32 v2, v11, v10 offset0:16 offset1:17
	ds_write2st64_b32 v2, v9, v8 offset0:18 offset1:19
	ds_write2st64_b32 v2, v7, v6 offset0:24 offset1:25
	ds_write2st64_b32 v2, v5, v4 offset0:26 offset1:27
	s_mov_b64 s[4:5], 0
; #define LAS __attribute__((address_space(3)))
; DI unsigned pk2(float lo, float hi) { return cvtpk_s(lo, hi); }
; DI int opaque_tid() { int t = threadIdx.x; asm volatile("" : "+v"(t)); return t; }
; #define HSTEP2(cc, RF, RN, RNN) do { if (prep) h_prep_step<RF, RN, RNN>(CR, A, lds, (cc), rb, h, vhalf); else h_mma_step(S0, S1, lds, (cc), F.wave); __syncthreads(); } while (0)
; DI void h_reduce_store2(LAS unsigned char* red, bf16_t* op, int c, int pt) {
; #pragma unroll
;     for (int s2 = 0; s2 < 2; ++s2) {
;         const int s = pt + 256 * s2, t = s >> 4, c4 = s & 15;
;         const f32x4 a = *(const LAS f32x4*)(red + ((0 * 32 + t) * 64 + 4 * c4) * 4), b2 = *(const LAS f32x4*)(red + ((1 * 32 + t) * 64 + 4 * c4) * 4);
;         const f32x4 sm = a + b2;
;         u32x2 w; w.x = pk2(sm[0], sm[1]); w.y = pk2(sm[2], sm[3]);
;         *(u32x2*)(op + (size_t)(32 * c + t) * D + 4 * c4) = w;
;     }
; }
; DI void p2_hgrn_roles(Frame& F, ArgsP A) {
;     ...
;         HSTEP2(63, 0, 1, 2);
;         if (prep) { const int pt = opaque_tid() & 255; h_reduce_store2(lds + H_RED2 + 16384, (bf16_t*)(A->ws + WS_OH) + rb + h * 128 + vhalf * 64, 63, pt); }
;         __syncthreads();
.LBB0_442:
	s_andn2_b64 vcc, exec, s[4:5]
	s_cbranch_vccnz .LBB0_444
	v_mov_b32_e32 v2, v0
	s_load_dwordx2 s[4:5], s[40:41], 0x98
	s_lshl_b64 s[6:7], s[52:53], 1
	v_lshlrev_b32_e32 v4, 2, v2
	v_and_b32_e32 v12, 60, v4
	v_bfe_u32 v19, v2, 4, 4
	s_waitcnt lgkmcnt(0)
	s_add_u32 s4, s4, s6
	s_addc_u32 s5, s5, s7
	s_lshl_b32 s6, s96, 1
	s_add_u32 s4, s4, s6
	s_addc_u32 s5, s5, 0
	s_lshl_b32 s6, s48, 1
	s_add_u32 s4, s4, s6
	s_addc_u32 s5, s5, 0
	s_add_i32 s6, 0, 0x16800
	v_lshl_add_u32 v18, v12, 2, s6
	v_lshl_add_u32 v2, v19, 8, v18
	ds_read_b128 v[4:7], v2
	ds_read_b128 v[8:11], v2 offset:8192
	v_lshlrev_b32_e32 v2, 1, v12
	v_lshl_add_u64 v[12:13], s[4:5], 0, v[2:3]
	v_lshl_add_u64 v[12:13], v[12:13], 0, s[50:51]
	v_lshlrev_b32_e32 v2, 12, v19
	v_lshl_add_u64 v[16:17], v[12:13], 0, v[2:3]
	v_or_b32_e32 v2, 16, v19
	s_waitcnt lgkmcnt(0)
	v_add_f32_e32 v7, v7, v11
	v_add_f32_e32 v6, v6, v10
	v_add_f32_e32 v5, v5, v9
	v_add_f32_e32 v4, v4, v8
	v_lshl_add_u32 v8, v2, 8, v18
	v_cvt_pk_bf16_f32 v14, v4, v5
	v_cvt_pk_bf16_f32 v15, v6, v7
	ds_read_b128 v[4:7], v8
	ds_read_b128 v[8:11], v8 offset:8192
	v_add_co_u32_e32 v16, vcc, s93, v16
	v_lshlrev_b32_e32 v2, 12, v2
	s_nop 0
	v_addc_co_u32_e32 v17, vcc, 0, v17, vcc
	s_waitcnt lgkmcnt(0)
	v_add_f32_e32 v7, v7, v11
	v_add_f32_e32 v6, v6, v10
	v_add_f32_e32 v5, v5, v9
	v_add_f32_e32 v4, v4, v8
	global_store_dwordx2 v[16:17], v[14:15], off
	v_cvt_pk_bf16_f32 v4, v4, v5
	v_cvt_pk_bf16_f32 v5, v6, v7
	v_lshl_add_u64 v[6:7], v[12:13], 0, v[2:3]
	v_add_co_u32_e32 v6, vcc, 0x7c0000, v6
	s_nop 1
	v_addc_co_u32_e32 v7, vcc, 0, v7, vcc
	global_store_dwordx2 v[6:7], v[4:5], off
.LBB0_444:
	s_and_b64 vcc, exec, s[36:37]
	s_waitcnt lgkmcnt(0)
	s_barrier
	s_cbranch_vccnz .LBB0_404
	v_mov_b32_e32 v2, v0
	s_load_dwordx2 s[4:5], s[40:41], 0x98
	s_lshl_b64 s[6:7], s[52:53], 1
	v_lshlrev_b32_e32 v4, 2, v2
	v_and_b32_e32 v12, 60, v4
	v_bfe_u32 v19, v2, 4, 4
	s_waitcnt lgkmcnt(0)
	s_add_u32 s4, s4, s6
	s_addc_u32 s5, s5, s7
	s_lshl_b32 s6, s96, 1
	s_add_u32 s4, s4, s6
	s_addc_u32 s5, s5, 0
	s_lshl_b32 s6, s48, 1
	s_add_u32 s4, s4, s6
	s_addc_u32 s5, s5, 0
	s_add_i32 s6, 0, 0x1a800
	v_lshl_add_u32 v18, v12, 2, s6
	v_lshl_add_u32 v2, v19, 8, v18
	ds_read_b128 v[4:7], v2
	ds_read_b128 v[8:11], v2 offset:8192
	v_lshlrev_b32_e32 v2, 1, v12
	v_lshl_add_u64 v[12:13], s[4:5], 0, v[2:3]
	v_lshl_add_u64 v[12:13], v[12:13], 0, s[50:51]
	v_lshlrev_b32_e32 v2, 12, v19
	v_lshl_add_u64 v[16:17], v[12:13], 0, v[2:3]
	v_or_b32_e32 v2, 16, v19
	s_waitcnt lgkmcnt(0)
	v_add_f32_e32 v7, v7, v11
	v_add_f32_e32 v6, v6, v10
	v_add_f32_e32 v5, v5, v9
	v_add_f32_e32 v4, v4, v8
	v_lshl_add_u32 v8, v2, 8, v18
	v_cvt_pk_bf16_f32 v14, v4, v5
	v_cvt_pk_bf16_f32 v15, v6, v7
	ds_read_b128 v[4:7], v8
	ds_read_b128 v[8:11], v8 offset:8192
	v_add_co_u32_e32 v16, vcc, s94, v16
	v_lshlrev_b32_e32 v2, 12, v2
	s_nop 0
	v_addc_co_u32_e32 v17, vcc, 0, v17, vcc
	s_waitcnt lgkmcnt(0)
	v_add_f32_e32 v7, v7, v11
	v_add_f32_e32 v6, v6, v10
	v_add_f32_e32 v5, v5, v9
	v_add_f32_e32 v4, v4, v8
	global_store_dwordx2 v[16:17], v[14:15], off
	v_cvt_pk_bf16_f32 v4, v4, v5
	v_cvt_pk_bf16_f32 v5, v6, v7
	v_lshl_add_u64 v[6:7], v[12:13], 0, v[2:3]
	v_add_co_u32_e32 v6, vcc, 0x7e0000, v6
	s_nop 1
	v_addc_co_u32_e32 v7, vcc, 0, v7, vcc
	global_store_dwordx2 v[6:7], v[4:5], off
	s_branch .LBB0_404

; #define LDS_WAIT() asm volatile("s_waitcnt lgkmcnt(0)" ::: "memory")
; DI int crow(int reg, int h) { return (reg & 3) + 8 * (reg >> 2) + 4 * h; }
; #define MFMA32(a, b, c) __builtin_amdgcn_mfma_f32_32x32x16_bf16((a), (b), (c), 0, 0, 0)
; #define P3_LOADV(buf, t_) do { const GAS char* vp_ = vb_u + (long)(t_) * 8192; _Pragma("unroll") for (int s2 = 0; s2 < 2; ++s2) _Pragma("unroll") for (int db = 0; db < 4; ++db) vf[buf][db][s2] = *(const GAS u32x4*)(vp_ + (s2 * 4 + db) * 1024 + voff); } while (0)
; DI void p3_attn_mfma(Frame& F, ArgsP A) {
;     ...
;         for (int t = 0; t < 5; ++t) {
;             if (t >= tlo) {
;                 if (t == tlo) P3_LOADV(t & 1, t);
;                 f32x16 acc;
; #pragma unroll
;                 for (int i = 0; i < 16; ++i) acc[i] = tb[32 + (128 - 32 * t + rq - crow(i, h))];
;                 LDS_WAIT(); __builtin_amdgcn_sched_barrier(0);
; #pragma unroll
;                 for (int st = 0; st < 8; ++st) acc = MFMA32(kf[st], qf[st], acc);
;                 __builtin_amdgcn_sched_barrier(0);
;                 float tm = -3.0e38f;
; #pragma unroll
;                 for (int i = 0; i < 16; ++i) {
;                     const int key = crow(i, h);
;                     const bool valid = (t == 0) ? (key >= rq) : ((t == 4) ? (key <= rq) : true);
;                     acc[i] = valid ? acc[i] : -3.0e38f; tm = fmaxf(tm, acc[i]);
;                 }
;                 tm = fmaxf(tm, __shfl_xor(tm, 32));
;                 const float mn = fmaxf(m, tm), alpha = __expf(m - mn);
;                 float ps = 0.f;
; #pragma unroll
;                 for (int i = 0; i < 16; ++i) { const float p = (acc[i] > -1.0e38f) ? __expf(acc[i] - mn) : 0.f; acc[i] = p; ps += p; }
;                 ps += __shfl_xor(ps, 32);
;                 lsum = lsum * alpha + ps; m = mn;
.LBB0_465:
	v_lshl_add_u32 v2, v241, 2, v237
	ds_read2_b32 v[70:71], v2 offset0:127 offset1:128
	ds_read2_b32 v[72:73], v2 offset0:125 offset1:126
	ds_read2_b32 v[74:75], v2 offset0:119 offset1:120
	ds_read2_b32 v[76:77], v2 offset0:117 offset1:118
	ds_read2_b32 v[78:79], v2 offset0:111 offset1:112
	ds_read2_b32 v[80:81], v2 offset0:109 offset1:110
	ds_read2_b32 v[82:83], v2 offset0:103 offset1:104
	ds_read2_b32 v[88:89], v2 offset0:101 offset1:102
	s_waitcnt lgkmcnt(0)
	s_waitcnt lgkmcnt(7)
	v_mov_b32_e32 v68, v71
	v_mov_b32_e32 v69, v70
	s_waitcnt lgkmcnt(6)
	v_mov_b32_e32 v70, v73
	v_mov_b32_e32 v71, v72
	s_waitcnt lgkmcnt(5)
	v_mov_b32_e32 v72, v75
	v_mov_b32_e32 v73, v74
	s_waitcnt lgkmcnt(4)
	v_mov_b32_e32 v74, v77
	v_mov_b32_e32 v75, v76
	s_waitcnt lgkmcnt(3)
	v_mov_b32_e32 v76, v79
	v_mov_b32_e32 v77, v78
	s_waitcnt lgkmcnt(2)
	v_mov_b32_e32 v78, v81
	v_mov_b32_e32 v79, v80
	s_waitcnt lgkmcnt(1)
	v_mov_b32_e32 v80, v83
	v_mov_b32_e32 v81, v82
	s_waitcnt lgkmcnt(0)
	v_mov_b32_e32 v82, v89
	v_mov_b32_e32 v83, v88
	s_waitcnt vmcnt(0)
	s_nop 0
	v_mfma_f32_32x32x16_bf16 v[68:83], v[208:211], v[172:175], v[68:83]
	v_mfma_f32_32x32x16_bf16 v[68:83], v[204:207], v[164:167], v[68:83]
	v_mfma_f32_32x32x16_bf16 v[68:83], v[200:203], v[156:159], v[68:83]
	v_mfma_f32_32x32x16_bf16 v[68:83], v[196:199], v[148:151], v[68:83]
	v_mfma_f32_32x32x16_bf16 v[68:83], v[192:195], v[176:179], v[68:83]
	v_mfma_f32_32x32x16_bf16 v[68:83], v[188:191], v[168:171], v[68:83]
	v_mfma_f32_32x32x16_bf16 v[68:83], v[184:187], v[160:163], v[68:83]
	v_mfma_f32_32x32x16_bf16 v[68:83], v[180:183], v[152:155], v[68:83]
	s_nop 11
	v_max3_f32 v2, v68, s53, v69
	v_max3_f32 v2, v2, v70, v71
	v_max3_f32 v2, v2, v72, v73
	v_max3_f32 v2, v2, v74, v75
	v_and_b32_e32 v89, 64, v239
	v_max3_f32 v2, v2, v76, v77
	v_xor_b32_e32 v88, 32, v239
	v_add_u32_e32 v89, 64, v89
	v_max3_f32 v2, v2, v78, v79
	v_cmp_lt_i32_e32 vcc, v88, v89
	v_max3_f32 v2, v2, v80, v81
	v_max3_f32 v2, v2, v82, v83
	v_cndmask_b32_e32 v88, v239, v88, vcc
	v_lshlrev_b32_e32 v88, 2, v88
	ds_bpermute_b32 v89, v88, v2
	v_cmp_lt_f32_e32 vcc, s54, v68
	s_waitcnt lgkmcnt(0)
	v_max3_f32 v244, v243, v2, v89
	v_sub_f32_e32 v89, v68, v244
	v_mul_f32_e32 v89, 0x3fb8aa3b, v89
	v_exp_f32_e32 v89, v89
	v_sub_f32_e32 v90, v69, v244
	v_sub_f32_e32 v2, v243, v244
	v_mul_f32_e32 v90, 0x3fb8aa3b, v90
	v_cndmask_b32_e32 v243, 0, v89, vcc
	v_cmp_lt_f32_e32 vcc, s54, v69
	v_sub_f32_e32 v69, v70, v244
	v_exp_f32_e32 v90, v90
	v_mul_f32_e32 v69, 0x3fb8aa3b, v69
	v_sub_f32_e32 v89, v71, v244
	v_exp_f32_e32 v69, v69
	v_mul_f32_e32 v89, 0x3fb8aa3b, v89
	v_exp_f32_e32 v89, v89
	v_cndmask_b32_e32 v245, 0, v90, vcc
	v_cmp_lt_f32_e32 vcc, s54, v70
	v_add_f32_e32 v68, 0, v243
	v_add_f32_e32 v68, v245, v68
	v_cndmask_b32_e32 v70, 0, v69, vcc
	v_cmp_lt_f32_e32 vcc, s54, v71
	v_sub_f32_e32 v69, v72, v244
	v_mul_f32_e32 v69, 0x3fb8aa3b, v69
	v_cndmask_b32_e32 v71, 0, v89, vcc
	v_sub_f32_e32 v89, v73, v244
	v_exp_f32_e32 v69, v69
	v_mul_f32_e32 v89, 0x3fb8aa3b, v89
	v_exp_f32_e32 v89, v89
	v_cmp_lt_f32_e32 vcc, s54, v72
	v_add_f32_e32 v68, v70, v68
	v_add_f32_e32 v68, v71, v68
	v_cndmask_b32_e32 v72, 0, v69, vcc
	v_cmp_lt_f32_e32 vcc, s54, v73
	v_sub_f32_e32 v69, v74, v244
	v_mul_f32_e32 v69, 0x3fb8aa3b, v69
	v_cndmask_b32_e32 v73, 0, v89, vcc
	v_sub_f32_e32 v89, v75, v244
	v_exp_f32_e32 v69, v69
	v_mul_f32_e32 v89, 0x3fb8aa3b, v89
	v_exp_f32_e32 v89, v89
	v_cmp_lt_f32_e32 vcc, s54, v74
	v_add_f32_e32 v68, v72, v68
	v_add_f32_e32 v68, v73, v68
	v_cndmask_b32_e32 v74, 0, v69, vcc
	v_cmp_lt_f32_e32 vcc, s54, v75
	v_sub_f32_e32 v69, v76, v244
	v_mul_f32_e32 v69, 0x3fb8aa3b, v69
	v_cndmask_b32_e32 v75, 0, v89, vcc
	v_sub_f32_e32 v89, v77, v244
	v_exp_f32_e32 v69, v69
	v_mul_f32_e32 v89, 0x3fb8aa3b, v89
	v_exp_f32_e32 v89, v89
	v_cmp_lt_f32_e32 vcc, s54, v76
	v_add_f32_e32 v68, v74, v68
	v_add_f32_e32 v68, v75, v68
	v_cndmask_b32_e32 v76, 0, v69, vcc
	v_cmp_lt_f32_e32 vcc, s54, v77
	v_sub_f32_e32 v69, v78, v244
	v_mul_f32_e32 v69, 0x3fb8aa3b, v69
	v_cndmask_b32_e32 v77, 0, v89, vcc
	v_sub_f32_e32 v89, v79, v244
	v_exp_f32_e32 v69, v69
	v_mul_f32_e32 v89, 0x3fb8aa3b, v89
	v_exp_f32_e32 v89, v89
	v_cmp_lt_f32_e32 vcc, s54, v78
	v_add_f32_e32 v68, v76, v68
	v_add_f32_e32 v68, v77, v68
	v_cndmask_b32_e32 v78, 0, v69, vcc
	v_cmp_lt_f32_e32 vcc, s54, v79
	v_sub_f32_e32 v69, v80, v244
	v_mul_f32_e32 v69, 0x3fb8aa3b, v69
	v_cndmask_b32_e32 v79, 0, v89, vcc
	v_sub_f32_e32 v89, v81, v244
	v_exp_f32_e32 v69, v69
	v_mul_f32_e32 v89, 0x3fb8aa3b, v89
	v_exp_f32_e32 v89, v89
	v_cmp_lt_f32_e32 vcc, s54, v80
	v_add_f32_e32 v68, v78, v68
	v_add_f32_e32 v68, v79, v68
	v_cndmask_b32_e32 v80, 0, v69, vcc
	v_cmp_lt_f32_e32 vcc, s54, v81
	v_sub_f32_e32 v69, v82, v244
	v_mul_f32_e32 v69, 0x3fb8aa3b, v69
	v_cndmask_b32_e32 v81, 0, v89, vcc
	v_sub_f32_e32 v89, v83, v244
	v_exp_f32_e32 v69, v69
	v_mul_f32_e32 v89, 0x3fb8aa3b, v89
	v_exp_f32_e32 v89, v89
	v_add_f32_e32 v68, v80, v68
	v_cmp_lt_f32_e32 vcc, s54, v82
	v_add_f32_e32 v68, v81, v68
	v_mul_f32_e32 v2, 0x3fb8aa3b, v2
	v_cndmask_b32_e32 v82, 0, v69, vcc
	v_cmp_lt_f32_e32 vcc, s54, v83
	v_add_f32_e32 v68, v82, v68
	v_exp_f32_e32 v2, v2
	v_cndmask_b32_e32 v83, 0, v89, vcc
	v_add_f32_e32 v68, v83, v68
	ds_bpermute_b32 v69, v88, v68
	s_waitcnt lgkmcnt(0)
; #define MFMA32(a, b, c) __builtin_amdgcn_mfma_f32_32x32x16_bf16((a), (b), (c), 0, 0, 0)
; #define P3_LOADK(t_) do { const GAS char* kp_ = kb_u + (long)(t_) * 8192; _Pragma("unroll") for (int st = 0; st < 8; ++st) kf[st] = *(const GAS bf16x8*)(kp_ + 1024 * st + voff); } while (0)
; #define P3_LOADV(buf, t_) do { const GAS char* vp_ = vb_u + (long)(t_) * 8192; _Pragma("unroll") for (int s2 = 0; s2 < 2; ++s2) _Pragma("unroll") for (int db = 0; db < 4; ++db) vf[buf][db][s2] = *(const GAS u32x4*)(vp_ + (s2 * 4 + db) * 1024 + voff); } while (0)
; DI void p3_attn_mfma(Frame& F, ArgsP A) {
;     ...
;                 tm = fmaxf(tm, __shfl_xor(tm, 32));
;                 const float mn = fmaxf(m, tm), alpha = __expf(m - mn);
;                 float ps = 0.f;
; #pragma unroll
;                 for (int i = 0; i < 16; ++i) { const float p = (acc[i] > -1.0e38f) ? __expf(acc[i] - mn) : 0.f; acc[i] = p; ps += p; }
;                 ps += __shfl_xor(ps, 32);
;                 lsum = lsum * alpha + ps; m = mn;
;                 __builtin_amdgcn_sched_barrier(0);
;                 if (t < 4) { P3_LOADK(t + 1); P3_LOADV((t + 1) & 1, t + 1); }
; #pragma unroll
;                 for (int db = 0; db < 4; ++db) {
; #pragma unroll
;                     for (int i = 0; i < 16; ++i) O[db][i] *= alpha; }
;                 const bf16x8 pb0 = pack_step(acc, 0), pb1 = pack_step(acc, 1);
;                 __builtin_amdgcn_sched_barrier(0);
; #pragma unroll
;                 for (int db = 0; db < 4; ++db) O[db] = MFMA32(__builtin_bit_cast(bf16x8, vf[t & 1][db][0]), pb0, O[db]);
; #pragma unroll
;                 for (int db = 0; db < 4; ++db) O[db] = MFMA32(__builtin_bit_cast(bf16x8, vf[t & 1][db][1]), pb1, O[db]);
	v_add_f32_e32 v246, v68, v69
	v_fmac_f32_e32 v246, v242, v2
	v_add_co_u32_e32 v68, vcc, s57, v214
	v_mul_f32_e32 v67, v67, v2
	v_mul_f32_e32 v66, v66, v2
	s_nop 0
	v_addc_co_u32_e32 v69, vcc, 0, v215, vcc
	global_load_dwordx4 v[180:183], v[68:69], off offset:3072
	global_load_dwordx4 v[184:187], v[68:69], off offset:2048
	global_load_dwordx4 v[188:191], v[68:69], off offset:1024
	global_load_dwordx4 v[192:195], v[68:69], off
	v_add_co_u32_e32 v68, vcc, s63, v214
	v_mul_f32_e32 v65, v65, v2
	v_mul_f32_e32 v64, v64, v2
	s_nop 0
	v_addc_co_u32_e32 v69, vcc, 0, v215, vcc
	global_load_dwordx4 v[196:199], v[68:69], off offset:3072
	global_load_dwordx4 v[200:203], v[68:69], off offset:2048
	global_load_dwordx4 v[204:207], v[68:69], off offset:1024
	global_load_dwordx4 v[208:211], v[68:69], off
	v_add_co_u32_e32 v68, vcc, s57, v212
	v_mul_f32_e32 v63, v63, v2
	v_mul_f32_e32 v62, v62, v2
	s_nop 0
	v_addc_co_u32_e32 v69, vcc, 0, v213, vcc
	global_load_dwordx4 v[132:135], v[68:69], off offset:3072
	global_load_dwordx4 v[136:139], v[68:69], off offset:2048
	global_load_dwordx4 v[140:143], v[68:69], off offset:1024
	global_load_dwordx4 v[144:147], v[68:69], off
	v_add_co_u32_e32 v68, vcc, s63, v212
	v_mul_f32_e32 v61, v61, v2
	v_mul_f32_e32 v60, v60, v2
	s_nop 0
	v_addc_co_u32_e32 v69, vcc, 0, v213, vcc
	global_load_dwordx4 v[88:91], v[68:69], off offset:3072
	global_load_dwordx4 v[92:95], v[68:69], off offset:2048
	global_load_dwordx4 v[100:103], v[68:69], off offset:1024
	global_load_dwordx4 v[108:111], v[68:69], off
	v_mul_f32_e32 v59, v59, v2
	v_mul_f32_e32 v58, v58, v2
	v_mul_f32_e32 v57, v57, v2
	v_mul_f32_e32 v56, v56, v2
	v_mul_f32_e32 v55, v55, v2
	v_mul_f32_e32 v54, v54, v2
	v_mul_f32_e32 v53, v53, v2
	v_mul_f32_e32 v52, v52, v2
	v_mul_f32_e32 v51, v51, v2
	v_mul_f32_e32 v50, v50, v2
	v_mul_f32_e32 v49, v49, v2
	v_mul_f32_e32 v48, v48, v2
	v_mul_f32_e32 v47, v47, v2
	v_mul_f32_e32 v46, v46, v2
	v_mul_f32_e32 v45, v45, v2
	v_mul_f32_e32 v44, v44, v2
	v_mul_f32_e32 v43, v43, v2
	v_mul_f32_e32 v42, v42, v2
	v_mul_f32_e32 v41, v41, v2
	v_mul_f32_e32 v40, v40, v2
	v_mul_f32_e32 v39, v39, v2
	v_mul_f32_e32 v38, v38, v2
	v_mul_f32_e32 v37, v37, v2
	v_mul_f32_e32 v36, v36, v2
	v_mul_f32_e32 v35, v35, v2
	v_mul_f32_e32 v34, v34, v2
	v_mul_f32_e32 v33, v33, v2
	v_mul_f32_e32 v32, v32, v2
	v_mul_f32_e32 v31, v31, v2
	v_mul_f32_e32 v30, v30, v2
	v_mul_f32_e32 v29, v29, v2
	v_mul_f32_e32 v28, v28, v2
	v_mul_f32_e32 v27, v27, v2
	v_mul_f32_e32 v26, v26, v2
	v_mul_f32_e32 v25, v25, v2
	v_mul_f32_e32 v24, v24, v2
	v_mul_f32_e32 v23, v23, v2
	v_mul_f32_e32 v22, v22, v2
	v_mul_f32_e32 v21, v21, v2
	v_mul_f32_e32 v20, v20, v2
	v_mul_f32_e32 v19, v19, v2
	v_mul_f32_e32 v18, v18, v2
	v_mul_f32_e32 v17, v17, v2
	v_mul_f32_e32 v16, v16, v2
	v_mul_f32_e32 v15, v15, v2
	v_mul_f32_e32 v14, v14, v2
	v_mul_f32_e32 v13, v13, v2
	v_mul_f32_e32 v12, v12, v2
	v_mul_f32_e32 v11, v11, v2
	v_mul_f32_e32 v10, v10, v2
	v_mul_f32_e32 v9, v9, v2
	v_mul_f32_e32 v8, v8, v2
	v_mul_f32_e32 v7, v7, v2
	v_mul_f32_e32 v6, v6, v2
	v_mul_f32_e32 v5, v5, v2
	v_mul_f32_e32 v4, v4, v2
	v_cvt_pk_bf16_f32 v68, v243, v245
	v_cvt_pk_bf16_f32 v69, v70, v71
	v_cvt_pk_bf16_f32 v70, v72, v73
	v_cvt_pk_bf16_f32 v71, v74, v75
	v_cvt_pk_bf16_f32 v72, v76, v77
	v_cvt_pk_bf16_f32 v73, v78, v79
	v_cvt_pk_bf16_f32 v74, v80, v81
	v_cvt_pk_bf16_f32 v75, v82, v83
	v_mfma_f32_32x32x16_bf16 v[52:67], v[120:123], v[68:71], v[52:67]
	v_mov_b32_e32 v243, v244
	v_mov_b32_e32 v242, v246
	v_mfma_f32_32x32x16_bf16 v[36:51], v[112:115], v[68:71], v[36:51]
	v_mfma_f32_32x32x16_bf16 v[20:35], v[96:99], v[68:71], v[20:35]
	v_mfma_f32_32x32x16_bf16 v[4:19], v[84:87], v[68:71], v[4:19]
	v_mfma_f32_32x32x16_bf16 v[52:67], v[128:131], v[72:75], v[52:67]
	v_mfma_f32_32x32x16_bf16 v[36:51], v[124:127], v[72:75], v[36:51]
	v_mfma_f32_32x32x16_bf16 v[20:35], v[116:119], v[72:75], v[20:35]
	v_mfma_f32_32x32x16_bf16 v[4:19], v[104:107], v[72:75], v[4:19]

; #define LDS_WAIT() asm volatile("s_waitcnt lgkmcnt(0)" ::: "memory")
; DI int crow(int reg, int h) { return (reg & 3) + 8 * (reg >> 2) + 4 * h; }
; #define MFMA32(a, b, c) __builtin_amdgcn_mfma_f32_32x32x16_bf16((a), (b), (c), 0, 0, 0)
; #define P3_LOADV(buf, t_) do { const GAS char* vp_ = vb_u + (long)(t_) * 8192; _Pragma("unroll") for (int s2 = 0; s2 < 2; ++s2) _Pragma("unroll") for (int db = 0; db < 4; ++db) vf[buf][db][s2] = *(const GAS u32x4*)(vp_ + (s2 * 4 + db) * 1024 + voff); } while (0)
; DI void p3_attn_mfma(Frame& F, ArgsP A) {
;     ...
;                 if (t == tlo) P3_LOADV(t & 1, t);
;                 f32x16 acc;
; #pragma unroll
;                 for (int i = 0; i < 16; ++i) acc[i] = tb[32 + (128 - 32 * t + rq - crow(i, h))];
;                 LDS_WAIT(); __builtin_amdgcn_sched_barrier(0);
; #pragma unroll
;                 for (int st = 0; st < 8; ++st) acc = MFMA32(kf[st], qf[st], acc);
;                 __builtin_amdgcn_sched_barrier(0);
;                 float tm = -3.0e38f;
; #pragma unroll
;                 for (int i = 0; i < 16; ++i) {
;                     const int key = crow(i, h);
;                     const bool valid = (t == 0) ? (key >= rq) : ((t == 4) ? (key <= rq) : true);
;                     acc[i] = valid ? acc[i] : -3.0e38f; tm = fmaxf(tm, acc[i]);
;                 }
;                 tm = fmaxf(tm, __shfl_xor(tm, 32));
;                 const float mn = fmaxf(m, tm), alpha = __expf(m - mn);
;                 float ps = 0.f;
; #pragma unroll
;                 for (int i = 0; i < 16; ++i) { const float p = (acc[i] > -1.0e38f) ? __expf(acc[i] - mn) : 0.f; acc[i] = p; ps += p; }
;                 ps += __shfl_xor(ps, 32);
.LBB0_469:
	v_lshl_add_u32 v2, v241, 2, v237
	ds_read2_b32 v[70:71], v2 offset0:95 offset1:96
	ds_read2_b32 v[72:73], v2 offset0:93 offset1:94
	ds_read2_b32 v[74:75], v2 offset0:87 offset1:88
	ds_read2_b32 v[76:77], v2 offset0:85 offset1:86
	ds_read2_b32 v[78:79], v2 offset0:79 offset1:80
	ds_read2_b32 v[80:81], v2 offset0:77 offset1:78
	ds_read2_b32 v[82:83], v2 offset0:71 offset1:72
	s_waitcnt vmcnt(11)
	ds_read2_b32 v[84:85], v2 offset0:69 offset1:70
	s_waitcnt lgkmcnt(0)
	s_waitcnt lgkmcnt(7)
	v_mov_b32_e32 v68, v71
	v_mov_b32_e32 v69, v70
	s_waitcnt lgkmcnt(6)
	v_mov_b32_e32 v70, v73
	v_mov_b32_e32 v71, v72
	s_waitcnt lgkmcnt(5)
	v_mov_b32_e32 v72, v75
	v_mov_b32_e32 v73, v74
	s_waitcnt lgkmcnt(4)
	v_mov_b32_e32 v74, v77
	v_mov_b32_e32 v75, v76
	s_waitcnt lgkmcnt(3)
	v_mov_b32_e32 v76, v79
	v_mov_b32_e32 v77, v78
	s_waitcnt lgkmcnt(2)
	v_mov_b32_e32 v78, v81
	v_mov_b32_e32 v79, v80
	s_waitcnt lgkmcnt(1)
	v_mov_b32_e32 v80, v83
	v_mov_b32_e32 v81, v82
	s_waitcnt lgkmcnt(0)
	v_mov_b32_e32 v82, v85
	v_mov_b32_e32 v83, v84
	s_waitcnt vmcnt(0)
	s_nop 0
	v_mfma_f32_32x32x16_bf16 v[68:83], v[208:211], v[172:175], v[68:83]
	v_mfma_f32_32x32x16_bf16 v[68:83], v[204:207], v[164:167], v[68:83]
	v_mfma_f32_32x32x16_bf16 v[68:83], v[200:203], v[156:159], v[68:83]
	v_mfma_f32_32x32x16_bf16 v[68:83], v[196:199], v[148:151], v[68:83]
	v_mfma_f32_32x32x16_bf16 v[68:83], v[192:195], v[176:179], v[68:83]
	v_mfma_f32_32x32x16_bf16 v[68:83], v[188:191], v[168:171], v[68:83]
	v_mfma_f32_32x32x16_bf16 v[68:83], v[184:187], v[160:163], v[68:83]
	v_mfma_f32_32x32x16_bf16 v[68:83], v[180:183], v[152:155], v[68:83]
	s_nop 11
	v_max3_f32 v2, v68, s53, v69
	v_max3_f32 v2, v2, v70, v71
	v_max3_f32 v2, v2, v72, v73
	v_max3_f32 v2, v2, v74, v75
	v_and_b32_e32 v85, 64, v239
	v_max3_f32 v2, v2, v76, v77
	v_xor_b32_e32 v84, 32, v239
	v_add_u32_e32 v85, 64, v85
	v_max3_f32 v2, v2, v78, v79
	v_cmp_lt_i32_e32 vcc, v84, v85
	v_max3_f32 v2, v2, v80, v81
	v_max3_f32 v2, v2, v82, v83
	v_cndmask_b32_e32 v84, v239, v84, vcc
	v_lshlrev_b32_e32 v84, 2, v84
	ds_bpermute_b32 v85, v84, v2
	v_cmp_lt_f32_e32 vcc, s54, v68
	s_waitcnt lgkmcnt(0)
	v_max3_f32 v244, v243, v2, v85
	v_sub_f32_e32 v85, v68, v244
	v_mul_f32_e32 v85, 0x3fb8aa3b, v85
	v_exp_f32_e32 v85, v85
	v_sub_f32_e32 v86, v69, v244
	v_sub_f32_e32 v2, v243, v244
	v_mul_f32_e32 v86, 0x3fb8aa3b, v86
	v_cndmask_b32_e32 v243, 0, v85, vcc
	v_cmp_lt_f32_e32 vcc, s54, v69
	v_sub_f32_e32 v69, v70, v244
	v_exp_f32_e32 v86, v86
	v_mul_f32_e32 v69, 0x3fb8aa3b, v69
	v_sub_f32_e32 v85, v71, v244
	v_exp_f32_e32 v69, v69
	v_mul_f32_e32 v85, 0x3fb8aa3b, v85
	v_exp_f32_e32 v85, v85
	v_cndmask_b32_e32 v245, 0, v86, vcc
	v_cmp_lt_f32_e32 vcc, s54, v70
	v_add_f32_e32 v68, 0, v243
	v_add_f32_e32 v68, v245, v68
	v_cndmask_b32_e32 v70, 0, v69, vcc
	v_cmp_lt_f32_e32 vcc, s54, v71
	v_sub_f32_e32 v69, v72, v244
	v_mul_f32_e32 v69, 0x3fb8aa3b, v69
	v_cndmask_b32_e32 v71, 0, v85, vcc
	v_sub_f32_e32 v85, v73, v244
	v_exp_f32_e32 v69, v69
	v_mul_f32_e32 v85, 0x3fb8aa3b, v85
	v_exp_f32_e32 v85, v85
	v_cmp_lt_f32_e32 vcc, s54, v72
	v_add_f32_e32 v68, v70, v68
	v_add_f32_e32 v68, v71, v68
	v_cndmask_b32_e32 v72, 0, v69, vcc
	v_cmp_lt_f32_e32 vcc, s54, v73
	v_sub_f32_e32 v69, v74, v244
	v_mul_f32_e32 v69, 0x3fb8aa3b, v69
	v_cndmask_b32_e32 v73, 0, v85, vcc
	v_sub_f32_e32 v85, v75, v244
	v_exp_f32_e32 v69, v69
	v_mul_f32_e32 v85, 0x3fb8aa3b, v85
	v_exp_f32_e32 v85, v85
	v_cmp_lt_f32_e32 vcc, s54, v74
	v_add_f32_e32 v68, v72, v68
	v_add_f32_e32 v68, v73, v68
	v_cndmask_b32_e32 v74, 0, v69, vcc
	v_cmp_lt_f32_e32 vcc, s54, v75
	v_sub_f32_e32 v69, v76, v244
	v_mul_f32_e32 v69, 0x3fb8aa3b, v69
	v_cndmask_b32_e32 v75, 0, v85, vcc
	v_sub_f32_e32 v85, v77, v244
	v_exp_f32_e32 v69, v69
	v_mul_f32_e32 v85, 0x3fb8aa3b, v85
	v_exp_f32_e32 v85, v85
	v_cmp_lt_f32_e32 vcc, s54, v76
	v_add_f32_e32 v68, v74, v68
	v_add_f32_e32 v68, v75, v68
	v_cndmask_b32_e32 v76, 0, v69, vcc
	v_cmp_lt_f32_e32 vcc, s54, v77
	v_sub_f32_e32 v69, v78, v244
	v_mul_f32_e32 v69, 0x3fb8aa3b, v69
	v_cndmask_b32_e32 v77, 0, v85, vcc
	v_sub_f32_e32 v85, v79, v244
	v_exp_f32_e32 v69, v69
	v_mul_f32_e32 v85, 0x3fb8aa3b, v85
	v_exp_f32_e32 v85, v85
	v_cmp_lt_f32_e32 vcc, s54, v78
	v_add_f32_e32 v68, v76, v68
	v_add_f32_e32 v68, v77, v68
	v_cndmask_b32_e32 v78, 0, v69, vcc
	v_cmp_lt_f32_e32 vcc, s54, v79
	v_sub_f32_e32 v69, v80, v244
	v_mul_f32_e32 v69, 0x3fb8aa3b, v69
	v_cndmask_b32_e32 v79, 0, v85, vcc
	v_sub_f32_e32 v85, v81, v244
	v_exp_f32_e32 v69, v69
	v_mul_f32_e32 v85, 0x3fb8aa3b, v85
	v_exp_f32_e32 v85, v85
	v_cmp_lt_f32_e32 vcc, s54, v80
	v_add_f32_e32 v68, v78, v68
	v_add_f32_e32 v68, v79, v68
	v_cndmask_b32_e32 v80, 0, v69, vcc
	v_cmp_lt_f32_e32 vcc, s54, v81
	v_sub_f32_e32 v69, v82, v244
	v_mul_f32_e32 v69, 0x3fb8aa3b, v69
	v_cndmask_b32_e32 v81, 0, v85, vcc
	v_sub_f32_e32 v85, v83, v244
	v_exp_f32_e32 v69, v69
	v_mul_f32_e32 v85, 0x3fb8aa3b, v85
	v_exp_f32_e32 v85, v85
	v_add_f32_e32 v68, v80, v68
	v_cmp_lt_f32_e32 vcc, s54, v82
	v_add_f32_e32 v68, v81, v68
	v_mul_f32_e32 v2, 0x3fb8aa3b, v2
	v_cndmask_b32_e32 v82, 0, v69, vcc
	v_cmp_lt_f32_e32 vcc, s54, v83
	v_add_f32_e32 v68, v82, v68
	v_exp_f32_e32 v2, v2
	v_cndmask_b32_e32 v83, 0, v85, vcc
	v_add_f32_e32 v68, v83, v68
	ds_bpermute_b32 v69, v84, v68
	s_waitcnt lgkmcnt(0)
; #define MFMA32(a, b, c) __builtin_amdgcn_mfma_f32_32x32x16_bf16((a), (b), (c), 0, 0, 0)
; #define P3_LOADK(t_) do { const GAS char* kp_ = kb_u + (long)(t_) * 8192; _Pragma("unroll") for (int st = 0; st < 8; ++st) kf[st] = *(const GAS bf16x8*)(kp_ + 1024 * st + voff); } while (0)
; #define P3_LOADV(buf, t_) do { const GAS char* vp_ = vb_u + (long)(t_) * 8192; _Pragma("unroll") for (int s2 = 0; s2 < 2; ++s2) _Pragma("unroll") for (int db = 0; db < 4; ++db) vf[buf][db][s2] = *(const GAS u32x4*)(vp_ + (s2 * 4 + db) * 1024 + voff); } while (0)
; DI void p3_attn_mfma(Frame& F, ArgsP A) {
;     ...
;                 lsum = lsum * alpha + ps; m = mn;
;                 __builtin_amdgcn_sched_barrier(0);
;                 if (t < 4) { P3_LOADK(t + 1); P3_LOADV((t + 1) & 1, t + 1); }
; #pragma unroll
;                 for (int db = 0; db < 4; ++db) {
; #pragma unroll
;                     for (int i = 0; i < 16; ++i) O[db][i] *= alpha; }
;                 const bf16x8 pb0 = pack_step(acc, 0), pb1 = pack_step(acc, 1);
;                 __builtin_amdgcn_sched_barrier(0);
; #pragma unroll
;                 for (int db = 0; db < 4; ++db) O[db] = MFMA32(__builtin_bit_cast(bf16x8, vf[t & 1][db][0]), pb0, O[db]);
; #pragma unroll
;                 for (int db = 0; db < 4; ++db) O[db] = MFMA32(__builtin_bit_cast(bf16x8, vf[t & 1][db][1]), pb1, O[db]);
	v_add_f32_e32 v246, v68, v69
	v_fmac_f32_e32 v246, v242, v2
	v_add_co_u32_e32 v68, vcc, s64, v214
	v_mul_f32_e32 v67, v67, v2
	v_mul_f32_e32 v66, v66, v2
	s_nop 0
	v_addc_co_u32_e32 v69, vcc, 0, v215, vcc
	global_load_dwordx4 v[180:183], v[68:69], off offset:3072
	global_load_dwordx4 v[184:187], v[68:69], off offset:2048
	global_load_dwordx4 v[188:191], v[68:69], off offset:1024
	global_load_dwordx4 v[192:195], v[68:69], off
	v_add_co_u32_e32 v68, vcc, s65, v214
	v_mul_f32_e32 v65, v65, v2
	v_mul_f32_e32 v64, v64, v2
	s_nop 0
	v_addc_co_u32_e32 v69, vcc, 0, v215, vcc
	global_load_dwordx4 v[196:199], v[68:69], off offset:3072
	global_load_dwordx4 v[200:203], v[68:69], off offset:2048
	global_load_dwordx4 v[204:207], v[68:69], off offset:1024
	global_load_dwordx4 v[208:211], v[68:69], off
	v_add_co_u32_e32 v68, vcc, s64, v212
	v_mul_f32_e32 v63, v63, v2
	v_mul_f32_e32 v62, v62, v2
	s_nop 0
	v_addc_co_u32_e32 v69, vcc, 0, v213, vcc
	global_load_dwordx4 v[104:107], v[68:69], off offset:3072
	global_load_dwordx4 v[116:119], v[68:69], off offset:2048
	global_load_dwordx4 v[124:127], v[68:69], off offset:1024
	global_load_dwordx4 v[128:131], v[68:69], off
	v_add_co_u32_e32 v68, vcc, s65, v212
	v_mul_f32_e32 v61, v61, v2
	v_mul_f32_e32 v60, v60, v2
	s_nop 0
	v_addc_co_u32_e32 v69, vcc, 0, v213, vcc
	global_load_dwordx4 v[84:87], v[68:69], off offset:3072
	global_load_dwordx4 v[96:99], v[68:69], off offset:2048
	global_load_dwordx4 v[112:115], v[68:69], off offset:1024
	global_load_dwordx4 v[120:123], v[68:69], off
	v_mul_f32_e32 v59, v59, v2
	v_mul_f32_e32 v58, v58, v2
	v_mul_f32_e32 v57, v57, v2
	v_mul_f32_e32 v56, v56, v2
	v_mul_f32_e32 v55, v55, v2
	v_mul_f32_e32 v54, v54, v2
	v_mul_f32_e32 v53, v53, v2
	v_mul_f32_e32 v52, v52, v2
	v_mul_f32_e32 v51, v51, v2
	v_mul_f32_e32 v50, v50, v2
	v_mul_f32_e32 v49, v49, v2
	v_mul_f32_e32 v48, v48, v2
	v_mul_f32_e32 v47, v47, v2
	v_mul_f32_e32 v46, v46, v2
	v_mul_f32_e32 v45, v45, v2
	v_mul_f32_e32 v44, v44, v2
	v_mul_f32_e32 v43, v43, v2
	v_mul_f32_e32 v42, v42, v2
	v_mul_f32_e32 v41, v41, v2
	v_mul_f32_e32 v40, v40, v2
	v_mul_f32_e32 v39, v39, v2
	v_mul_f32_e32 v38, v38, v2
	v_mul_f32_e32 v37, v37, v2
	v_mul_f32_e32 v36, v36, v2
	v_mul_f32_e32 v35, v35, v2
	v_mul_f32_e32 v34, v34, v2
	v_mul_f32_e32 v33, v33, v2
	v_mul_f32_e32 v32, v32, v2
	v_mul_f32_e32 v31, v31, v2
	v_mul_f32_e32 v30, v30, v2
	v_mul_f32_e32 v29, v29, v2
	v_mul_f32_e32 v28, v28, v2
	v_mul_f32_e32 v27, v27, v2
	v_mul_f32_e32 v26, v26, v2
	v_mul_f32_e32 v25, v25, v2
	v_mul_f32_e32 v24, v24, v2
	v_mul_f32_e32 v23, v23, v2
	v_mul_f32_e32 v22, v22, v2
	v_mul_f32_e32 v21, v21, v2
	v_mul_f32_e32 v20, v20, v2
	v_mul_f32_e32 v19, v19, v2
	v_mul_f32_e32 v18, v18, v2
	v_mul_f32_e32 v17, v17, v2
	v_mul_f32_e32 v16, v16, v2
	v_mul_f32_e32 v15, v15, v2
	v_mul_f32_e32 v14, v14, v2
	v_mul_f32_e32 v13, v13, v2
	v_mul_f32_e32 v12, v12, v2
	v_mul_f32_e32 v11, v11, v2
	v_mul_f32_e32 v10, v10, v2
	v_mul_f32_e32 v9, v9, v2
	v_mul_f32_e32 v8, v8, v2
	v_mul_f32_e32 v7, v7, v2
	v_mul_f32_e32 v6, v6, v2
	v_mul_f32_e32 v5, v5, v2
	v_mul_f32_e32 v4, v4, v2
	v_cvt_pk_bf16_f32 v68, v243, v245
	v_cvt_pk_bf16_f32 v69, v70, v71
	v_cvt_pk_bf16_f32 v70, v72, v73
	v_cvt_pk_bf16_f32 v71, v74, v75
	v_cvt_pk_bf16_f32 v72, v76, v77
	v_cvt_pk_bf16_f32 v73, v78, v79
	v_cvt_pk_bf16_f32 v74, v80, v81
	v_cvt_pk_bf16_f32 v75, v82, v83
	v_mfma_f32_32x32x16_bf16 v[52:67], v[108:111], v[68:71], v[52:67]
	v_mov_b32_e32 v243, v244
	v_mov_b32_e32 v242, v246
	v_mfma_f32_32x32x16_bf16 v[36:51], v[100:103], v[68:71], v[36:51]
	v_mfma_f32_32x32x16_bf16 v[20:35], v[92:95], v[68:71], v[20:35]
	v_mfma_f32_32x32x16_bf16 v[4:19], v[88:91], v[68:71], v[4:19]
	v_mfma_f32_32x32x16_bf16 v[52:67], v[144:147], v[72:75], v[52:67]
	v_mfma_f32_32x32x16_bf16 v[36:51], v[140:143], v[72:75], v[36:51]
	v_mfma_f32_32x32x16_bf16 v[20:35], v[136:139], v[72:75], v[20:35]
	v_mfma_f32_32x32x16_bf16 v[4:19], v[132:135], v[72:75], v[4:19]

; #define LDS_WAIT() asm volatile("s_waitcnt lgkmcnt(0)" ::: "memory")
; DI int crow(int reg, int h) { return (reg & 3) + 8 * (reg >> 2) + 4 * h; }
; #define MFMA32(a, b, c) __builtin_amdgcn_mfma_f32_32x32x16_bf16((a), (b), (c), 0, 0, 0)
; #define P3_LOADV(buf, t_) do { const GAS char* vp_ = vb_u + (long)(t_) * 8192; _Pragma("unroll") for (int s2 = 0; s2 < 2; ++s2) _Pragma("unroll") for (int db = 0; db < 4; ++db) vf[buf][db][s2] = *(const GAS u32x4*)(vp_ + (s2 * 4 + db) * 1024 + voff); } while (0)
; DI void p3_attn_mfma(Frame& F, ArgsP A) {
;     ...
;                 if (t == tlo) P3_LOADV(t & 1, t);
;                 f32x16 acc;
; #pragma unroll
;                 for (int i = 0; i < 16; ++i) acc[i] = tb[32 + (128 - 32 * t + rq - crow(i, h))];
;                 LDS_WAIT(); __builtin_amdgcn_sched_barrier(0);
; #pragma unroll
;                 for (int st = 0; st < 8; ++st) acc = MFMA32(kf[st], qf[st], acc);
;                 __builtin_amdgcn_sched_barrier(0);
;                 float tm = -3.0e38f;
; #pragma unroll
;                 for (int i = 0; i < 16; ++i) {
;                     const int key = crow(i, h);
;                     const bool valid = (t == 0) ? (key >= rq) : ((t == 4) ? (key <= rq) : true);
;                     acc[i] = valid ? acc[i] : -3.0e38f; tm = fmaxf(tm, acc[i]);
;                 }
;                 tm = fmaxf(tm, __shfl_xor(tm, 32));
;                 const float mn = fmaxf(m, tm), alpha = __expf(m - mn);
;                 float ps = 0.f;
; #pragma unroll
;                 for (int i = 0; i < 16; ++i) { const float p = (acc[i] > -1.0e38f) ? __expf(acc[i] - mn) : 0.f; acc[i] = p; ps += p; }
;                 ps += __shfl_xor(ps, 32);
.LBB0_473:
	v_lshl_add_u32 v2, v241, 2, v237
	ds_read2_b32 v[70:71], v2 offset0:63 offset1:64
	ds_read2_b32 v[72:73], v2 offset0:61 offset1:62
	ds_read2_b32 v[74:75], v2 offset0:55 offset1:56
	ds_read2_b32 v[76:77], v2 offset0:53 offset1:54
	ds_read2_b32 v[78:79], v2 offset0:47 offset1:48
	ds_read2_b32 v[80:81], v2 offset0:45 offset1:46
	ds_read2_b32 v[82:83], v2 offset0:39 offset1:40
	s_waitcnt vmcnt(3)
	ds_read2_b32 v[88:89], v2 offset0:37 offset1:38
	s_waitcnt lgkmcnt(0)
	s_waitcnt lgkmcnt(7)
	v_mov_b32_e32 v68, v71
	v_mov_b32_e32 v69, v70
	s_waitcnt lgkmcnt(6)
	v_mov_b32_e32 v70, v73
	v_mov_b32_e32 v71, v72
	s_waitcnt lgkmcnt(5)
	v_mov_b32_e32 v72, v75
	v_mov_b32_e32 v73, v74
	s_waitcnt lgkmcnt(4)
	v_mov_b32_e32 v74, v77
	v_mov_b32_e32 v75, v76
	s_waitcnt lgkmcnt(3)
	v_mov_b32_e32 v76, v79
	v_mov_b32_e32 v77, v78
	s_waitcnt lgkmcnt(2)
	v_mov_b32_e32 v78, v81
	v_mov_b32_e32 v79, v80
	s_waitcnt lgkmcnt(1)
	v_mov_b32_e32 v80, v83
	v_mov_b32_e32 v81, v82
	s_waitcnt lgkmcnt(0)
	v_mov_b32_e32 v82, v89
	v_mov_b32_e32 v83, v88
	s_waitcnt vmcnt(0)
	s_nop 0
	v_mfma_f32_32x32x16_bf16 v[68:83], v[208:211], v[172:175], v[68:83]
	v_mfma_f32_32x32x16_bf16 v[68:83], v[204:207], v[164:167], v[68:83]
	v_mfma_f32_32x32x16_bf16 v[68:83], v[200:203], v[156:159], v[68:83]
	v_mfma_f32_32x32x16_bf16 v[68:83], v[196:199], v[148:151], v[68:83]
	v_mfma_f32_32x32x16_bf16 v[68:83], v[192:195], v[176:179], v[68:83]
	v_mfma_f32_32x32x16_bf16 v[68:83], v[188:191], v[168:171], v[68:83]
	v_mfma_f32_32x32x16_bf16 v[68:83], v[184:187], v[160:163], v[68:83]
	v_mfma_f32_32x32x16_bf16 v[68:83], v[180:183], v[152:155], v[68:83]
	s_nop 11
	v_max3_f32 v2, v68, s53, v69
	v_max3_f32 v2, v2, v70, v71
	v_max3_f32 v2, v2, v72, v73
	v_max3_f32 v2, v2, v74, v75
	v_and_b32_e32 v89, 64, v239
	v_max3_f32 v2, v2, v76, v77
	v_xor_b32_e32 v88, 32, v239
	v_add_u32_e32 v89, 64, v89
	v_max3_f32 v2, v2, v78, v79
	v_cmp_lt_i32_e32 vcc, v88, v89
	v_max3_f32 v2, v2, v80, v81
	v_max3_f32 v2, v2, v82, v83
	v_cndmask_b32_e32 v88, v239, v88, vcc
	v_lshlrev_b32_e32 v88, 2, v88
	ds_bpermute_b32 v89, v88, v2
	v_cmp_lt_f32_e32 vcc, s54, v68
	s_waitcnt lgkmcnt(0)
	v_max3_f32 v244, v243, v2, v89
	v_sub_f32_e32 v89, v68, v244
	v_mul_f32_e32 v89, 0x3fb8aa3b, v89
	v_exp_f32_e32 v89, v89
	v_sub_f32_e32 v90, v69, v244
	v_sub_f32_e32 v2, v243, v244
	v_mul_f32_e32 v90, 0x3fb8aa3b, v90
	v_cndmask_b32_e32 v243, 0, v89, vcc
	v_cmp_lt_f32_e32 vcc, s54, v69
	v_sub_f32_e32 v69, v70, v244
	v_exp_f32_e32 v90, v90
	v_mul_f32_e32 v69, 0x3fb8aa3b, v69
	v_sub_f32_e32 v89, v71, v244
	v_exp_f32_e32 v69, v69
	v_mul_f32_e32 v89, 0x3fb8aa3b, v89
	v_exp_f32_e32 v89, v89
	v_cndmask_b32_e32 v245, 0, v90, vcc
	v_cmp_lt_f32_e32 vcc, s54, v70
	v_add_f32_e32 v68, 0, v243
	v_add_f32_e32 v68, v245, v68
	v_cndmask_b32_e32 v70, 0, v69, vcc
	v_cmp_lt_f32_e32 vcc, s54, v71
	v_sub_f32_e32 v69, v72, v244
	v_mul_f32_e32 v69, 0x3fb8aa3b, v69
	v_cndmask_b32_e32 v71, 0, v89, vcc
	v_sub_f32_e32 v89, v73, v244
	v_exp_f32_e32 v69, v69
	v_mul_f32_e32 v89, 0x3fb8aa3b, v89
	v_exp_f32_e32 v89, v89
	v_cmp_lt_f32_e32 vcc, s54, v72
	v_add_f32_e32 v68, v70, v68
	v_add_f32_e32 v68, v71, v68
	v_cndmask_b32_e32 v72, 0, v69, vcc
	v_cmp_lt_f32_e32 vcc, s54, v73
	v_sub_f32_e32 v69, v74, v244
	v_mul_f32_e32 v69, 0x3fb8aa3b, v69
	v_cndmask_b32_e32 v73, 0, v89, vcc
	v_sub_f32_e32 v89, v75, v244
	v_exp_f32_e32 v69, v69
	v_mul_f32_e32 v89, 0x3fb8aa3b, v89
	v_exp_f32_e32 v89, v89
	v_cmp_lt_f32_e32 vcc, s54, v74
	v_add_f32_e32 v68, v72, v68
	v_add_f32_e32 v68, v73, v68
	v_cndmask_b32_e32 v74, 0, v69, vcc
	v_cmp_lt_f32_e32 vcc, s54, v75
	v_sub_f32_e32 v69, v76, v244
	v_mul_f32_e32 v69, 0x3fb8aa3b, v69
	v_cndmask_b32_e32 v75, 0, v89, vcc
	v_sub_f32_e32 v89, v77, v244
	v_exp_f32_e32 v69, v69
	v_mul_f32_e32 v89, 0x3fb8aa3b, v89
	v_exp_f32_e32 v89, v89
	v_cmp_lt_f32_e32 vcc, s54, v76
	v_add_f32_e32 v68, v74, v68
	v_add_f32_e32 v68, v75, v68
	v_cndmask_b32_e32 v76, 0, v69, vcc
	v_cmp_lt_f32_e32 vcc, s54, v77
	v_sub_f32_e32 v69, v78, v244
	v_mul_f32_e32 v69, 0x3fb8aa3b, v69
	v_cndmask_b32_e32 v77, 0, v89, vcc
	v_sub_f32_e32 v89, v79, v244
	v_exp_f32_e32 v69, v69
	v_mul_f32_e32 v89, 0x3fb8aa3b, v89
	v_exp_f32_e32 v89, v89
	v_cmp_lt_f32_e32 vcc, s54, v78
	v_add_f32_e32 v68, v76, v68
	v_add_f32_e32 v68, v77, v68
	v_cndmask_b32_e32 v78, 0, v69, vcc
	v_cmp_lt_f32_e32 vcc, s54, v79
	v_sub_f32_e32 v69, v80, v244
	v_mul_f32_e32 v69, 0x3fb8aa3b, v69
	v_cndmask_b32_e32 v79, 0, v89, vcc
	v_sub_f32_e32 v89, v81, v244
	v_exp_f32_e32 v69, v69
	v_mul_f32_e32 v89, 0x3fb8aa3b, v89
	v_exp_f32_e32 v89, v89
	v_cmp_lt_f32_e32 vcc, s54, v80
	v_add_f32_e32 v68, v78, v68
	v_add_f32_e32 v68, v79, v68
	v_cndmask_b32_e32 v80, 0, v69, vcc
	v_cmp_lt_f32_e32 vcc, s54, v81
	v_sub_f32_e32 v69, v82, v244
	v_mul_f32_e32 v69, 0x3fb8aa3b, v69
	v_cndmask_b32_e32 v81, 0, v89, vcc
	v_sub_f32_e32 v89, v83, v244
	v_exp_f32_e32 v69, v69
	v_mul_f32_e32 v89, 0x3fb8aa3b, v89
	v_exp_f32_e32 v89, v89
	v_add_f32_e32 v68, v80, v68
	v_cmp_lt_f32_e32 vcc, s54, v82
	v_add_f32_e32 v68, v81, v68
	v_mul_f32_e32 v2, 0x3fb8aa3b, v2
	v_cndmask_b32_e32 v82, 0, v69, vcc
	v_cmp_lt_f32_e32 vcc, s54, v83
	v_add_f32_e32 v68, v82, v68
	v_exp_f32_e32 v2, v2
	v_cndmask_b32_e32 v83, 0, v89, vcc
	v_add_f32_e32 v68, v83, v68
	ds_bpermute_b32 v69, v88, v68
	s_waitcnt lgkmcnt(0)
; #define MFMA32(a, b, c) __builtin_amdgcn_mfma_f32_32x32x16_bf16((a), (b), (c), 0, 0, 0)
; #define P3_LOADK(t_) do { const GAS char* kp_ = kb_u + (long)(t_) * 8192; _Pragma("unroll") for (int st = 0; st < 8; ++st) kf[st] = *(const GAS bf16x8*)(kp_ + 1024 * st + voff); } while (0)
; #define P3_LOADV(buf, t_) do { const GAS char* vp_ = vb_u + (long)(t_) * 8192; _Pragma("unroll") for (int s2 = 0; s2 < 2; ++s2) _Pragma("unroll") for (int db = 0; db < 4; ++db) vf[buf][db][s2] = *(const GAS u32x4*)(vp_ + (s2 * 4 + db) * 1024 + voff); } while (0)
; DI void p3_attn_mfma(Frame& F, ArgsP A) {
;     ...
;                 lsum = lsum * alpha + ps; m = mn;
;                 __builtin_amdgcn_sched_barrier(0);
;                 if (t < 4) { P3_LOADK(t + 1); P3_LOADV((t + 1) & 1, t + 1); }
; #pragma unroll
;                 for (int db = 0; db < 4; ++db) {
; #pragma unroll
;                     for (int i = 0; i < 16; ++i) O[db][i] *= alpha; }
;                 const bf16x8 pb0 = pack_step(acc, 0), pb1 = pack_step(acc, 1);
;                 __builtin_amdgcn_sched_barrier(0);
; #pragma unroll
;                 for (int db = 0; db < 4; ++db) O[db] = MFMA32(__builtin_bit_cast(bf16x8, vf[t & 1][db][0]), pb0, O[db]);
; #pragma unroll
;                 for (int db = 0; db < 4; ++db) O[db] = MFMA32(__builtin_bit_cast(bf16x8, vf[t & 1][db][1]), pb1, O[db]);
	v_add_f32_e32 v246, v68, v69
	v_fmac_f32_e32 v246, v242, v2
	v_add_co_u32_e32 v68, vcc, s66, v214
	v_mul_f32_e32 v67, v67, v2
	v_mul_f32_e32 v66, v66, v2
	s_nop 0
	v_addc_co_u32_e32 v69, vcc, 0, v215, vcc
	global_load_dwordx4 v[180:183], v[68:69], off offset:3072
	global_load_dwordx4 v[184:187], v[68:69], off offset:2048
	global_load_dwordx4 v[188:191], v[68:69], off offset:1024
	global_load_dwordx4 v[192:195], v[68:69], off
	v_add_co_u32_e32 v68, vcc, s67, v214
	v_mul_f32_e32 v65, v65, v2
	v_mul_f32_e32 v64, v64, v2
	s_nop 0
	v_addc_co_u32_e32 v69, vcc, 0, v215, vcc
	global_load_dwordx4 v[196:199], v[68:69], off offset:3072
	global_load_dwordx4 v[200:203], v[68:69], off offset:2048
	global_load_dwordx4 v[204:207], v[68:69], off offset:1024
	global_load_dwordx4 v[208:211], v[68:69], off
	v_add_co_u32_e32 v68, vcc, s66, v212
	v_mul_f32_e32 v63, v63, v2
	v_mul_f32_e32 v62, v62, v2
	s_nop 0
	v_addc_co_u32_e32 v69, vcc, 0, v213, vcc
	global_load_dwordx4 v[132:135], v[68:69], off offset:3072
	global_load_dwordx4 v[136:139], v[68:69], off offset:2048
	global_load_dwordx4 v[140:143], v[68:69], off offset:1024
	global_load_dwordx4 v[144:147], v[68:69], off
	v_add_co_u32_e32 v68, vcc, s67, v212
	v_mul_f32_e32 v61, v61, v2
	v_mul_f32_e32 v60, v60, v2
	s_nop 0
	v_addc_co_u32_e32 v69, vcc, 0, v213, vcc
	global_load_dwordx4 v[88:91], v[68:69], off offset:3072
	global_load_dwordx4 v[92:95], v[68:69], off offset:2048
	global_load_dwordx4 v[100:103], v[68:69], off offset:1024
	global_load_dwordx4 v[108:111], v[68:69], off
	v_mul_f32_e32 v59, v59, v2
	v_mul_f32_e32 v58, v58, v2
	v_mul_f32_e32 v57, v57, v2
	v_mul_f32_e32 v56, v56, v2
	v_mul_f32_e32 v55, v55, v2
	v_mul_f32_e32 v54, v54, v2
	v_mul_f32_e32 v53, v53, v2
	v_mul_f32_e32 v52, v52, v2
	v_mul_f32_e32 v51, v51, v2
	v_mul_f32_e32 v50, v50, v2
	v_mul_f32_e32 v49, v49, v2
	v_mul_f32_e32 v48, v48, v2
	v_mul_f32_e32 v47, v47, v2
	v_mul_f32_e32 v46, v46, v2
	v_mul_f32_e32 v45, v45, v2
	v_mul_f32_e32 v44, v44, v2
	v_mul_f32_e32 v43, v43, v2
	v_mul_f32_e32 v42, v42, v2
	v_mul_f32_e32 v41, v41, v2
	v_mul_f32_e32 v40, v40, v2
	v_mul_f32_e32 v39, v39, v2
	v_mul_f32_e32 v38, v38, v2
	v_mul_f32_e32 v37, v37, v2
	v_mul_f32_e32 v36, v36, v2
	v_mul_f32_e32 v35, v35, v2
	v_mul_f32_e32 v34, v34, v2
	v_mul_f32_e32 v33, v33, v2
	v_mul_f32_e32 v32, v32, v2
	v_mul_f32_e32 v31, v31, v2
	v_mul_f32_e32 v30, v30, v2
	v_mul_f32_e32 v29, v29, v2
	v_mul_f32_e32 v28, v28, v2
	v_mul_f32_e32 v27, v27, v2
	v_mul_f32_e32 v26, v26, v2
	v_mul_f32_e32 v25, v25, v2
	v_mul_f32_e32 v24, v24, v2
	v_mul_f32_e32 v23, v23, v2
	v_mul_f32_e32 v22, v22, v2
	v_mul_f32_e32 v21, v21, v2
	v_mul_f32_e32 v20, v20, v2
	v_mul_f32_e32 v19, v19, v2
	v_mul_f32_e32 v18, v18, v2
	v_mul_f32_e32 v17, v17, v2
	v_mul_f32_e32 v16, v16, v2
	v_mul_f32_e32 v15, v15, v2
	v_mul_f32_e32 v14, v14, v2
	v_mul_f32_e32 v13, v13, v2
	v_mul_f32_e32 v12, v12, v2
	v_mul_f32_e32 v11, v11, v2
	v_mul_f32_e32 v10, v10, v2
	v_mul_f32_e32 v9, v9, v2
	v_mul_f32_e32 v8, v8, v2
	v_mul_f32_e32 v7, v7, v2
	v_mul_f32_e32 v6, v6, v2
	v_mul_f32_e32 v5, v5, v2
	v_mul_f32_e32 v4, v4, v2
	v_cvt_pk_bf16_f32 v68, v243, v245
	v_cvt_pk_bf16_f32 v69, v70, v71
	v_cvt_pk_bf16_f32 v70, v72, v73
	v_cvt_pk_bf16_f32 v71, v74, v75
	v_cvt_pk_bf16_f32 v72, v76, v77
	v_cvt_pk_bf16_f32 v73, v78, v79
	v_cvt_pk_bf16_f32 v74, v80, v81
	v_cvt_pk_bf16_f32 v75, v82, v83
	v_mfma_f32_32x32x16_bf16 v[52:67], v[120:123], v[68:71], v[52:67]
	v_mov_b32_e32 v243, v244
	v_mov_b32_e32 v242, v246
	v_mfma_f32_32x32x16_bf16 v[36:51], v[112:115], v[68:71], v[36:51]
	v_mfma_f32_32x32x16_bf16 v[20:35], v[96:99], v[68:71], v[20:35]
	v_mfma_f32_32x32x16_bf16 v[4:19], v[84:87], v[68:71], v[4:19]
	v_mfma_f32_32x32x16_bf16 v[52:67], v[128:131], v[72:75], v[52:67]
	v_mfma_f32_32x32x16_bf16 v[36:51], v[124:127], v[72:75], v[36:51]
	v_mfma_f32_32x32x16_bf16 v[20:35], v[116:119], v[72:75], v[20:35]
	v_mfma_f32_32x32x16_bf16 v[4:19], v[104:107], v[72:75], v[4:19]

; #define LDS_WAIT() asm volatile("s_waitcnt lgkmcnt(0)" ::: "memory")
; DI int crow(int reg, int h) { return (reg & 3) + 8 * (reg >> 2) + 4 * h; }
; #define MFMA32(a, b, c) __builtin_amdgcn_mfma_f32_32x32x16_bf16((a), (b), (c), 0, 0, 0)
; DI void p3_attn_mfma(Frame& F, ArgsP A) {
;     ...
; #pragma unroll
;                 for (int i = 0; i < 16; ++i) acc[i] = tb[32 + (128 - 32 * t + rq - crow(i, h))];
;                 LDS_WAIT(); __builtin_amdgcn_sched_barrier(0);
; #pragma unroll
;                 for (int st = 0; st < 8; ++st) acc = MFMA32(kf[st], qf[st], acc);
;                 __builtin_amdgcn_sched_barrier(0);
;                 float tm = -3.0e38f;
; #pragma unroll
;                 for (int i = 0; i < 16; ++i) {
;                     const int key = crow(i, h);
;                     const bool valid = (t == 0) ? (key >= rq) : ((t == 4) ? (key <= rq) : true);
;                     acc[i] = valid ? acc[i] : -3.0e38f; tm = fmaxf(tm, acc[i]);
;                 }
;                 tm = fmaxf(tm, __shfl_xor(tm, 32));
;                 const float mn = fmaxf(m, tm), alpha = __expf(m - mn);
;                 float ps = 0.f;
; #pragma unroll
;                 for (int i = 0; i < 16; ++i) { const float p = (acc[i] > -1.0e38f) ? __expf(acc[i] - mn) : 0.f; acc[i] = p; ps += p; }
;                 ps += __shfl_xor(ps, 32);
.LBB0_476:
	v_lshl_add_u32 v2, v241, 2, v237
	ds_read2_b32 v[70:71], v2 offset0:31 offset1:32
	ds_read2_b32 v[72:73], v2 offset0:29 offset1:30
	ds_read2_b32 v[74:75], v2 offset0:23 offset1:24
	ds_read2_b32 v[76:77], v2 offset0:21 offset1:22
	ds_read2_b32 v[78:79], v2 offset0:15 offset1:16
	ds_read2_b32 v[80:81], v2 offset0:13 offset1:14
	ds_read2_b32 v[82:83], v2 offset0:7 offset1:8
	ds_read2_b32 v[212:213], v2 offset0:5 offset1:6
	s_waitcnt lgkmcnt(0)
	s_sub_i32 s10, 11, s15
	s_waitcnt lgkmcnt(7)
	v_mov_b32_e32 v68, v71
	v_mov_b32_e32 v69, v70
	s_waitcnt lgkmcnt(6)
	v_mov_b32_e32 v70, v73
	s_lshr_b32 s10, s17, s10
	v_mov_b32_e32 v71, v72
	s_waitcnt lgkmcnt(5)
	v_mov_b32_e32 v72, v75
	v_mov_b32_e32 v73, v74
	s_waitcnt lgkmcnt(4)
	v_mov_b32_e32 v74, v77
	v_mov_b32_e32 v75, v76
	s_waitcnt lgkmcnt(3)
	v_mov_b32_e32 v76, v79
	v_mov_b32_e32 v77, v78
	s_waitcnt lgkmcnt(2)
	v_mov_b32_e32 v78, v81
	v_mov_b32_e32 v79, v80
	s_waitcnt lgkmcnt(1)
	v_mov_b32_e32 v80, v83
	v_mov_b32_e32 v81, v82
	s_waitcnt lgkmcnt(0)
	v_mov_b32_e32 v82, v213
	v_mov_b32_e32 v83, v212
	s_waitcnt vmcnt(0)
	s_nop 0
	v_mfma_f32_32x32x16_bf16 v[68:83], v[208:211], v[172:175], v[68:83]
	v_mfma_f32_32x32x16_bf16 v[68:83], v[204:207], v[164:167], v[68:83]
	v_mfma_f32_32x32x16_bf16 v[68:83], v[200:203], v[156:159], v[68:83]
	v_mfma_f32_32x32x16_bf16 v[68:83], v[196:199], v[148:151], v[68:83]
	v_mfma_f32_32x32x16_bf16 v[68:83], v[192:195], v[176:179], v[68:83]
	v_mfma_f32_32x32x16_bf16 v[68:83], v[188:191], v[168:171], v[68:83]
	v_mfma_f32_32x32x16_bf16 v[68:83], v[184:187], v[160:163], v[68:83]
	v_mfma_f32_32x32x16_bf16 v[68:83], v[180:183], v[152:155], v[68:83]
	v_cmp_le_i32_e32 vcc, v220, v241
	v_and_b32_e32 v149, 64, v239
	v_xor_b32_e32 v148, 32, v239
	s_nop 8
	v_cndmask_b32_e32 v2, v238, v68, vcc
	v_cmp_lt_i32_e32 vcc, v220, v241
	v_add_u32_e32 v149, 64, v149
	s_nop 0
	v_cndmask_b32_e32 v68, v238, v69, vcc
	v_cmp_le_i32_e32 vcc, v223, v241
	v_max3_f32 v69, v2, s53, v68
	s_nop 0
	v_cndmask_b32_e32 v70, v238, v70, vcc
	v_cmp_le_i32_e32 vcc, v224, v241
	s_nop 1
	v_cndmask_b32_e32 v71, v238, v71, vcc
	v_cmp_le_i32_e32 vcc, v225, v241
	v_max3_f32 v69, v69, v70, v71
	s_nop 0
	v_cndmask_b32_e32 v72, v238, v72, vcc
	v_cmp_le_i32_e32 vcc, v226, v241
	s_nop 1
	v_cndmask_b32_e32 v73, v238, v73, vcc
	v_cmp_le_i32_e32 vcc, v227, v241
	v_max3_f32 v69, v69, v72, v73
	s_nop 0
	v_cndmask_b32_e32 v74, v238, v74, vcc
	v_cmp_le_i32_e32 vcc, v228, v241
	s_nop 1
	v_cndmask_b32_e32 v75, v238, v75, vcc
	v_cmp_le_i32_e32 vcc, v229, v241
	v_max3_f32 v69, v69, v74, v75
	s_nop 0
	v_cndmask_b32_e32 v76, v238, v76, vcc
	v_cmp_le_i32_e32 vcc, v230, v241
	s_nop 1
	v_cndmask_b32_e32 v77, v238, v77, vcc
	v_cmp_le_i32_e32 vcc, v231, v241
	v_max3_f32 v69, v69, v76, v77
	s_nop 0
	v_cndmask_b32_e32 v78, v238, v78, vcc
	v_cmp_le_i32_e32 vcc, v232, v241
	s_nop 1
	v_cndmask_b32_e32 v79, v238, v79, vcc
	v_cmp_le_i32_e32 vcc, v233, v241
	v_max3_f32 v69, v69, v78, v79
	s_nop 0
	v_cndmask_b32_e32 v80, v238, v80, vcc
	v_cmp_le_i32_e32 vcc, v234, v241
	s_nop 1
	v_cndmask_b32_e32 v81, v238, v81, vcc
	v_cmp_le_i32_e32 vcc, v235, v241
	v_max3_f32 v69, v69, v80, v81
	s_nop 0
	v_cndmask_b32_e32 v82, v238, v82, vcc
	v_cmp_le_i32_e32 vcc, v236, v241
	s_nop 1
	v_cndmask_b32_e32 v83, v238, v83, vcc
	v_cmp_lt_i32_e32 vcc, v148, v149
	v_max3_f32 v69, v69, v82, v83
	s_nop 0
	v_cndmask_b32_e32 v148, v239, v148, vcc
	v_lshlrev_b32_e32 v148, 2, v148
	ds_bpermute_b32 v149, v148, v69
	v_cmp_lt_f32_e32 vcc, s54, v2
	s_waitcnt lgkmcnt(0)
	v_max3_f32 v69, v243, v69, v149
	v_sub_f32_e32 v150, v2, v69
	v_mul_f32_e32 v150, 0x3fb8aa3b, v150
	v_sub_f32_e32 v151, v68, v69
	v_exp_f32_e32 v150, v150
	v_mul_f32_e32 v151, 0x3fb8aa3b, v151
	v_exp_f32_e32 v151, v151
	v_sub_f32_e32 v152, v71, v69
	v_cndmask_b32_e32 v150, 0, v150, vcc
	v_cmp_lt_f32_e32 vcc, s54, v68
	v_mul_f32_e32 v152, 0x3fb8aa3b, v152
	v_exp_f32_e32 v152, v152
	v_cndmask_b32_e32 v68, 0, v151, vcc
	v_sub_f32_e32 v151, v70, v69
	v_mul_f32_e32 v151, 0x3fb8aa3b, v151
	v_exp_f32_e32 v151, v151
	v_cmp_lt_f32_e32 vcc, s54, v70
	v_sub_f32_e32 v70, v72, v69
	v_mul_f32_e32 v70, 0x3fb8aa3b, v70
	v_exp_f32_e32 v70, v70
	v_cndmask_b32_e32 v151, 0, v151, vcc
	v_cmp_lt_f32_e32 vcc, s54, v71
	v_add_f32_e32 v2, 0, v150
	v_add_f32_e32 v2, v68, v2
	v_cndmask_b32_e32 v71, 0, v152, vcc
	v_sub_f32_e32 v152, v73, v69
	v_cmp_lt_f32_e32 vcc, s54, v72
	v_mul_f32_e32 v152, 0x3fb8aa3b, v152
	v_exp_f32_e32 v152, v152
	v_cndmask_b32_e32 v153, 0, v70, vcc
	v_sub_f32_e32 v70, v74, v69
	v_mul_f32_e32 v70, 0x3fb8aa3b, v70
	v_sub_f32_e32 v72, v75, v69
	v_exp_f32_e32 v70, v70
	v_mul_f32_e32 v72, 0x3fb8aa3b, v72
	v_exp_f32_e32 v72, v72
	v_cmp_lt_f32_e32 vcc, s54, v73
	v_add_f32_e32 v2, v151, v2
	v_add_f32_e32 v2, v71, v2
	v_cndmask_b32_e32 v152, 0, v152, vcc
	v_cmp_lt_f32_e32 vcc, s54, v74
	v_add_f32_e32 v2, v153, v2
	v_add_f32_e32 v2, v152, v2
	v_cndmask_b32_e32 v154, 0, v70, vcc
	v_cmp_lt_f32_e32 vcc, s54, v75
	v_sub_f32_e32 v70, v76, v69
	v_mul_f32_e32 v70, 0x3fb8aa3b, v70
	v_cndmask_b32_e32 v75, 0, v72, vcc
	v_sub_f32_e32 v72, v77, v69
	v_exp_f32_e32 v70, v70
	v_mul_f32_e32 v72, 0x3fb8aa3b, v72
	v_exp_f32_e32 v72, v72
	v_cmp_lt_f32_e32 vcc, s54, v76
	v_add_f32_e32 v2, v154, v2
	v_add_f32_e32 v2, v75, v2
	v_cndmask_b32_e32 v76, 0, v70, vcc
	v_cmp_lt_f32_e32 vcc, s54, v77
	v_sub_f32_e32 v70, v78, v69
	v_mul_f32_e32 v70, 0x3fb8aa3b, v70
	v_cndmask_b32_e32 v77, 0, v72, vcc
	v_sub_f32_e32 v72, v79, v69
	v_exp_f32_e32 v70, v70
	v_mul_f32_e32 v72, 0x3fb8aa3b, v72
	v_exp_f32_e32 v72, v72
	v_cmp_lt_f32_e32 vcc, s54, v78
	v_add_f32_e32 v2, v76, v2
	v_add_f32_e32 v2, v77, v2
	v_cndmask_b32_e32 v78, 0, v70, vcc
	v_cmp_lt_f32_e32 vcc, s54, v79
	v_sub_f32_e32 v70, v80, v69
	v_mul_f32_e32 v70, 0x3fb8aa3b, v70
	v_cndmask_b32_e32 v79, 0, v72, vcc
	v_sub_f32_e32 v72, v81, v69
	v_exp_f32_e32 v70, v70
	v_mul_f32_e32 v72, 0x3fb8aa3b, v72
	v_exp_f32_e32 v72, v72
	v_cmp_lt_f32_e32 vcc, s54, v80
	v_add_f32_e32 v2, v78, v2
	v_add_f32_e32 v2, v79, v2
	v_cndmask_b32_e32 v80, 0, v70, vcc
	v_cmp_lt_f32_e32 vcc, s54, v81
	v_sub_f32_e32 v70, v82, v69
	v_mul_f32_e32 v70, 0x3fb8aa3b, v70
	v_cndmask_b32_e32 v81, 0, v72, vcc
	v_sub_f32_e32 v72, v83, v69
	v_exp_f32_e32 v70, v70
	v_mul_f32_e32 v72, 0x3fb8aa3b, v72
	v_exp_f32_e32 v72, v72
	v_add_f32_e32 v2, v80, v2
	v_cmp_lt_f32_e32 vcc, s54, v82
	v_add_f32_e32 v2, v81, v2
	v_sub_f32_e32 v149, v243, v69
	v_cndmask_b32_e32 v82, 0, v70, vcc
	v_cmp_lt_f32_e32 vcc, s54, v83
	v_add_f32_e32 v2, v82, v2
	s_nop 0
	v_cndmask_b32_e32 v83, 0, v72, vcc
	v_add_f32_e32 v70, v83, v2
	ds_bpermute_b32 v72, v148, v70
	v_mul_f32_e32 v2, 0x3fb8aa3b, v149
	v_exp_f32_e32 v2, v2
	s_waitcnt lgkmcnt(0)
; #define GAS __attribute__((address_space(1)))
; DI unsigned cvtpk_s(float lo, float hi) { f32x2_t v = {lo, hi}; bf16x2_t b = __builtin_convertvector(v, bf16x2_t); return __builtin_bit_cast(unsigned, b); }
; #define MFMA32(a, b, c) __builtin_amdgcn_mfma_f32_32x32x16_bf16((a), (b), (c), 0, 0, 0)
; DI void p3_attn_mfma(Frame& F, ArgsP A) {
;     ...
;                 lsum = lsum * alpha + ps; m = mn;
;                 __builtin_amdgcn_sched_barrier(0);
;                 if (t < 4) { P3_LOADK(t + 1); P3_LOADV((t + 1) & 1, t + 1); }
; #pragma unroll
;                 for (int db = 0; db < 4; ++db) {
; #pragma unroll
;                     for (int i = 0; i < 16; ++i) O[db][i] *= alpha; }
;                 const bf16x8 pb0 = pack_step(acc, 0), pb1 = pack_step(acc, 1);
;                 __builtin_amdgcn_sched_barrier(0);
; #pragma unroll
;                 for (int db = 0; db < 4; ++db) O[db] = MFMA32(__builtin_bit_cast(bf16x8, vf[t & 1][db][0]), pb0, O[db]);
; #pragma unroll
;                 for (int db = 0; db < 4; ++db) O[db] = MFMA32(__builtin_bit_cast(bf16x8, vf[t & 1][db][1]), pb1, O[db]);
;             }
;             __builtin_amdgcn_sched_barrier(0);
;         }
;     ...
;         const float inv = 1.0f / lsum;
;         const size_t obase = (size_t)g * T + (size_t)b * SEQ;
;         GAS bf16_t* og_u = (GAS bf16_t*)OG + obase * 512 + (head & 3) * 128; asm volatile("" : "+s"(og_u));
;         int r32s = r32, hs = h; asm volatile("" : "+v"(r32s), "+v"(hs));
;         const unsigned rowo = (unsigned)((((l0 + r32s) << sh) + r) * 512 + 8 * hs);
; #pragma unroll
;         for (int db = 0; db < 4; ++db) {
; #pragma unroll
;             for (int gq = 0; gq < 4; gq += 2) {
;                 unsigned ax = cvtpk_s(O[db][4 * gq] * inv, O[db][4 * gq + 1] * inv), ay = cvtpk_s(O[db][4 * gq + 2] * inv, O[db][4 * gq + 3] * inv);
;                 unsigned bx = cvtpk_s(O[db][4 * gq + 4] * inv, O[db][4 * gq + 5] * inv), by = cvtpk_s(O[db][4 * gq + 6] * inv, O[db][4 * gq + 7] * inv);
;                 const auto rx = __builtin_amdgcn_permlane32_swap(ax, bx, false, false); const auto ry = __builtin_amdgcn_permlane32_swap(ay, by, false, false);
;                 u32x4 w; w.x = rx[0]; w.y = ry[0]; w.z = rx[1]; w.w = ry[1];
;                 *(GAS u32x4*)(og_u + rowo + db * 32 + 8 * gq) = w;
	v_add_f32_e32 v70, v70, v72
	v_fmac_f32_e32 v70, v242, v2
	v_mul_f32_e32 v67, v67, v2
	v_mul_f32_e32 v66, v66, v2
	v_mul_f32_e32 v65, v65, v2
	v_mul_f32_e32 v64, v64, v2
	v_mul_f32_e32 v63, v63, v2
	v_mul_f32_e32 v62, v62, v2
	v_mul_f32_e32 v61, v61, v2
	v_mul_f32_e32 v60, v60, v2
	v_mul_f32_e32 v59, v59, v2
	v_mul_f32_e32 v58, v58, v2
	v_mul_f32_e32 v57, v57, v2
	v_mul_f32_e32 v56, v56, v2
	v_mul_f32_e32 v55, v55, v2
	v_mul_f32_e32 v54, v54, v2
	v_mul_f32_e32 v53, v53, v2
	v_mul_f32_e32 v52, v52, v2
	v_mul_f32_e32 v51, v51, v2
	v_mul_f32_e32 v50, v50, v2
	v_mul_f32_e32 v49, v49, v2
	v_mul_f32_e32 v48, v48, v2
	v_mul_f32_e32 v47, v47, v2
	v_mul_f32_e32 v46, v46, v2
	v_mul_f32_e32 v45, v45, v2
	v_mul_f32_e32 v44, v44, v2
	v_mul_f32_e32 v43, v43, v2
	v_mul_f32_e32 v42, v42, v2
	v_mul_f32_e32 v41, v41, v2
	v_mul_f32_e32 v40, v40, v2
	v_mul_f32_e32 v39, v39, v2
	v_mul_f32_e32 v38, v38, v2
	v_mul_f32_e32 v37, v37, v2
	v_mul_f32_e32 v36, v36, v2
	v_mul_f32_e32 v35, v35, v2
	v_mul_f32_e32 v34, v34, v2
	v_mul_f32_e32 v33, v33, v2
	v_mul_f32_e32 v32, v32, v2
	v_mul_f32_e32 v31, v31, v2
	v_mul_f32_e32 v30, v30, v2
	v_mul_f32_e32 v29, v29, v2
	v_mul_f32_e32 v28, v28, v2
	v_mul_f32_e32 v27, v27, v2
	v_mul_f32_e32 v26, v26, v2
	v_mul_f32_e32 v25, v25, v2
	v_mul_f32_e32 v24, v24, v2
	v_mul_f32_e32 v23, v23, v2
	v_mul_f32_e32 v22, v22, v2
	v_mul_f32_e32 v21, v21, v2
	v_mul_f32_e32 v20, v20, v2
	v_mul_f32_e32 v19, v19, v2
	v_mul_f32_e32 v18, v18, v2
	v_mul_f32_e32 v17, v17, v2
	v_mul_f32_e32 v16, v16, v2
	v_mul_f32_e32 v15, v15, v2
	v_mul_f32_e32 v14, v14, v2
	v_mul_f32_e32 v13, v13, v2
	v_mul_f32_e32 v12, v12, v2
	v_mul_f32_e32 v11, v11, v2
	v_mul_f32_e32 v10, v10, v2
	v_mul_f32_e32 v9, v9, v2
	v_mul_f32_e32 v8, v8, v2
	v_mul_f32_e32 v7, v7, v2
	v_mul_f32_e32 v6, v6, v2
	v_mul_f32_e32 v5, v5, v2
	v_mul_f32_e32 v4, v4, v2
	v_cvt_pk_bf16_f32 v72, v150, v68
	v_cvt_pk_bf16_f32 v73, v151, v71
	v_cvt_pk_bf16_f32 v74, v153, v152
	v_cvt_pk_bf16_f32 v75, v154, v75
	v_cvt_pk_bf16_f32 v76, v76, v77
	v_cvt_pk_bf16_f32 v77, v78, v79
	v_cvt_pk_bf16_f32 v78, v80, v81
	v_cvt_pk_bf16_f32 v79, v82, v83
	v_mfma_f32_32x32x16_bf16 v[52:67], v[108:111], v[72:75], v[52:67]
	v_mfma_f32_32x32x16_bf16 v[36:51], v[100:103], v[72:75], v[36:51]
	v_mfma_f32_32x32x16_bf16 v[20:35], v[92:95], v[72:75], v[20:35]
	v_mfma_f32_32x32x16_bf16 v[4:19], v[88:91], v[72:75], v[4:19]
	v_mfma_f32_32x32x16_bf16 v[52:67], v[144:147], v[76:79], v[52:67]
	v_mfma_f32_32x32x16_bf16 v[36:51], v[140:143], v[76:79], v[36:51]
	v_mfma_f32_32x32x16_bf16 v[20:35], v[136:139], v[76:79], v[20:35]
	v_mfma_f32_32x32x16_bf16 v[4:19], v[132:135], v[76:79], v[4:19]
	v_div_scale_f32 v2, s[20:21], v70, v70, 1.0
	v_rcp_f32_e32 v68, v2
	s_ashr_i32 s19, s18, 31
	s_ashr_i32 s17, s16, 31
	s_lshl_b64 s[18:19], s[18:19], 14
	s_lshl_b64 s[16:17], s[16:17], 11
	v_fma_f32 v72, -v2, v68, 1.0
	s_add_u32 s16, s18, s16
	v_div_scale_f32 v71, vcc, 1.0, v70, 1.0
	v_fmac_f32_e32 v68, v72, v68
	s_addc_u32 s17, s19, s17
	v_mul_f32_e32 v72, v71, v68
	s_lshl_b64 s[18:19], s[16:17], 10
	v_fma_f32 v73, -v2, v72, v71
	s_add_u32 s20, s36, s18
	v_fmac_f32_e32 v72, v73, v68
	s_addc_u32 s19, s37, s19
	s_and_b32 s18, s14, 3
	v_fma_f32 v2, -v2, v72, v71
	s_lshl_b32 s14, s18, 8
	v_div_fmas_f32 v2, v2, v68, v72
	s_add_u32 s20, s20, s14
	v_div_fixup_f32 v72, v2, v70, 1.0
	s_addc_u32 s21, s19, 0
	v_mov_b32_e32 v2, v216
	v_mov_b32_e32 v71, v217
	v_mul_f32_e32 v53, v53, v72
	v_mul_f32_e32 v52, v52, v72
	v_add_u32_e32 v2, s71, v2
	v_lshlrev_b32_e32 v2, s15, v2
	v_mul_f32_e32 v55, v55, v72
	v_mul_f32_e32 v54, v54, v72
	v_mul_f32_e32 v37, v37, v72
	v_mul_f32_e32 v36, v36, v72
	v_mul_f32_e32 v39, v39, v72
	v_mul_f32_e32 v38, v38, v72
	v_mul_f32_e32 v21, v21, v72
	v_mul_f32_e32 v20, v20, v72
	v_mul_f32_e32 v23, v23, v72
	v_mul_f32_e32 v22, v22, v72
	v_mul_f32_e32 v5, v5, v72
	v_mul_f32_e32 v4, v4, v72
	v_mul_f32_e32 v7, v7, v72
	v_mul_f32_e32 v6, v6, v72
	v_add_u32_e32 v68, s10, v2
	v_lshlrev_b32_e32 v2, 3, v71
	v_cvt_pk_bf16_f32 v52, v52, v53
	v_cvt_pk_bf16_f32 v53, v54, v55
	v_mul_f32_e32 v55, v57, v72
	v_mul_f32_e32 v54, v56, v72
	v_mul_f32_e32 v57, v59, v72
; #define GAS __attribute__((address_space(1)))
; DI unsigned cvtpk_s(float lo, float hi) { f32x2_t v = {lo, hi}; bf16x2_t b = __builtin_convertvector(v, bf16x2_t); return __builtin_bit_cast(unsigned, b); }
; DI void p3_attn_mfma(Frame& F, ArgsP A) {
;     ...
;         const float inv = 1.0f / lsum;
;         const size_t obase = (size_t)g * T + (size_t)b * SEQ;
;         GAS bf16_t* og_u = (GAS bf16_t*)OG + obase * 512 + (head & 3) * 128; asm volatile("" : "+s"(og_u));
;         int r32s = r32, hs = h; asm volatile("" : "+v"(r32s), "+v"(hs));
;         const unsigned rowo = (unsigned)((((l0 + r32s) << sh) + r) * 512 + 8 * hs);
; #pragma unroll
;         for (int db = 0; db < 4; ++db) {
; #pragma unroll
;             for (int gq = 0; gq < 4; gq += 2) {
;                 unsigned ax = cvtpk_s(O[db][4 * gq] * inv, O[db][4 * gq + 1] * inv), ay = cvtpk_s(O[db][4 * gq + 2] * inv, O[db][4 * gq + 3] * inv);
;                 unsigned bx = cvtpk_s(O[db][4 * gq + 4] * inv, O[db][4 * gq + 5] * inv), by = cvtpk_s(O[db][4 * gq + 6] * inv, O[db][4 * gq + 7] * inv);
;                 const auto rx = __builtin_amdgcn_permlane32_swap(ax, bx, false, false); const auto ry = __builtin_amdgcn_permlane32_swap(ay, by, false, false);
;                 u32x4 w; w.x = rx[0]; w.y = ry[0]; w.z = rx[1]; w.w = ry[1];
;                 *(GAS u32x4*)(og_u + rowo + db * 32 + 8 * gq) = w;
;             }
;         }
;         if (hs == 0) { const int tok = ((l0 + r32s) << sh) + r; LSE[(obase + tok) * 4 + (head & 3)] = m + __logf(lsum); }
	v_mul_f32_e32 v56, v58, v72
	v_cvt_pk_bf16_f32 v36, v36, v37
	v_cvt_pk_bf16_f32 v37, v38, v39
	v_mul_f32_e32 v39, v41, v72
	v_mul_f32_e32 v38, v40, v72
	v_mul_f32_e32 v41, v43, v72
	v_mul_f32_e32 v40, v42, v72
	v_cvt_pk_bf16_f32 v20, v20, v21
	v_cvt_pk_bf16_f32 v21, v22, v23
	v_mul_f32_e32 v23, v25, v72
	v_mul_f32_e32 v22, v24, v72
	v_mul_f32_e32 v25, v27, v72
	v_mul_f32_e32 v24, v26, v72
	v_cvt_pk_bf16_f32 v4, v4, v5
	v_cvt_pk_bf16_f32 v5, v6, v7
	v_mul_f32_e32 v7, v9, v72
	v_mul_f32_e32 v6, v8, v72
	v_mul_f32_e32 v9, v11, v72
	v_mul_f32_e32 v8, v10, v72
	v_lshl_add_u32 v2, v68, 9, v2
	v_cvt_pk_bf16_f32 v54, v54, v55
	v_cvt_pk_bf16_f32 v55, v56, v57
	v_cvt_pk_bf16_f32 v38, v38, v39
	v_cvt_pk_bf16_f32 v39, v40, v41
	v_cvt_pk_bf16_f32 v22, v22, v23
	v_cvt_pk_bf16_f32 v23, v24, v25
	v_cvt_pk_bf16_f32 v6, v6, v7
	v_cvt_pk_bf16_f32 v7, v8, v9
	v_lshl_add_u64 v[74:75], v[2:3], 1, s[20:21]
	v_permlane32_swap_b32_e32 v52, v54
	v_permlane32_swap_b32_e32 v53, v55
	v_permlane32_swap_b32_e32 v36, v38
	v_permlane32_swap_b32_e32 v37, v39
	v_permlane32_swap_b32_e32 v20, v22
	v_permlane32_swap_b32_e32 v21, v23
	v_permlane32_swap_b32_e32 v4, v6
	v_permlane32_swap_b32_e32 v5, v7
	global_store_dwordx4 v[74:75], v[52:55], off
	global_store_dwordx4 v[74:75], v[36:39], off offset:64
	global_store_dwordx4 v[74:75], v[20:23], off offset:128
	v_mul_f32_e32 v53, v61, v72
	v_mul_f32_e32 v52, v60, v72
	v_mul_f32_e32 v55, v63, v72
	v_mul_f32_e32 v54, v62, v72
	v_mul_f32_e32 v37, v45, v72
	v_mul_f32_e32 v36, v44, v72
	v_mul_f32_e32 v39, v47, v72
	v_mul_f32_e32 v38, v46, v72
	v_mul_f32_e32 v21, v29, v72
	v_mul_f32_e32 v20, v28, v72
	v_mul_f32_e32 v23, v31, v72
	v_mul_f32_e32 v22, v30, v72
	global_store_dwordx4 v[74:75], v[4:7], off offset:192
	v_cvt_pk_bf16_f32 v52, v52, v53
	v_cvt_pk_bf16_f32 v53, v54, v55
	v_mul_f32_e32 v5, v13, v72
	v_mul_f32_e32 v4, v12, v72
	v_mul_f32_e32 v7, v15, v72
	v_mul_f32_e32 v6, v14, v72
	v_mul_f32_e32 v55, v65, v72
	v_mul_f32_e32 v54, v64, v72
	v_mul_f32_e32 v57, v67, v72
	v_mul_f32_e32 v56, v66, v72
	v_cvt_pk_bf16_f32 v36, v36, v37
	v_cvt_pk_bf16_f32 v37, v38, v39
	v_mul_f32_e32 v39, v49, v72
	v_mul_f32_e32 v38, v48, v72
	v_mul_f32_e32 v41, v51, v72
	v_mul_f32_e32 v40, v50, v72
	v_cvt_pk_bf16_f32 v20, v20, v21
	v_cvt_pk_bf16_f32 v21, v22, v23
	v_mul_f32_e32 v23, v33, v72
	v_mul_f32_e32 v22, v32, v72
	v_mul_f32_e32 v25, v35, v72
	v_mul_f32_e32 v24, v34, v72
	v_cvt_pk_bf16_f32 v4, v4, v5
	v_cvt_pk_bf16_f32 v5, v6, v7
	v_mul_f32_e32 v7, v17, v72
	v_mul_f32_e32 v6, v16, v72
	v_mul_f32_e32 v9, v19, v72
	v_mul_f32_e32 v8, v18, v72
	v_cvt_pk_bf16_f32 v54, v54, v55
	v_cvt_pk_bf16_f32 v55, v56, v57
	v_cvt_pk_bf16_f32 v38, v38, v39
	v_cvt_pk_bf16_f32 v39, v40, v41
	v_cvt_pk_bf16_f32 v22, v22, v23
	v_cvt_pk_bf16_f32 v23, v24, v25
	v_cvt_pk_bf16_f32 v6, v6, v7
	v_cvt_pk_bf16_f32 v7, v8, v9
	v_permlane32_swap_b32_e32 v52, v54
	v_permlane32_swap_b32_e32 v53, v55
	v_permlane32_swap_b32_e32 v36, v38
	v_permlane32_swap_b32_e32 v37, v39
	v_permlane32_swap_b32_e32 v20, v22
	v_permlane32_swap_b32_e32 v21, v23
	v_permlane32_swap_b32_e32 v4, v6
	v_permlane32_swap_b32_e32 v5, v7
	v_cmp_eq_u32_e32 vcc, 0, v71
	global_store_dwordx4 v[74:75], v[52:55], off offset:32
	global_store_dwordx4 v[74:75], v[36:39], off offset:96
	global_store_dwordx4 v[74:75], v[20:23], off offset:160
	global_store_dwordx4 v[74:75], v[4:7], off offset:224
	s_and_saveexec_b64 s[14:15], vcc
	s_cbranch_execz .LBB0_450
	v_cmp_gt_f32_e32 vcc, s68, v70
	s_lshl_b32 s10, s18, 2
	s_nop 0
	v_cndmask_b32_e64 v2, 0, 32, vcc
	v_ldexp_f32 v2, v70, v2
	v_log_f32_e32 v2, v2
	v_cndmask_b32_e32 v4, 0, v240, vcc
	v_mul_f32_e32 v5, 0x3f317217, v2
	v_fma_f32 v5, v2, s69, -v5
	v_fmac_f32_e32 v5, 0x3377d1cf, v2
	v_fmac_f32_e32 v5, 0x3f317217, v2
	v_cmp_lt_f32_e64 vcc, |v2|, s70
	s_nop 1
	v_cndmask_b32_e32 v2, v2, v5, vcc
	v_sub_f32_e32 v2, v2, v4
	v_add_f32_e32 v2, v69, v2
	v_ashrrev_i32_e32 v69, 31, v68
	v_lshl_add_u64 v[4:5], s[16:17], 0, v[68:69]
	v_lshl_add_u64 v[4:5], v[4:5], 4, s[12:13]
	v_lshl_add_u64 v[4:5], v[4:5], 0, s[10:11]
	global_store_dword v[4:5], v2, off
	s_branch .LBB0_450
